# stacked: GEMM2 epilogue lane exchange via permlane16_swap, combine second-token gathers issued early, DPP lane exchanges in dwconv and combine
# speedup vs baseline: 1.0071x; 1.0021x over previous
.LBB0_432:
	s_or_b64 exec, exec, s[12:13]
	v_mov_b32_e32 v88, s14
	v_mov_b32_e32 v90, s68
	v_mov_b32_e32 v92, s69
	s_waitcnt lgkmcnt(0)
	s_barrier
	ds_read2_b32 v[88:89], v88 offset1:1
	ds_read2_b32 v[90:91], v90 offset1:1
	ds_read2_b32 v[92:93], v92 offset1:1
	v_readlane_b32 s12, v254, 53
	s_mov_b32 s66, 0x3a800000
	s_waitcnt lgkmcnt(2)
	v_pk_add_f32 v[88:89], v[88:89], 0 op_sel_hi:[1,0]
	v_mov_b32_e32 v96, s12
	v_readlane_b32 s12, v254, 54
	ds_read2_b32 v[96:97], v96 offset1:1
	s_waitcnt lgkmcnt(2)
	v_pk_add_f32 v[88:89], v[88:89], v[90:91]
	v_mov_b32_e32 v90, s12
	v_readlane_b32 s12, v254, 45
	s_waitcnt lgkmcnt(1)
	v_pk_add_f32 v[88:89], v[88:89], v[92:93]
	s_mov_b32 s13, 0x800000
	v_mov_b32_e32 v92, s12
	v_readlane_b32 s12, v254, 43
	s_waitcnt lgkmcnt(0)
	v_pk_add_f32 v[88:89], v[88:89], v[96:97]
	s_xor_b64 s[10:11], s[10:11], -1
	v_mov_b32_e32 v102, s12
	v_readlane_b32 s12, v254, 49
	s_nop 1
	v_mov_b32_e32 v108, s12
	ds_read2_b32 v[90:91], v90 offset1:1
	ds_read2_b32 v[92:93], v92 offset1:1
	ds_read2_b32 v[102:103], v102 offset1:1
	ds_read2_b32 v[108:109], v108 offset1:1
	s_mov_b32 s12, 0x3727c5ac
	s_waitcnt lgkmcnt(3)
	v_pk_add_f32 v[88:89], v[88:89], v[90:91]
	s_waitcnt lgkmcnt(2)
	v_pk_add_f32 v[88:89], v[88:89], v[92:93]
	s_waitcnt lgkmcnt(1)
	v_pk_add_f32 v[88:89], v[88:89], v[102:103]
	s_waitcnt lgkmcnt(0)
	v_pk_add_f32 v[88:89], v[88:89], v[108:109]
	s_nop 0
	v_pk_mul_f32 v[90:91], v[88:89], s[66:67] op_sel_hi:[1,0]
	s_nop 0
	v_fma_f32 v88, -v90, v90, v91
	v_max_f32_e32 v88, 0, v88
	v_add_f32_e32 v88, s12, v88
	v_mul_f32_e32 v89, 0x4b800000, v88
	v_cmp_gt_f32_e32 vcc, s13, v88
	v_readlane_b32 s12, v254, 50
	v_sub_f32_e32 v0, v0, v90
	v_cndmask_b32_e32 v88, v88, v89, vcc
	v_rsq_f32_e32 v88, v88
	v_sub_f32_e32 v1, v1, v90
	v_mul_f32_e32 v89, 0x45800000, v88
	v_cndmask_b32_e32 v91, v88, v89, vcc
	v_mov_b32_e32 v88, s12
	v_readlane_b32 s12, v254, 52
	v_mul_f32_e32 v0, v0, v91
	v_fma_f32 v0, v70, v0, v68
	v_mov_b32_e32 v92, s12
	v_readlane_b32 s12, v254, 47
	v_mul_f32_e32 v1, v1, v91
	v_fma_f32 v1, v71, v1, v69
	v_mov_b32_e32 v96, s12
	ds_read2_b32 v[88:89], v88 offset1:1
	ds_read2_b32 v[92:93], v92 offset1:1
	ds_read2_b32 v[96:97], v96 offset1:1
	v_readlane_b32 s12, v254, 61
	v_mul_f32_e32 v91, 0xbfb8aa3b, v1
	s_waitcnt lgkmcnt(2)
	v_pk_add_f32 v[88:89], v[88:89], 0 op_sel_hi:[1,0]
	v_mov_b32_e32 v102, s12
	v_readlane_b32 s12, v254, 62
	ds_read2_b32 v[102:103], v102 offset1:1
	s_waitcnt lgkmcnt(2)
	v_pk_add_f32 v[88:89], v[88:89], v[92:93]
	v_mov_b32_e32 v92, s12
	v_readlane_b32 s12, v254, 63
	s_waitcnt lgkmcnt(1)
	v_pk_add_f32 v[88:89], v[88:89], v[96:97]
	v_exp_f32_e32 v91, v91
	v_mov_b32_e32 v96, s12
	v_readlane_b32 s12, v255, 0
	s_waitcnt lgkmcnt(0)
	v_pk_add_f32 v[88:89], v[88:89], v[102:103]
	v_mov_b32_e32 v108, s12
	v_readlane_b32 s12, v255, 1
	s_nop 1
	v_mov_b32_e32 v110, s12
	ds_read2_b32 v[92:93], v92 offset1:1
	ds_read2_b32 v[96:97], v96 offset1:1
	ds_read2_b32 v[108:109], v108 offset1:1
	ds_read2_b32 v[110:111], v110 offset1:1
	s_mov_b32 s12, 0x3727c5ac
	s_waitcnt lgkmcnt(3)
	v_pk_add_f32 v[88:89], v[88:89], v[92:93]
	s_waitcnt lgkmcnt(2)
	v_pk_add_f32 v[88:89], v[88:89], v[96:97]
	s_waitcnt lgkmcnt(1)
	v_pk_add_f32 v[88:89], v[88:89], v[108:109]
	s_waitcnt lgkmcnt(0)
	v_pk_add_f32 v[88:89], v[88:89], v[110:111]
	s_nop 0
	v_pk_mul_f32 v[92:93], v[88:89], s[66:67] op_sel_hi:[1,0]
	s_nop 0
	v_fma_f32 v88, -v92, v92, v93
	v_mul_f32_e32 v93, 0xbfb8aa3b, v0
	v_max_f32_e32 v88, 0, v88
	v_exp_f32_e32 v93, v93
	v_add_f32_e32 v88, s12, v88
	v_mul_f32_e32 v89, 0x4b800000, v88
	v_cmp_gt_f32_e32 vcc, s13, v88
	v_add_f32_e32 v90, 1.0, v93
	v_rcp_f32_e32 v90, v90
	v_cndmask_b32_e32 v88, v88, v89, vcc
	v_rsq_f32_e32 v88, v88
	v_readlane_b32 s12, v255, 2
	v_mul_f32_e32 v0, v0, v90
	v_add_f32_e32 v90, 1.0, v91
	v_mul_f32_e32 v89, 0x45800000, v88
	v_cndmask_b32_e32 v89, v88, v89, vcc
	v_sub_f32_e32 v91, v104, v92
	v_sub_f32_e32 v92, v105, v92
	v_mul_f32_e32 v91, v91, v89
	v_mul_f32_e32 v89, v92, v89
	v_fma_f32 v91, v70, v91, v68
	v_fma_f32 v89, v71, v89, v69
	v_mul_f32_e32 v92, 0xbfb8aa3b, v91
	v_mul_f32_e32 v93, 0xbfb8aa3b, v89
	v_rcp_f32_e32 v90, v90
	v_exp_f32_e32 v92, v92
	v_exp_f32_e32 v93, v93
	v_lshl_or_b32 v88, s18, 4, v167
	v_mul_f32_e32 v1, v1, v90
	v_add_f32_e32 v90, 1.0, v92
	v_add_f32_e32 v92, 1.0, v93
	v_rcp_f32_e32 v90, v90
	v_rcp_f32_e32 v92, v92
	v_mov_b32_e32 v93, v201
	v_cvt_pk_fp8_f32 v93, v0, v1
	v_mul_f32_e32 v0, v91, v90
	v_mul_f32_e32 v1, v89, v92
	v_mov_b32_e32 v89, v201
	v_cvt_pk_fp8_f32 v89, v0, v1
	v_cvt_pk_fp8_f32 v93, 0, 0 op_sel:[0,0,1]
	s_mov_b32 s18, 1
	v_cvt_pk_fp8_f32 v89, 0, 0 op_sel:[0,0,1]
	v_and_b32_e32 v0, 0xffff, v93
	v_and_b32_e32 v1, 0xffff, v89
	v_cndmask_b32_e64 v1, v0, v1, s[8:9]
	s_nop 1
	v_mov_b32_dpp v1, v1 quad_perm:[1,0,3,2] row_mask:0xf bank_mask:0xf
	s_waitcnt lgkmcnt(0)
	v_lshl_or_b32 v89, v89, 16, v1
	v_lshl_or_b32 v0, v1, 16, v0
	v_cndmask_b32_e64 v90, v89, v0, s[8:9]
	v_ashrrev_i32_e32 v89, 31, v88
	v_lshlrev_b64 v[0:1], 10, v[88:89]
	v_lshl_add_u64 v[0:1], v[72:73], 0, v[0:1]
	global_store_dword v[0:1], v90, off
	v_mov_b32_e32 v0, s12
	v_readlane_b32 s12, v255, 3
	s_nop 1
	v_mov_b32_e32 v89, s12
	v_readlane_b32 s12, v255, 4
	s_nop 1
	v_mov_b32_e32 v92, s12
	ds_read2_b32 v[0:1], v0 offset1:1
	ds_read2_b32 v[90:91], v89 offset1:1
	ds_read2_b32 v[92:93], v92 offset1:1
	v_readlane_b32 s12, v255, 5
	s_waitcnt lgkmcnt(2)
	v_pk_add_f32 v[0:1], v[0:1], 0 op_sel_hi:[1,0]
	v_mov_b32_e32 v89, s12
	v_readlane_b32 s12, v255, 6
	ds_read2_b32 v[96:97], v89 offset1:1
	s_waitcnt lgkmcnt(2)
	v_pk_add_f32 v[0:1], v[0:1], v[90:91]
	v_mov_b32_e32 v89, s12
	v_readlane_b32 s12, v255, 7
	s_waitcnt lgkmcnt(1)
	v_pk_add_f32 v[0:1], v[0:1], v[92:93]
	v_mov_b32_e32 v92, s12
	v_readlane_b32 s12, v255, 8
	s_waitcnt lgkmcnt(0)
	v_pk_add_f32 v[0:1], v[0:1], v[96:97]
	v_mov_b32_e32 v102, s12
	v_readlane_b32 s12, v255, 9
	s_nop 1
	v_mov_b32_e32 v104, s12
	ds_read2_b32 v[90:91], v89 offset1:1
	ds_read2_b32 v[92:93], v92 offset1:1
	ds_read2_b32 v[102:103], v102 offset1:1
	ds_read2_b32 v[104:105], v104 offset1:1
	s_mov_b32 s12, 0x3727c5ac
	s_waitcnt lgkmcnt(3)
	v_pk_add_f32 v[0:1], v[0:1], v[90:91]
	s_waitcnt lgkmcnt(2)
	v_pk_add_f32 v[0:1], v[0:1], v[92:93]
	s_waitcnt lgkmcnt(1)
	v_pk_add_f32 v[0:1], v[0:1], v[102:103]
	s_waitcnt lgkmcnt(0)
	v_pk_add_f32 v[0:1], v[0:1], v[104:105]
	s_nop 0
	v_pk_mul_f32 v[0:1], v[0:1], s[66:67] op_sel_hi:[1,0]
	s_nop 0
	v_fma_f32 v1, -v0, v0, v1
	v_max_f32_e32 v1, 0, v1
	v_add_f32_e32 v1, s12, v1
	v_mul_f32_e32 v89, 0x4b800000, v1
	v_cmp_gt_f32_e32 vcc, s13, v1
	v_readlane_b32 s12, v255, 10
	v_sub_f32_e32 v74, v74, v0
	v_cndmask_b32_e32 v1, v1, v89, vcc
	v_rsq_f32_e32 v1, v1
	v_sub_f32_e32 v0, v75, v0
	v_mul_f32_e32 v89, 0x45800000, v1
	v_cndmask_b32_e32 v1, v1, v89, vcc
	v_mov_b32_e32 v89, s12
	v_readlane_b32 s12, v255, 11
	v_mul_f32_e32 v74, v74, v1
	v_fma_f32 v74, v70, v74, v68
	v_mov_b32_e32 v92, s12
	v_readlane_b32 s12, v255, 12
	v_mul_f32_e32 v0, v0, v1
	v_fma_f32 v0, v71, v0, v69
	v_mov_b32_e32 v96, s12
	ds_read2_b32 v[90:91], v89 offset1:1
	ds_read2_b32 v[92:93], v92 offset1:1
	ds_read2_b32 v[96:97], v96 offset1:1
	v_readlane_b32 s12, v255, 13
	v_mul_f32_e32 v75, 0xbfb8aa3b, v0
	s_waitcnt lgkmcnt(2)
	v_pk_add_f32 v[90:91], v[90:91], 0 op_sel_hi:[1,0]
	v_mov_b32_e32 v89, s12
	v_readlane_b32 s12, v255, 14
	ds_read2_b32 v[102:103], v89 offset1:1
	s_waitcnt lgkmcnt(2)
	v_pk_add_f32 v[90:91], v[90:91], v[92:93]
	v_mov_b32_e32 v89, s12
	v_readlane_b32 s12, v255, 15
	s_waitcnt lgkmcnt(1)
	v_pk_add_f32 v[90:91], v[90:91], v[96:97]
	v_exp_f32_e32 v75, v75
	v_mov_b32_e32 v96, s12
	v_readlane_b32 s12, v255, 16
	s_waitcnt lgkmcnt(0)
	v_pk_add_f32 v[90:91], v[90:91], v[102:103]
	v_mov_b32_e32 v104, s12
	v_readlane_b32 s12, v255, 17
	s_nop 1
	v_mov_b32_e32 v108, s12
	ds_read2_b32 v[92:93], v89 offset1:1
	ds_read2_b32 v[96:97], v96 offset1:1
	ds_read2_b32 v[104:105], v104 offset1:1
	ds_read2_b32 v[108:109], v108 offset1:1
	s_mov_b32 s12, 0x3727c5ac
	s_waitcnt lgkmcnt(3)
	v_pk_add_f32 v[90:91], v[90:91], v[92:93]
	s_waitcnt lgkmcnt(2)
	v_pk_add_f32 v[90:91], v[90:91], v[96:97]
	s_waitcnt lgkmcnt(1)
	v_pk_add_f32 v[90:91], v[90:91], v[104:105]
	s_waitcnt lgkmcnt(0)
	v_pk_add_f32 v[90:91], v[90:91], v[108:109]
	s_nop 0
	v_pk_mul_f32 v[90:91], v[90:91], s[66:67] op_sel_hi:[1,0]
	s_nop 0
	v_fma_f32 v89, -v90, v90, v91
	v_max_f32_e32 v89, 0, v89
	v_add_f32_e32 v89, s12, v89
	v_mul_f32_e32 v91, 0x4b800000, v89
	v_cmp_gt_f32_e32 vcc, s13, v89
	v_readlane_b32 s12, v255, 18
	s_nop 0
	v_cndmask_b32_e32 v89, v89, v91, vcc
	v_rsq_f32_e32 v89, v89
	s_nop 0
	v_mul_f32_e32 v91, 0x45800000, v89
	v_cndmask_b32_e32 v89, v89, v91, vcc
	v_mul_f32_e32 v91, 0xbfb8aa3b, v74
	v_exp_f32_e32 v91, v91
	s_nop 0
	v_add_f32_e32 v1, 1.0, v91
	v_rcp_f32_e32 v1, v1
	s_nop 0
	v_mul_f32_e32 v1, v74, v1
	v_add_f32_e32 v74, 1.0, v75
	v_sub_f32_e32 v75, v98, v90
	v_sub_f32_e32 v90, v99, v90
	v_mul_f32_e32 v75, v75, v89
	v_mul_f32_e32 v89, v90, v89
	v_fma_f32 v75, v70, v75, v68
	v_fma_f32 v89, v71, v89, v69
	v_mul_f32_e32 v90, 0xbfb8aa3b, v75
	v_mul_f32_e32 v91, 0xbfb8aa3b, v89
	v_rcp_f32_e32 v74, v74
	v_exp_f32_e32 v90, v90
	v_exp_f32_e32 v91, v91
	v_mul_f32_e32 v0, v0, v74
	v_add_f32_e32 v74, 1.0, v90
	v_add_f32_e32 v90, 1.0, v91
	v_rcp_f32_e32 v74, v74
	v_rcp_f32_e32 v90, v90
	v_mov_b32_e32 v91, v201
	v_cvt_pk_fp8_f32 v91, v1, v0
	v_mul_f32_e32 v0, v75, v74
	v_mul_f32_e32 v1, v89, v90
	v_mov_b32_e32 v74, v201
	v_cvt_pk_fp8_f32 v74, v0, v1
	v_cvt_pk_fp8_f32 v91, 0, 0 op_sel:[0,0,1]
	v_cvt_pk_fp8_f32 v74, 0, 0 op_sel:[0,0,1]
	v_and_b32_e32 v0, 0xffff, v91
	v_and_b32_e32 v1, 0xffff, v74
	v_cndmask_b32_e64 v1, v0, v1, s[8:9]
	s_nop 1
	v_mov_b32_dpp v1, v1 quad_perm:[1,0,3,2] row_mask:0xf bank_mask:0xf
	s_waitcnt lgkmcnt(0)
	v_lshl_or_b32 v74, v74, 16, v1
	v_lshl_or_b32 v0, v1, 16, v0
	v_cndmask_b32_e64 v74, v74, v0, s[8:9]
	v_or_b32_e32 v0, 2, v88
	v_ashrrev_i32_e32 v1, 31, v0
	v_lshlrev_b64 v[0:1], 10, v[0:1]
	v_lshl_add_u64 v[0:1], v[72:73], 0, v[0:1]
	global_store_dword v[0:1], v74, off
	v_mov_b32_e32 v0, s12
	v_readlane_b32 s12, v255, 19
	s_nop 1
	v_mov_b32_e32 v74, s12
	v_readlane_b32 s12, v255, 20
	s_nop 1
	v_mov_b32_e32 v89, s12
	ds_read2_b32 v[0:1], v0 offset1:1
	ds_read2_b32 v[74:75], v74 offset1:1
	ds_read2_b32 v[90:91], v89 offset1:1
	v_readlane_b32 s12, v255, 21
	s_waitcnt lgkmcnt(2)
	v_pk_add_f32 v[0:1], v[0:1], 0 op_sel_hi:[1,0]
	v_mov_b32_e32 v89, s12
	v_readlane_b32 s12, v255, 22
	ds_read2_b32 v[92:93], v89 offset1:1
	s_waitcnt lgkmcnt(2)
	v_pk_add_f32 v[0:1], v[0:1], v[74:75]
	v_mov_b32_e32 v74, s12
	v_readlane_b32 s12, v255, 23
	s_waitcnt lgkmcnt(1)
	v_pk_add_f32 v[0:1], v[0:1], v[90:91]
	v_mov_b32_e32 v89, s12
	v_readlane_b32 s12, v255, 24
	s_waitcnt lgkmcnt(0)
	v_pk_add_f32 v[0:1], v[0:1], v[92:93]
	v_mov_b32_e32 v96, s12
	v_readlane_b32 s12, v255, 25
	s_nop 1
	v_mov_b32_e32 v98, s12
	ds_read2_b32 v[74:75], v74 offset1:1
	ds_read2_b32 v[90:91], v89 offset1:1
	ds_read2_b32 v[96:97], v96 offset1:1
	ds_read2_b32 v[98:99], v98 offset1:1
	s_mov_b32 s12, 0x3727c5ac
	s_waitcnt lgkmcnt(3)
	v_pk_add_f32 v[0:1], v[0:1], v[74:75]
	s_waitcnt lgkmcnt(2)
	v_pk_add_f32 v[0:1], v[0:1], v[90:91]
	s_waitcnt lgkmcnt(1)
	v_pk_add_f32 v[0:1], v[0:1], v[96:97]
	s_waitcnt lgkmcnt(0)
	v_pk_add_f32 v[0:1], v[0:1], v[98:99]
	s_nop 0
	v_pk_mul_f32 v[0:1], v[0:1], s[66:67] op_sel_hi:[1,0]
	s_nop 0
	v_fma_f32 v1, -v0, v0, v1
	v_max_f32_e32 v1, 0, v1
	v_add_f32_e32 v1, s12, v1
	v_mul_f32_e32 v74, 0x4b800000, v1
	v_cmp_gt_f32_e32 vcc, s13, v1
	v_readlane_b32 s12, v255, 26
	v_sub_f32_e32 v2, v2, v0
	v_cndmask_b32_e32 v1, v1, v74, vcc
	v_rsq_f32_e32 v1, v1
	v_sub_f32_e32 v0, v3, v0
	v_mul_f32_e32 v74, 0x45800000, v1
	v_cndmask_b32_e32 v1, v1, v74, vcc
	v_mov_b32_e32 v74, s12
	v_readlane_b32 s12, v255, 27
	v_mul_f32_e32 v2, v2, v1
	v_fma_f32 v2, v70, v2, v68
	v_mov_b32_e32 v89, s12
	v_readlane_b32 s12, v255, 28
	v_mul_f32_e32 v0, v0, v1
	v_fma_f32 v0, v71, v0, v69
	v_mov_b32_e32 v92, s12
	ds_read2_b32 v[74:75], v74 offset1:1
	ds_read2_b32 v[90:91], v89 offset1:1
	ds_read2_b32 v[92:93], v92 offset1:1
	v_readlane_b32 s12, v255, 29
	v_mul_f32_e32 v3, 0xbfb8aa3b, v0
	s_waitcnt lgkmcnt(2)
	v_pk_add_f32 v[74:75], v[74:75], 0 op_sel_hi:[1,0]
	v_mov_b32_e32 v89, s12
	v_readlane_b32 s12, v255, 30
	ds_read2_b32 v[96:97], v89 offset1:1
	s_waitcnt lgkmcnt(2)
	v_pk_add_f32 v[74:75], v[74:75], v[90:91]
	v_mov_b32_e32 v89, s12
	v_readlane_b32 s12, v255, 31
	s_waitcnt lgkmcnt(1)
	v_pk_add_f32 v[74:75], v[74:75], v[92:93]
	v_exp_f32_e32 v3, v3
	v_mov_b32_e32 v92, s12
	v_readlane_b32 s12, v255, 32
	s_waitcnt lgkmcnt(0)
	v_pk_add_f32 v[74:75], v[74:75], v[96:97]
	v_mov_b32_e32 v96, s85
	v_mov_b32_e32 v98, s12
	v_readlane_b32 s12, v255, 33
	s_nop 1
	v_mov_b32_e32 v102, s12
	ds_read2_b32 v[90:91], v89 offset1:1
	ds_read2_b32 v[92:93], v92 offset1:1
	ds_read2_b32 v[98:99], v98 offset1:1
	ds_read2_b32 v[102:103], v102 offset1:1
	s_mov_b32 s12, 0x3727c5ac
	s_waitcnt lgkmcnt(3)
	v_pk_add_f32 v[74:75], v[74:75], v[90:91]
	s_waitcnt lgkmcnt(2)
	v_pk_add_f32 v[74:75], v[74:75], v[92:93]
	s_waitcnt lgkmcnt(1)
	v_pk_add_f32 v[74:75], v[74:75], v[98:99]
	s_waitcnt lgkmcnt(0)
	v_pk_add_f32 v[74:75], v[74:75], v[102:103]
	s_nop 0
	v_pk_mul_f32 v[74:75], v[74:75], s[66:67] op_sel_hi:[1,0]
	s_nop 0
	v_fma_f32 v75, -v74, v74, v75
	v_max_f32_e32 v75, 0, v75
	v_add_f32_e32 v75, s12, v75
	v_mul_f32_e32 v89, 0x4b800000, v75
	v_cmp_gt_f32_e32 vcc, s13, v75
	v_readlane_b32 s12, v255, 34
	s_nop 0
	v_cndmask_b32_e32 v75, v75, v89, vcc
	v_rsq_f32_e32 v75, v75
	s_nop 0
	v_mul_f32_e32 v89, 0x45800000, v75
	v_cndmask_b32_e32 v75, v75, v89, vcc
	v_mul_f32_e32 v89, 0xbfb8aa3b, v2
	v_exp_f32_e32 v89, v89
	s_nop 0
	v_add_f32_e32 v1, 1.0, v89
	v_rcp_f32_e32 v1, v1
	s_nop 0
	v_mul_f32_e32 v1, v2, v1
	v_add_f32_e32 v2, 1.0, v3
	v_sub_f32_e32 v3, v94, v74
	v_sub_f32_e32 v74, v95, v74
	v_mul_f32_e32 v3, v3, v75
	v_mul_f32_e32 v74, v74, v75
	v_fma_f32 v3, v70, v3, v68
	v_fma_f32 v74, v71, v74, v69
	v_mul_f32_e32 v75, 0xbfb8aa3b, v3
	v_mul_f32_e32 v89, 0xbfb8aa3b, v74
	v_rcp_f32_e32 v2, v2
	v_exp_f32_e32 v75, v75
	v_exp_f32_e32 v89, v89
	v_mov_b32_e32 v94, s75
	v_mul_f32_e32 v0, v0, v2
	v_add_f32_e32 v2, 1.0, v75
	v_add_f32_e32 v75, 1.0, v89
	v_rcp_f32_e32 v2, v2
	v_rcp_f32_e32 v75, v75
	v_mov_b32_e32 v89, v201
	v_cvt_pk_fp8_f32 v89, v1, v0
	v_mul_f32_e32 v0, v3, v2
	v_mul_f32_e32 v1, v74, v75
	v_mov_b32_e32 v2, v201
	v_cvt_pk_fp8_f32 v2, v0, v1
	v_cvt_pk_fp8_f32 v89, 0, 0 op_sel:[0,0,1]
	v_mov_b32_e32 v74, s70
	v_cvt_pk_fp8_f32 v2, 0, 0 op_sel:[0,0,1]
	v_and_b32_e32 v0, 0xffff, v89
	v_mov_b32_e32 v89, s71
	v_and_b32_e32 v1, 0xffff, v2
	v_cndmask_b32_e64 v1, v0, v1, s[8:9]
	s_nop 1
	v_mov_b32_dpp v1, v1 quad_perm:[1,0,3,2] row_mask:0xf bank_mask:0xf
	s_waitcnt lgkmcnt(0)
	v_lshl_or_b32 v2, v2, 16, v1
	v_lshl_or_b32 v0, v1, 16, v0
	v_cndmask_b32_e64 v2, v2, v0, s[8:9]
	v_or_b32_e32 v0, 4, v88
	v_ashrrev_i32_e32 v1, 31, v0
	v_lshlrev_b64 v[0:1], 10, v[0:1]
	v_lshl_add_u64 v[0:1], v[72:73], 0, v[0:1]
	global_store_dword v[0:1], v2, off
	v_mov_b32_e32 v0, s12
	v_readlane_b32 s12, v255, 35
	s_nop 1
	v_mov_b32_e32 v2, s12
	ds_read2_b32 v[0:1], v0 offset1:1
	ds_read2_b32 v[2:3], v2 offset1:1
	ds_read2_b32 v[74:75], v74 offset1:1
	ds_read2_b32 v[90:91], v89 offset1:1
	v_mov_b32_e32 v89, s74
	s_waitcnt lgkmcnt(3)
	v_pk_add_f32 v[0:1], v[0:1], 0 op_sel_hi:[1,0]
	s_mov_b32 s12, 0x3727c5ac
	s_waitcnt lgkmcnt(2)
	v_pk_add_f32 v[0:1], v[0:1], v[2:3]
	v_mov_b32_e32 v2, s72
	s_waitcnt lgkmcnt(1)
	v_pk_add_f32 v[0:1], v[0:1], v[74:75]
	v_mov_b32_e32 v74, s73
	ds_read2_b32 v[2:3], v2 offset1:1
	ds_read2_b32 v[74:75], v74 offset1:1
	ds_read2_b32 v[92:93], v89 offset1:1
	ds_read2_b32 v[94:95], v94 offset1:1
	s_waitcnt lgkmcnt(4)
	v_pk_add_f32 v[0:1], v[0:1], v[90:91]
	v_mov_b32_e32 v89, s80
	s_waitcnt lgkmcnt(3)
	v_pk_add_f32 v[0:1], v[0:1], v[2:3]
	s_waitcnt lgkmcnt(2)
	v_pk_add_f32 v[0:1], v[0:1], v[74:75]
	v_mov_b32_e32 v74, s79
	s_waitcnt lgkmcnt(1)
	v_pk_add_f32 v[0:1], v[0:1], v[92:93]
	s_waitcnt lgkmcnt(0)
	v_pk_add_f32 v[0:1], v[0:1], v[94:95]
	v_mov_b32_e32 v94, s84
	v_pk_mul_f32 v[0:1], v[0:1], s[66:67] op_sel_hi:[1,0]
	s_nop 0
	v_fma_f32 v1, -v0, v0, v1
	v_max_f32_e32 v1, 0, v1
	v_add_f32_e32 v1, s12, v1
	v_mul_f32_e32 v2, 0x4b800000, v1
	v_cmp_gt_f32_e32 vcc, s13, v1
	s_mov_b32 s12, 0x3727c5ac
	s_nop 0
	v_cndmask_b32_e32 v1, v1, v2, vcc
	v_rsq_f32_e32 v1, v1
	s_nop 0
	v_mul_f32_e32 v2, 0x45800000, v1
	v_cndmask_b32_e32 v1, v1, v2, vcc
	v_mov_b32_e32 v2, s76
	ds_read2_b32 v[2:3], v2 offset1:1
	ds_read2_b32 v[74:75], v74 offset1:1
	ds_read2_b32 v[90:91], v89 offset1:1
	v_mov_b32_e32 v89, s81
	ds_read2_b32 v[92:93], v89 offset1:1
	s_waitcnt lgkmcnt(3)
	v_pk_add_f32 v[2:3], v[2:3], 0 op_sel_hi:[1,0]
	v_mov_b32_e32 v89, s83
	s_waitcnt lgkmcnt(2)
	v_pk_add_f32 v[2:3], v[2:3], v[74:75]
	v_mov_b32_e32 v74, s82
	s_waitcnt lgkmcnt(1)
	v_pk_add_f32 v[2:3], v[2:3], v[90:91]
	ds_read2_b32 v[74:75], v74 offset1:1
	ds_read2_b32 v[90:91], v89 offset1:1
	ds_read2_b32 v[94:95], v94 offset1:1
	ds_read2_b32 v[96:97], v96 offset1:1
	s_waitcnt lgkmcnt(4)
	v_pk_add_f32 v[2:3], v[2:3], v[92:93]
	v_mov_b32_e32 v92, s96
	s_waitcnt lgkmcnt(3)
	v_pk_add_f32 v[2:3], v[2:3], v[74:75]
	v_mov_b32_e32 v89, s95
	s_waitcnt lgkmcnt(2)
	v_pk_add_f32 v[2:3], v[2:3], v[90:91]
	s_waitcnt lgkmcnt(1)
	v_pk_add_f32 v[2:3], v[2:3], v[94:95]
	v_mov_b32_e32 v94, s77
	s_waitcnt lgkmcnt(0)
	v_pk_add_f32 v[2:3], v[2:3], v[96:97]
	s_nop 0
	v_pk_mul_f32 v[2:3], v[2:3], s[66:67] op_sel_hi:[1,0]
	s_nop 0
	v_fma_f32 v3, -v2, v2, v3
	v_max_f32_e32 v3, 0, v3
	v_add_f32_e32 v3, s12, v3
	v_mul_f32_e32 v74, 0x4b800000, v3
	v_cmp_gt_f32_e32 vcc, s13, v3
	s_mov_b32 s12, 0x3727c5ac
	s_nop 0
	v_cndmask_b32_e32 v3, v3, v74, vcc
	v_rsq_f32_e32 v3, v3
	s_nop 0
	v_mul_f32_e32 v74, 0x45800000, v3
	v_cndmask_b32_e32 v3, v3, v74, vcc
	v_sub_f32_e32 v74, v76, v0
	v_mul_f32_e32 v74, v74, v1
	v_fma_f32 v74, v70, v74, v68
	v_mul_f32_e32 v75, 0xbfb8aa3b, v74
	v_exp_f32_e32 v75, v75
	v_sub_f32_e32 v0, v77, v0
	v_mul_f32_e32 v0, v0, v1
	v_fma_f32 v0, v71, v0, v69
	v_add_f32_e32 v1, 1.0, v75
	v_mul_f32_e32 v75, 0xbfb8aa3b, v0
	v_rcp_f32_e32 v1, v1
	v_exp_f32_e32 v75, v75
	v_mul_f32_e32 v1, v74, v1
	v_add_f32_e32 v74, 1.0, v75
	v_sub_f32_e32 v75, v100, v2
	v_sub_f32_e32 v2, v101, v2
	v_mul_f32_e32 v75, v75, v3
	v_mul_f32_e32 v2, v2, v3
	v_fma_f32 v75, v70, v75, v68
	v_fma_f32 v2, v71, v2, v69
	v_mul_f32_e32 v3, 0xbfb8aa3b, v75
	v_mul_f32_e32 v76, 0xbfb8aa3b, v2
	v_rcp_f32_e32 v74, v74
	v_exp_f32_e32 v3, v3
	v_exp_f32_e32 v76, v76
	v_mul_f32_e32 v0, v0, v74
	v_add_f32_e32 v3, 1.0, v3
	v_add_f32_e32 v74, 1.0, v76
	v_rcp_f32_e32 v3, v3
	v_rcp_f32_e32 v74, v74
	v_mov_b32_e32 v76, v201
	v_cvt_pk_fp8_f32 v76, v1, v0
	v_mul_f32_e32 v0, v75, v3
	v_mul_f32_e32 v1, v2, v74
	v_mov_b32_e32 v2, v201
	v_cvt_pk_fp8_f32 v2, v0, v1
	v_cvt_pk_fp8_f32 v76, 0, 0 op_sel:[0,0,1]
	v_mov_b32_e32 v74, s88
	v_cvt_pk_fp8_f32 v2, 0, 0 op_sel:[0,0,1]
	v_and_b32_e32 v0, 0xffff, v76
	v_mov_b32_e32 v76, s89
	v_and_b32_e32 v1, 0xffff, v2
	v_cndmask_b32_e64 v1, v0, v1, s[8:9]
	s_nop 1
	v_mov_b32_dpp v1, v1 quad_perm:[1,0,3,2] row_mask:0xf bank_mask:0xf
	s_waitcnt lgkmcnt(0)
	v_lshl_or_b32 v2, v2, 16, v1
	v_lshl_or_b32 v0, v1, 16, v0
	v_cndmask_b32_e64 v2, v2, v0, s[8:9]
	v_or_b32_e32 v0, 6, v88
	v_ashrrev_i32_e32 v1, 31, v0
	v_lshlrev_b64 v[0:1], 10, v[0:1]
	v_lshl_add_u64 v[0:1], v[72:73], 0, v[0:1]
	global_store_dword v[0:1], v2, off
	v_mov_b32_e32 v0, s86
	v_mov_b32_e32 v2, s87
	ds_read2_b32 v[0:1], v0 offset1:1
	ds_read2_b32 v[2:3], v2 offset1:1
	ds_read2_b32 v[74:75], v74 offset1:1
	ds_read2_b32 v[76:77], v76 offset1:1
	s_waitcnt lgkmcnt(3)
	v_pk_add_f32 v[0:1], v[0:1], 0 op_sel_hi:[1,0]
	s_waitcnt lgkmcnt(2)
	v_pk_add_f32 v[0:1], v[0:1], v[2:3]
	v_mov_b32_e32 v2, s90
	s_waitcnt lgkmcnt(1)
	v_pk_add_f32 v[0:1], v[0:1], v[74:75]
	v_mov_b32_e32 v74, s94
	ds_read2_b32 v[2:3], v2 offset1:1
	ds_read2_b32 v[74:75], v74 offset1:1
	ds_read2_b32 v[90:91], v89 offset1:1
	ds_read2_b32 v[92:93], v92 offset1:1
	s_waitcnt lgkmcnt(4)
	v_pk_add_f32 v[0:1], v[0:1], v[76:77]
	v_mov_b32_e32 v76, s1
	s_waitcnt lgkmcnt(3)
	v_pk_add_f32 v[0:1], v[0:1], v[2:3]
	v_mov_b32_e32 v89, s4
	s_waitcnt lgkmcnt(2)
	v_pk_add_f32 v[0:1], v[0:1], v[74:75]
	v_mov_b32_e32 v74, s0
	s_waitcnt lgkmcnt(1)
	v_pk_add_f32 v[0:1], v[0:1], v[90:91]
	s_waitcnt lgkmcnt(0)
	v_pk_add_f32 v[0:1], v[0:1], v[92:93]
	s_nop 0
	v_pk_mul_f32 v[0:1], v[0:1], s[66:67] op_sel_hi:[1,0]
	s_nop 0
	v_fma_f32 v1, -v0, v0, v1
	v_max_f32_e32 v1, 0, v1
	v_add_f32_e32 v1, s12, v1
	v_mul_f32_e32 v2, 0x4b800000, v1
	v_cmp_gt_f32_e32 vcc, s13, v1
	s_mov_b32 s12, 0x3727c5ac
	s_nop 0
	v_cndmask_b32_e32 v1, v1, v2, vcc
	v_rsq_f32_e32 v1, v1
	s_nop 0
	v_mul_f32_e32 v2, 0x45800000, v1
	v_cndmask_b32_e32 v1, v1, v2, vcc
	v_mov_b32_e32 v2, s97
	ds_read2_b32 v[2:3], v2 offset1:1
	ds_read2_b32 v[74:75], v74 offset1:1
	ds_read2_b32 v[76:77], v76 offset1:1
	ds_read2_b32 v[90:91], v89 offset1:1
	v_mov_b32_e32 v89, s3
	s_waitcnt lgkmcnt(3)
	v_pk_add_f32 v[2:3], v[2:3], 0 op_sel_hi:[1,0]
	s_waitcnt lgkmcnt(2)
	v_pk_add_f32 v[2:3], v[2:3], v[74:75]
	v_mov_b32_e32 v74, s5
	s_waitcnt lgkmcnt(1)
	v_pk_add_f32 v[2:3], v[2:3], v[76:77]
	v_mov_b32_e32 v76, s2
	ds_read2_b32 v[74:75], v74 offset1:1
	ds_read2_b32 v[76:77], v76 offset1:1
	ds_read2_b32 v[92:93], v89 offset1:1
	ds_read2_b32 v[94:95], v94 offset1:1
	s_waitcnt lgkmcnt(4)
	v_pk_add_f32 v[2:3], v[2:3], v[90:91]
	v_mov_b32_e32 v89, s21
	s_waitcnt lgkmcnt(3)
	v_pk_add_f32 v[2:3], v[2:3], v[74:75]
	s_waitcnt lgkmcnt(2)
	v_pk_add_f32 v[2:3], v[2:3], v[76:77]
	s_waitcnt lgkmcnt(1)
	v_pk_add_f32 v[2:3], v[2:3], v[92:93]
	v_mov_b32_e32 v92, s29
	s_waitcnt lgkmcnt(0)
	v_pk_add_f32 v[2:3], v[2:3], v[94:95]
	s_nop 0
	v_pk_mul_f32 v[2:3], v[2:3], s[66:67] op_sel_hi:[1,0]
	s_nop 0
	v_fma_f32 v3, -v2, v2, v3
	v_max_f32_e32 v3, 0, v3
	v_add_f32_e32 v3, s12, v3
	v_mul_f32_e32 v74, 0x4b800000, v3
	v_cmp_gt_f32_e32 vcc, s13, v3
	s_mov_b32 s12, 0x3727c5ac
	s_nop 0
	v_cndmask_b32_e32 v3, v3, v74, vcc
	v_rsq_f32_e32 v3, v3
	s_nop 0
	v_mul_f32_e32 v74, 0x45800000, v3
	v_cndmask_b32_e32 v3, v3, v74, vcc
	v_sub_f32_e32 v74, v78, v0
	v_mul_f32_e32 v74, v74, v1
	v_fma_f32 v74, v70, v74, v68
	v_mul_f32_e32 v75, 0xbfb8aa3b, v74
	v_exp_f32_e32 v75, v75
	v_sub_f32_e32 v0, v79, v0
	v_mul_f32_e32 v0, v0, v1
	v_fma_f32 v0, v71, v0, v69
	v_add_f32_e32 v1, 1.0, v75
	v_mul_f32_e32 v75, 0xbfb8aa3b, v0
	v_rcp_f32_e32 v1, v1
	v_exp_f32_e32 v75, v75
	v_mov_b32_e32 v78, s20
	v_mul_f32_e32 v1, v74, v1
	v_add_f32_e32 v74, 1.0, v75
	v_sub_f32_e32 v75, v106, v2
	v_sub_f32_e32 v2, v107, v2
	v_mul_f32_e32 v75, v75, v3
	v_mul_f32_e32 v2, v2, v3
	v_fma_f32 v75, v70, v75, v68
	v_fma_f32 v2, v71, v2, v69
	v_mul_f32_e32 v3, 0xbfb8aa3b, v75
	v_mul_f32_e32 v76, 0xbfb8aa3b, v2
	v_rcp_f32_e32 v74, v74
	v_exp_f32_e32 v3, v3
	v_exp_f32_e32 v76, v76
	v_mul_f32_e32 v0, v0, v74
	v_add_f32_e32 v3, 1.0, v3
	v_add_f32_e32 v74, 1.0, v76
	v_rcp_f32_e32 v3, v3
	v_rcp_f32_e32 v74, v74
	v_mov_b32_e32 v76, v201
	v_cvt_pk_fp8_f32 v76, v1, v0
	v_mul_f32_e32 v0, v75, v3
	v_mul_f32_e32 v1, v2, v74
	v_mov_b32_e32 v2, v201
	v_cvt_pk_fp8_f32 v2, v0, v1
	v_cvt_pk_fp8_f32 v76, 0, 0 op_sel:[0,0,1]
	v_mov_b32_e32 v74, s33
	v_cvt_pk_fp8_f32 v2, 0, 0 op_sel:[0,0,1]
	v_and_b32_e32 v0, 0xffff, v76
	v_mov_b32_e32 v76, s15
	v_and_b32_e32 v1, 0xffff, v2
	v_cndmask_b32_e64 v1, v0, v1, s[8:9]
	s_nop 1
	v_mov_b32_dpp v1, v1 quad_perm:[1,0,3,2] row_mask:0xf bank_mask:0xf
	s_waitcnt lgkmcnt(0)
	v_lshl_or_b32 v2, v2, 16, v1
	v_lshl_or_b32 v0, v1, 16, v0
	v_cndmask_b32_e64 v2, v2, v0, s[8:9]
	v_or_b32_e32 v0, 8, v88
	v_ashrrev_i32_e32 v1, 31, v0
	v_lshlrev_b64 v[0:1], 10, v[0:1]
	v_lshl_add_u64 v[0:1], v[72:73], 0, v[0:1]
	global_store_dword v[0:1], v2, off
	v_mov_b32_e32 v0, s92
	v_mov_b32_e32 v2, s93
	ds_read2_b32 v[0:1], v0 offset1:1
	ds_read2_b32 v[2:3], v2 offset1:1
	ds_read2_b32 v[74:75], v74 offset1:1
	ds_read2_b32 v[76:77], v76 offset1:1
	s_waitcnt lgkmcnt(3)
	v_pk_add_f32 v[0:1], v[0:1], 0 op_sel_hi:[1,0]
	s_waitcnt lgkmcnt(2)
	v_pk_add_f32 v[0:1], v[0:1], v[2:3]
	v_mov_b32_e32 v2, s16
	s_waitcnt lgkmcnt(1)
	v_pk_add_f32 v[0:1], v[0:1], v[74:75]
	v_mov_b32_e32 v74, s17
	ds_read2_b32 v[2:3], v2 offset1:1
	ds_read2_b32 v[74:75], v74 offset1:1
	ds_read2_b32 v[78:79], v78 offset1:1
	ds_read2_b32 v[90:91], v89 offset1:1
	s_waitcnt lgkmcnt(4)
	v_pk_add_f32 v[0:1], v[0:1], v[76:77]
	v_mov_b32_e32 v76, s24
	s_waitcnt lgkmcnt(3)
	v_pk_add_f32 v[0:1], v[0:1], v[2:3]
	v_mov_b32_e32 v89, s28
	s_waitcnt lgkmcnt(2)
	v_pk_add_f32 v[0:1], v[0:1], v[74:75]
	v_mov_b32_e32 v74, s23
	s_waitcnt lgkmcnt(1)
	v_pk_add_f32 v[0:1], v[0:1], v[78:79]
	v_mov_b32_e32 v78, s25
	s_waitcnt lgkmcnt(0)
	v_pk_add_f32 v[0:1], v[0:1], v[90:91]
	s_nop 0
	v_pk_mul_f32 v[0:1], v[0:1], s[66:67] op_sel_hi:[1,0]
	s_nop 0
	v_fma_f32 v1, -v0, v0, v1
	v_max_f32_e32 v1, 0, v1
	v_add_f32_e32 v1, s12, v1
	v_mul_f32_e32 v2, 0x4b800000, v1
	v_cmp_gt_f32_e32 vcc, s13, v1
	s_mov_b32 s12, 0x3727c5ac
	s_nop 0
	v_cndmask_b32_e32 v1, v1, v2, vcc
	v_rsq_f32_e32 v1, v1
	s_nop 0
	v_mul_f32_e32 v2, 0x45800000, v1
	v_cndmask_b32_e32 v1, v1, v2, vcc
	v_mov_b32_e32 v2, s22
	ds_read2_b32 v[2:3], v2 offset1:1
	ds_read2_b32 v[74:75], v74 offset1:1
	ds_read2_b32 v[76:77], v76 offset1:1
	ds_read2_b32 v[78:79], v78 offset1:1
	s_waitcnt lgkmcnt(3)
	v_pk_add_f32 v[2:3], v[2:3], 0 op_sel_hi:[1,0]
	s_waitcnt lgkmcnt(2)
	v_pk_add_f32 v[2:3], v[2:3], v[74:75]
	v_mov_b32_e32 v74, s26
	s_waitcnt lgkmcnt(1)
	v_pk_add_f32 v[2:3], v[2:3], v[76:77]
	v_mov_b32_e32 v76, s27
	ds_read2_b32 v[74:75], v74 offset1:1
	ds_read2_b32 v[76:77], v76 offset1:1
	ds_read2_b32 v[90:91], v89 offset1:1
	ds_read2_b32 v[92:93], v92 offset1:1
	s_waitcnt lgkmcnt(4)
	v_pk_add_f32 v[2:3], v[2:3], v[78:79]
	v_mov_b32_e32 v78, s39
	s_waitcnt lgkmcnt(3)
	v_pk_add_f32 v[2:3], v[2:3], v[74:75]
	v_mov_b32_e32 v89, s48
	s_waitcnt lgkmcnt(2)
	v_pk_add_f32 v[2:3], v[2:3], v[76:77]
	s_waitcnt lgkmcnt(1)
	v_pk_add_f32 v[2:3], v[2:3], v[90:91]
	s_waitcnt lgkmcnt(0)
	v_pk_add_f32 v[2:3], v[2:3], v[92:93]
	s_nop 0
	v_pk_mul_f32 v[2:3], v[2:3], s[66:67] op_sel_hi:[1,0]
	s_nop 0
	v_fma_f32 v3, -v2, v2, v3
	v_max_f32_e32 v3, 0, v3
	v_add_f32_e32 v3, s12, v3
	v_mul_f32_e32 v74, 0x4b800000, v3
	v_cmp_gt_f32_e32 vcc, s13, v3
	s_mov_b32 s12, 0x3727c5ac
	s_nop 0
	v_cndmask_b32_e32 v3, v3, v74, vcc
	v_rsq_f32_e32 v3, v3
	s_nop 0
	v_mul_f32_e32 v74, 0x45800000, v3
	v_cndmask_b32_e32 v3, v3, v74, vcc
	v_sub_f32_e32 v74, v80, v0
	v_mul_f32_e32 v74, v74, v1
	v_fma_f32 v74, v70, v74, v68
	v_mul_f32_e32 v75, 0xbfb8aa3b, v74
	v_exp_f32_e32 v75, v75
	v_sub_f32_e32 v0, v81, v0
	v_mul_f32_e32 v0, v0, v1
	v_fma_f32 v0, v71, v0, v69
	v_add_f32_e32 v1, 1.0, v75
	v_mul_f32_e32 v75, 0xbfb8aa3b, v0
	v_rcp_f32_e32 v1, v1
	v_exp_f32_e32 v75, v75
	v_mov_b32_e32 v80, s40
	v_mul_f32_e32 v1, v74, v1
	v_add_f32_e32 v74, 1.0, v75
	v_sub_f32_e32 v75, v114, v2
	v_sub_f32_e32 v2, v115, v2
	v_mul_f32_e32 v75, v75, v3
	v_mul_f32_e32 v2, v2, v3
	v_fma_f32 v75, v70, v75, v68
	v_fma_f32 v2, v71, v2, v69
	v_mul_f32_e32 v3, 0xbfb8aa3b, v75
	v_mul_f32_e32 v76, 0xbfb8aa3b, v2
	v_rcp_f32_e32 v74, v74
	v_exp_f32_e32 v3, v3
	v_exp_f32_e32 v76, v76
	v_mul_f32_e32 v0, v0, v74
	v_add_f32_e32 v3, 1.0, v3
	v_add_f32_e32 v74, 1.0, v76
	v_rcp_f32_e32 v3, v3
	v_rcp_f32_e32 v74, v74
	v_mov_b32_e32 v76, v201
	v_cvt_pk_fp8_f32 v76, v1, v0
	v_mul_f32_e32 v0, v75, v3
	v_mul_f32_e32 v1, v2, v74
	v_mov_b32_e32 v2, v201
	v_cvt_pk_fp8_f32 v2, v0, v1
	v_cvt_pk_fp8_f32 v76, 0, 0 op_sel:[0,0,1]
	v_mov_b32_e32 v74, s34
	v_cvt_pk_fp8_f32 v2, 0, 0 op_sel:[0,0,1]
	v_and_b32_e32 v0, 0xffff, v76
	v_mov_b32_e32 v76, s35
	v_and_b32_e32 v1, 0xffff, v2
	v_cndmask_b32_e64 v1, v0, v1, s[8:9]
	s_nop 1
	v_mov_b32_dpp v1, v1 quad_perm:[1,0,3,2] row_mask:0xf bank_mask:0xf
	s_waitcnt lgkmcnt(0)
	v_lshl_or_b32 v2, v2, 16, v1
	v_lshl_or_b32 v0, v1, 16, v0
	v_cndmask_b32_e64 v2, v2, v0, s[8:9]
	v_or_b32_e32 v0, 10, v88
	v_ashrrev_i32_e32 v1, 31, v0
	v_lshlrev_b64 v[0:1], 10, v[0:1]
	v_lshl_add_u64 v[0:1], v[72:73], 0, v[0:1]
	global_store_dword v[0:1], v2, off
	v_mov_b32_e32 v0, s30
	v_mov_b32_e32 v2, s31
	ds_read2_b32 v[0:1], v0 offset1:1
	ds_read2_b32 v[2:3], v2 offset1:1
	ds_read2_b32 v[74:75], v74 offset1:1
	ds_read2_b32 v[76:77], v76 offset1:1
	s_waitcnt lgkmcnt(3)
	v_pk_add_f32 v[0:1], v[0:1], 0 op_sel_hi:[1,0]
	s_waitcnt lgkmcnt(2)
	v_pk_add_f32 v[0:1], v[0:1], v[2:3]
	v_mov_b32_e32 v2, s36
	s_waitcnt lgkmcnt(1)
	v_pk_add_f32 v[0:1], v[0:1], v[74:75]
	v_mov_b32_e32 v74, s38
	ds_read2_b32 v[2:3], v2 offset1:1
	ds_read2_b32 v[74:75], v74 offset1:1
	ds_read2_b32 v[78:79], v78 offset1:1
	ds_read2_b32 v[80:81], v80 offset1:1
	s_waitcnt lgkmcnt(4)
	v_pk_add_f32 v[0:1], v[0:1], v[76:77]
	v_mov_b32_e32 v76, s43
	s_waitcnt lgkmcnt(3)
	v_pk_add_f32 v[0:1], v[0:1], v[2:3]
	s_waitcnt lgkmcnt(2)
	v_pk_add_f32 v[0:1], v[0:1], v[74:75]
	v_mov_b32_e32 v74, s42
	s_waitcnt lgkmcnt(1)
	v_pk_add_f32 v[0:1], v[0:1], v[78:79]
	v_mov_b32_e32 v78, s44
	s_waitcnt lgkmcnt(0)
	v_pk_add_f32 v[0:1], v[0:1], v[80:81]
	v_mov_b32_e32 v80, s47
	v_pk_mul_f32 v[0:1], v[0:1], s[66:67] op_sel_hi:[1,0]
	s_nop 0
	v_fma_f32 v1, -v0, v0, v1
	v_max_f32_e32 v1, 0, v1
	v_add_f32_e32 v1, s12, v1
	v_mul_f32_e32 v2, 0x4b800000, v1
	v_cmp_gt_f32_e32 vcc, s13, v1
	s_mov_b32 s12, 0x3727c5ac
	s_nop 0
	v_cndmask_b32_e32 v1, v1, v2, vcc
	v_rsq_f32_e32 v1, v1
	s_nop 0
	v_mul_f32_e32 v2, 0x45800000, v1
	v_cndmask_b32_e32 v1, v1, v2, vcc
	v_mov_b32_e32 v2, s41
	ds_read2_b32 v[2:3], v2 offset1:1
	ds_read2_b32 v[74:75], v74 offset1:1
	ds_read2_b32 v[76:77], v76 offset1:1
	ds_read2_b32 v[78:79], v78 offset1:1
	s_waitcnt lgkmcnt(3)
	v_pk_add_f32 v[2:3], v[2:3], 0 op_sel_hi:[1,0]
	s_waitcnt lgkmcnt(2)
	v_pk_add_f32 v[2:3], v[2:3], v[74:75]
	v_mov_b32_e32 v74, s45
	s_waitcnt lgkmcnt(1)
	v_pk_add_f32 v[2:3], v[2:3], v[76:77]
	v_mov_b32_e32 v76, s46
	ds_read2_b32 v[74:75], v74 offset1:1
	ds_read2_b32 v[76:77], v76 offset1:1
	ds_read2_b32 v[80:81], v80 offset1:1
	ds_read2_b32 v[90:91], v89 offset1:1
	s_waitcnt lgkmcnt(4)
	v_pk_add_f32 v[2:3], v[2:3], v[78:79]
	v_mov_b32_e32 v78, s55
	s_waitcnt lgkmcnt(3)
	v_pk_add_f32 v[2:3], v[2:3], v[74:75]
	s_waitcnt lgkmcnt(2)
	v_pk_add_f32 v[2:3], v[2:3], v[76:77]
	s_waitcnt lgkmcnt(1)
	v_pk_add_f32 v[2:3], v[2:3], v[80:81]
	v_mov_b32_e32 v80, s56
	s_waitcnt lgkmcnt(0)
	v_pk_add_f32 v[2:3], v[2:3], v[90:91]
	s_nop 0
	v_pk_mul_f32 v[2:3], v[2:3], s[66:67] op_sel_hi:[1,0]
	s_nop 0
	v_fma_f32 v3, -v2, v2, v3
	v_max_f32_e32 v3, 0, v3
	v_add_f32_e32 v3, s12, v3
	v_mul_f32_e32 v74, 0x4b800000, v3
	v_cmp_gt_f32_e32 vcc, s13, v3
	s_mov_b32 s12, 0x3727c5ac
	s_nop 0
	v_cndmask_b32_e32 v3, v3, v74, vcc
	v_rsq_f32_e32 v3, v3
	s_nop 0
	v_mul_f32_e32 v74, 0x45800000, v3
	v_cndmask_b32_e32 v3, v3, v74, vcc
	v_sub_f32_e32 v74, v82, v0
	v_mul_f32_e32 v74, v74, v1
	v_fma_f32 v74, v70, v74, v68
	v_mul_f32_e32 v75, 0xbfb8aa3b, v74
	v_exp_f32_e32 v75, v75
	v_sub_f32_e32 v0, v83, v0
	v_mul_f32_e32 v0, v0, v1
	v_fma_f32 v0, v71, v0, v69
	v_add_f32_e32 v1, 1.0, v75
	v_mul_f32_e32 v75, 0xbfb8aa3b, v0
	v_rcp_f32_e32 v1, v1
	v_exp_f32_e32 v75, v75
	v_mov_b32_e32 v82, s63
	v_mul_f32_e32 v1, v74, v1
	v_add_f32_e32 v74, 1.0, v75
	v_sub_f32_e32 v75, v116, v2
	v_sub_f32_e32 v2, v117, v2
	v_mul_f32_e32 v75, v75, v3
	v_mul_f32_e32 v2, v2, v3
	v_fma_f32 v75, v70, v75, v68
	v_fma_f32 v2, v71, v2, v69
	v_mul_f32_e32 v3, 0xbfb8aa3b, v75
	v_mul_f32_e32 v76, 0xbfb8aa3b, v2
	v_rcp_f32_e32 v74, v74
	v_exp_f32_e32 v3, v3
	v_exp_f32_e32 v76, v76
	v_mul_f32_e32 v0, v0, v74
	v_add_f32_e32 v3, 1.0, v3
	v_add_f32_e32 v74, 1.0, v76
	v_rcp_f32_e32 v3, v3
	v_rcp_f32_e32 v74, v74
	v_mov_b32_e32 v76, v201
	v_cvt_pk_fp8_f32 v76, v1, v0
	v_mul_f32_e32 v0, v75, v3
	v_mul_f32_e32 v1, v2, v74
	v_mov_b32_e32 v2, v201
	v_cvt_pk_fp8_f32 v2, v0, v1
	v_cvt_pk_fp8_f32 v76, 0, 0 op_sel:[0,0,1]
	v_mov_b32_e32 v74, s51
	v_cvt_pk_fp8_f32 v2, 0, 0 op_sel:[0,0,1]
	v_and_b32_e32 v0, 0xffff, v76
	v_mov_b32_e32 v76, s52
	v_and_b32_e32 v1, 0xffff, v2
	v_cndmask_b32_e64 v1, v0, v1, s[8:9]
	s_nop 1
	v_mov_b32_dpp v1, v1 quad_perm:[1,0,3,2] row_mask:0xf bank_mask:0xf
	s_waitcnt lgkmcnt(0)
	v_lshl_or_b32 v2, v2, 16, v1
	v_lshl_or_b32 v0, v1, 16, v0
	v_cndmask_b32_e64 v2, v2, v0, s[8:9]
	v_or_b32_e32 v0, 12, v88
	v_ashrrev_i32_e32 v1, 31, v0
	v_lshlrev_b64 v[0:1], 10, v[0:1]
	v_lshl_add_u64 v[0:1], v[72:73], 0, v[0:1]
	global_store_dword v[0:1], v2, off
	v_mov_b32_e32 v0, s49
	v_mov_b32_e32 v2, s50
	ds_read2_b32 v[0:1], v0 offset1:1
	ds_read2_b32 v[2:3], v2 offset1:1
	ds_read2_b32 v[74:75], v74 offset1:1
	ds_read2_b32 v[76:77], v76 offset1:1
	s_waitcnt lgkmcnt(3)
	v_pk_add_f32 v[0:1], v[0:1], 0 op_sel_hi:[1,0]
	s_waitcnt lgkmcnt(2)
	v_pk_add_f32 v[0:1], v[0:1], v[2:3]
	v_mov_b32_e32 v2, s53
	s_waitcnt lgkmcnt(1)
	v_pk_add_f32 v[0:1], v[0:1], v[74:75]
	v_mov_b32_e32 v74, s54
	ds_read2_b32 v[2:3], v2 offset1:1
	ds_read2_b32 v[74:75], v74 offset1:1
	ds_read2_b32 v[78:79], v78 offset1:1
	ds_read2_b32 v[80:81], v80 offset1:1
	s_waitcnt lgkmcnt(4)
	v_pk_add_f32 v[0:1], v[0:1], v[76:77]
	v_mov_b32_e32 v76, s58
	s_waitcnt lgkmcnt(3)
	v_pk_add_f32 v[0:1], v[0:1], v[2:3]
	s_waitcnt lgkmcnt(2)
	v_pk_add_f32 v[0:1], v[0:1], v[74:75]
	v_mov_b32_e32 v74, s57
	s_waitcnt lgkmcnt(1)
	v_pk_add_f32 v[0:1], v[0:1], v[78:79]
	v_mov_b32_e32 v78, s59
	s_waitcnt lgkmcnt(0)
	v_pk_add_f32 v[0:1], v[0:1], v[80:81]
	v_mov_b32_e32 v80, s62
	v_pk_mul_f32 v[0:1], v[0:1], s[66:67] op_sel_hi:[1,0]
	s_nop 0
	v_fma_f32 v1, -v0, v0, v1
	v_max_f32_e32 v1, 0, v1
	v_add_f32_e32 v1, s12, v1
	v_mul_f32_e32 v2, 0x4b800000, v1
	v_cmp_gt_f32_e32 vcc, s13, v1
	s_mov_b32 s12, 0x3727c5ac
	s_nop 0
	v_cndmask_b32_e32 v1, v1, v2, vcc
	v_rsq_f32_e32 v1, v1
	s_nop 0
	v_mul_f32_e32 v2, 0x45800000, v1
	v_cndmask_b32_e32 v1, v1, v2, vcc
	v_mov_b32_e32 v2, s65
	ds_read2_b32 v[2:3], v2 offset1:1
	ds_read2_b32 v[74:75], v74 offset1:1
	ds_read2_b32 v[76:77], v76 offset1:1
	ds_read2_b32 v[78:79], v78 offset1:1
	s_waitcnt lgkmcnt(3)
	v_pk_add_f32 v[2:3], v[2:3], 0 op_sel_hi:[1,0]
	s_waitcnt lgkmcnt(2)
	v_pk_add_f32 v[2:3], v[2:3], v[74:75]
	v_mov_b32_e32 v74, s60
	s_waitcnt lgkmcnt(1)
	v_pk_add_f32 v[2:3], v[2:3], v[76:77]
	v_mov_b32_e32 v76, s61
	ds_read2_b32 v[74:75], v74 offset1:1
	ds_read2_b32 v[76:77], v76 offset1:1
	ds_read2_b32 v[80:81], v80 offset1:1
	ds_read2_b32 v[82:83], v82 offset1:1
	s_waitcnt lgkmcnt(4)
	v_pk_add_f32 v[2:3], v[2:3], v[78:79]
	s_waitcnt lgkmcnt(3)
	v_pk_add_f32 v[2:3], v[2:3], v[74:75]
	s_waitcnt lgkmcnt(2)
	v_pk_add_f32 v[2:3], v[2:3], v[76:77]
	s_waitcnt lgkmcnt(1)
	v_pk_add_f32 v[2:3], v[2:3], v[80:81]
	s_waitcnt lgkmcnt(0)
	v_pk_add_f32 v[2:3], v[2:3], v[82:83]
	s_nop 0
	v_pk_mul_f32 v[2:3], v[2:3], s[66:67] op_sel_hi:[1,0]
	s_nop 0
	v_fma_f32 v3, -v2, v2, v3
	v_max_f32_e32 v3, 0, v3
	v_add_f32_e32 v3, s12, v3
	v_mul_f32_e32 v74, 0x4b800000, v3
	v_cmp_gt_f32_e32 vcc, s13, v3
	s_nop 1
	v_cndmask_b32_e32 v3, v3, v74, vcc
	v_rsq_f32_e32 v3, v3
	s_nop 0
	v_mul_f32_e32 v74, 0x45800000, v3
	v_cndmask_b32_e32 v3, v3, v74, vcc
	v_sub_f32_e32 v74, v84, v0
	v_mul_f32_e32 v74, v74, v1
	v_fma_f32 v74, v70, v74, v68
	v_mul_f32_e32 v75, 0xbfb8aa3b, v74
	v_exp_f32_e32 v75, v75
	v_sub_f32_e32 v0, v85, v0
	v_mul_f32_e32 v0, v0, v1
	v_fma_f32 v0, v71, v0, v69
	v_add_f32_e32 v1, 1.0, v75
	v_mul_f32_e32 v75, 0xbfb8aa3b, v0
	v_rcp_f32_e32 v1, v1
	v_exp_f32_e32 v75, v75
	s_and_b64 vcc, exec, s[10:11]
	s_mov_b64 s[10:11], 0
	v_mul_f32_e32 v1, v74, v1
	v_add_f32_e32 v74, 1.0, v75
	v_sub_f32_e32 v75, v86, v2
	v_sub_f32_e32 v2, v87, v2
	v_mul_f32_e32 v75, v75, v3
	v_mul_f32_e32 v2, v2, v3
	v_fma_f32 v75, v70, v75, v68
	v_fma_f32 v2, v71, v2, v69
	v_mul_f32_e32 v3, 0xbfb8aa3b, v75
	v_mul_f32_e32 v76, 0xbfb8aa3b, v2
	v_rcp_f32_e32 v74, v74
	v_exp_f32_e32 v3, v3
	v_exp_f32_e32 v76, v76
	v_mul_f32_e32 v0, v0, v74
	v_add_f32_e32 v3, 1.0, v3
	v_add_f32_e32 v74, 1.0, v76
	v_rcp_f32_e32 v3, v3
	v_rcp_f32_e32 v74, v74
	v_mov_b32_e32 v76, v201
	v_cvt_pk_fp8_f32 v76, v1, v0
	v_mul_f32_e32 v0, v75, v3
	v_mul_f32_e32 v1, v2, v74
	v_mov_b32_e32 v2, v201
	v_cvt_pk_fp8_f32 v2, v0, v1
	v_cvt_pk_fp8_f32 v76, 0, 0 op_sel:[0,0,1]
	v_cvt_pk_fp8_f32 v2, 0, 0 op_sel:[0,0,1]
	v_and_b32_e32 v0, 0xffff, v76
	v_and_b32_e32 v1, 0xffff, v2
	v_cndmask_b32_e64 v1, v0, v1, s[8:9]
	s_nop 1
	v_mov_b32_dpp v1, v1 quad_perm:[1,0,3,2] row_mask:0xf bank_mask:0xf
	s_waitcnt lgkmcnt(0)
	v_lshl_or_b32 v2, v2, 16, v1
	v_lshl_or_b32 v0, v1, 16, v0
	v_cndmask_b32_e64 v2, v2, v0, s[8:9]
	v_or_b32_e32 v0, 14, v88
	v_ashrrev_i32_e32 v1, 31, v0
	v_lshlrev_b64 v[0:1], 10, v[0:1]
	v_lshl_add_u64 v[0:1], v[72:73], 0, v[0:1]
	global_store_dword v[0:1], v2, off
	s_barrier
	s_cbranch_vccnz .LBB0_425
.LBB0_433:
	v_lshl_add_u32 v136, s18, 15, v165
	ds_read2st64_b32 v[0:1], v136 offset1:8
	ds_read2st64_b32 v[2:3], v136 offset0:16 offset1:24
	ds_read2st64_b32 v[76:77], v136 offset0:32 offset1:40
	ds_read2st64_b32 v[78:79], v136 offset0:48 offset1:56
	s_waitcnt lgkmcnt(3)
	v_lshlrev_b32_e32 v74, 16, v0
	v_and_b32_e32 v75, 0xffff0000, v0
	v_lshlrev_b32_e32 v104, 16, v1
	v_and_b32_e32 v105, 0xffff0000, v1
	v_pk_fma_f32 v[0:1], v[4:5], v[74:75], v[66:67]
	s_waitcnt lgkmcnt(2)
	v_lshlrev_b32_e32 v74, 16, v2
	v_pk_fma_f32 v[0:1], v[6:7], v[104:105], v[0:1]
	v_and_b32_e32 v75, 0xffff0000, v2
	v_pk_fma_f32 v[0:1], v[8:9], v[74:75], v[0:1]
	v_lshlrev_b32_e32 v98, 16, v3
	v_and_b32_e32 v99, 0xffff0000, v3
	v_pk_fma_f32 v[0:1], v[10:11], v[98:99], v[0:1]
	s_waitcnt lgkmcnt(1)
	v_lshlrev_b32_e32 v2, 16, v76
	v_and_b32_e32 v3, 0xffff0000, v76
	v_pk_fma_f32 v[0:1], v[12:13], v[2:3], v[0:1]
	v_lshlrev_b32_e32 v94, 16, v77
	v_and_b32_e32 v95, 0xffff0000, v77
	v_pk_fma_f32 v[0:1], v[14:15], v[94:95], v[0:1]
	s_waitcnt lgkmcnt(0)
	v_lshlrev_b32_e32 v76, 16, v78
	v_and_b32_e32 v77, 0xffff0000, v78
	v_pk_fma_f32 v[0:1], v[16:17], v[76:77], v[0:1]
	v_lshlrev_b32_e32 v100, 16, v79
	v_and_b32_e32 v101, 0xffff0000, v79
	v_pk_fma_f32 v[0:1], v[18:19], v[100:101], v[0:1]
	ds_read2st64_b32 v[80:81], v136 offset0:64 offset1:72
	ds_read2st64_b32 v[82:83], v136 offset0:80 offset1:88
	ds_read2st64_b32 v[84:85], v136 offset0:96 offset1:104
	ds_read2st64_b32 v[86:87], v136 offset0:112 offset1:120
	s_waitcnt lgkmcnt(3)
	v_lshlrev_b32_e32 v78, 16, v80
	v_and_b32_e32 v79, 0xffff0000, v80
	v_lshlrev_b32_e32 v106, 16, v81
	v_and_b32_e32 v107, 0xffff0000, v81
	v_pk_fma_f32 v[0:1], v[20:21], v[78:79], v[0:1]
	s_waitcnt lgkmcnt(2)
	v_lshlrev_b32_e32 v80, 16, v82
	v_pk_fma_f32 v[0:1], v[22:23], v[106:107], v[0:1]
	v_and_b32_e32 v81, 0xffff0000, v82
	v_pk_fma_f32 v[0:1], v[24:25], v[80:81], v[0:1]
	v_lshlrev_b32_e32 v114, 16, v83
	v_and_b32_e32 v115, 0xffff0000, v83
	v_pk_fma_f32 v[0:1], v[26:27], v[114:115], v[0:1]
	s_waitcnt lgkmcnt(1)
	v_lshlrev_b32_e32 v82, 16, v84
	v_and_b32_e32 v83, 0xffff0000, v84
	v_pk_fma_f32 v[0:1], v[28:29], v[82:83], v[0:1]
	v_lshlrev_b32_e32 v116, 16, v85
	v_and_b32_e32 v117, 0xffff0000, v85
	v_pk_fma_f32 v[0:1], v[30:31], v[116:117], v[0:1]
	s_waitcnt lgkmcnt(0)
	v_lshlrev_b32_e32 v84, 16, v86
	v_and_b32_e32 v85, 0xffff0000, v86
	v_pk_fma_f32 v[0:1], v[32:33], v[84:85], v[0:1]
	v_lshlrev_b32_e32 v86, 16, v87
	v_and_b32_e32 v87, 0xffff0000, v87
	v_pk_fma_f32 v[0:1], v[34:35], v[86:87], v[0:1]
	ds_read2st64_b32 v[90:91], v136 offset0:128 offset1:136
	ds_read2st64_b32 v[96:97], v136 offset0:144 offset1:152
	ds_read2st64_b32 v[108:109], v136 offset0:160 offset1:168
	ds_read2st64_b32 v[112:113], v136 offset0:176 offset1:184
	s_waitcnt lgkmcnt(3)
	v_lshlrev_b32_e32 v88, 16, v90
	v_and_b32_e32 v89, 0xffff0000, v90
	v_lshlrev_b32_e32 v90, 16, v91
	v_and_b32_e32 v91, 0xffff0000, v91
	v_pk_fma_f32 v[0:1], v[36:37], v[88:89], v[0:1]
	s_waitcnt lgkmcnt(2)
	v_lshlrev_b32_e32 v92, 16, v96
	v_pk_fma_f32 v[0:1], v[38:39], v[90:91], v[0:1]
	v_and_b32_e32 v93, 0xffff0000, v96
	v_pk_fma_f32 v[0:1], v[40:41], v[92:93], v[0:1]
	v_lshlrev_b32_e32 v96, 16, v97
	v_and_b32_e32 v97, 0xffff0000, v97
	v_pk_fma_f32 v[0:1], v[42:43], v[96:97], v[0:1]
	s_waitcnt lgkmcnt(1)
	v_lshlrev_b32_e32 v102, 16, v108
	v_and_b32_e32 v103, 0xffff0000, v108
	v_pk_fma_f32 v[0:1], v[44:45], v[102:103], v[0:1]
	v_lshlrev_b32_e32 v108, 16, v109
	v_and_b32_e32 v109, 0xffff0000, v109
	v_pk_fma_f32 v[0:1], v[46:47], v[108:109], v[0:1]
	s_waitcnt lgkmcnt(0)
	v_lshlrev_b32_e32 v110, 16, v112
	v_and_b32_e32 v111, 0xffff0000, v112
	v_pk_fma_f32 v[0:1], v[48:49], v[110:111], v[0:1]
	v_lshlrev_b32_e32 v112, 16, v113
	v_and_b32_e32 v113, 0xffff0000, v113
	v_pk_fma_f32 v[0:1], v[50:51], v[112:113], v[0:1]
	ds_read2st64_b32 v[120:121], v136 offset0:192 offset1:200
	ds_read2st64_b32 v[124:125], v136 offset0:208 offset1:216
	ds_read2st64_b32 v[128:129], v136 offset0:224 offset1:232
	ds_read2st64_b32 v[132:133], v136 offset0:240 offset1:248
	s_waitcnt lgkmcnt(3)
	v_lshlrev_b32_e32 v118, 16, v120
	v_and_b32_e32 v119, 0xffff0000, v120
	v_lshlrev_b32_e32 v120, 16, v121
	v_and_b32_e32 v121, 0xffff0000, v121
	v_pk_fma_f32 v[0:1], v[52:53], v[118:119], v[0:1]
	s_waitcnt lgkmcnt(2)
	v_lshlrev_b32_e32 v122, 16, v124
	v_pk_fma_f32 v[0:1], v[54:55], v[120:121], v[0:1]
	v_and_b32_e32 v123, 0xffff0000, v124
	v_pk_fma_f32 v[0:1], v[56:57], v[122:123], v[0:1]
	v_lshlrev_b32_e32 v124, 16, v125
	v_and_b32_e32 v125, 0xffff0000, v125
	v_pk_fma_f32 v[0:1], v[58:59], v[124:125], v[0:1]
	s_waitcnt lgkmcnt(1)
	v_lshlrev_b32_e32 v126, 16, v128
	v_and_b32_e32 v127, 0xffff0000, v128
	v_pk_fma_f32 v[0:1], v[60:61], v[126:127], v[0:1]
	v_lshlrev_b32_e32 v128, 16, v129
	v_and_b32_e32 v129, 0xffff0000, v129
	v_pk_fma_f32 v[0:1], v[62:63], v[128:129], v[0:1]
	s_waitcnt lgkmcnt(0)
	v_lshlrev_b32_e32 v130, 16, v132
	v_and_b32_e32 v131, 0xffff0000, v132
	v_pk_fma_f32 v[0:1], v[64:65], v[130:131], v[0:1]
	v_add_u32_e32 v132, 0x10000, v136
	v_add_u32_e32 v134, 0x10800, v136
	v_add_u32_e32 v135, 0x11000, v136
	v_add_u32_e32 v137, 0x11800, v136
	v_add_u32_e32 v139, 0x12000, v136
	v_add_u32_e32 v141, 0x12800, v136
	v_add_u32_e32 v143, 0x13000, v136
	v_add_u32_e32 v145, 0x13800, v136
	ds_read_b32 v138, v132
	ds_read_b32 v140, v134
	ds_read_b32 v142, v135
	ds_read_b32 v144, v137
	ds_read_b32 v146, v139
	ds_read_b32 v148, v141
	ds_read_b32 v150, v143
	ds_read_b32 v152, v145
	v_pk_mul_f32 v[134:135], v[0:1], v[0:1]
	v_add_f32_e32 v132, v0, v1
	v_add_f32_e32 v134, v134, v135
	s_nop 1
	v_mov_b32_dpp v137, v132 quad_perm:[1,0,3,2] row_mask:0xf bank_mask:0xf
	s_nop 1
	v_mov_b32_dpp v135, v134 quad_perm:[1,0,3,2] row_mask:0xf bank_mask:0xf
	v_add_u32_e32 v139, 0x14000, v136
	v_add_u32_e32 v141, 0x14800, v136
	v_add_u32_e32 v143, 0x15000, v136
	s_waitcnt lgkmcnt(0)
	v_add_f32_e32 v132, v132, v137
	s_waitcnt lgkmcnt(0)
	v_add_f32_e32 v134, v134, v135
	s_nop 1
	v_mov_b32_dpp v137, v132 quad_perm:[2,3,0,1] row_mask:0xf bank_mask:0xf
	s_nop 1
	v_mov_b32_dpp v135, v134 quad_perm:[2,3,0,1] row_mask:0xf bank_mask:0xf
	v_add_u32_e32 v145, 0x15800, v136
	v_add_u32_e32 v147, 0x16000, v136
	v_add_u32_e32 v136, 0x16800, v136
	s_waitcnt lgkmcnt(0)
	v_add_f32_e32 v132, v132, v137
	s_waitcnt lgkmcnt(0)
	v_add_f32_e32 v134, v134, v135
	s_nop 1
	v_mov_b32_dpp v137, v132 row_half_mirror row_mask:0xf bank_mask:0xf
	s_nop 1
	v_mov_b32_dpp v137, v137 quad_perm:[3,2,1,0] row_mask:0xf bank_mask:0xf
	s_nop 1
	v_mov_b32_dpp v135, v134 row_half_mirror row_mask:0xf bank_mask:0xf
	s_nop 1
	v_mov_b32_dpp v135, v135 quad_perm:[3,2,1,0] row_mask:0xf bank_mask:0xf
	ds_read_b32 v154, v139
	ds_read_b32 v156, v141
	ds_read_b32 v158, v143
	ds_read_b32 v160, v145
	ds_read_b32 v162, v147
	ds_read_b32 v168, v136
	s_waitcnt lgkmcnt(6)
	v_add_f32_e32 v132, v132, v137
	s_waitcnt lgkmcnt(6)
	v_add_f32_e32 v134, v134, v135
	s_nop 1
	v_mov_b32_dpp v137, v132 row_ror:8 row_mask:0xf bank_mask:0xf
	s_nop 1
	v_mov_b32_dpp v135, v134 row_ror:8 row_mask:0xf bank_mask:0xf
	s_waitcnt lgkmcnt(0)
	v_add_f32_e32 v132, v132, v137
	s_waitcnt lgkmcnt(0)
	v_add_f32_e32 v135, v134, v135
	ds_swizzle_b32 v137, v132 offset:swizzle(SWAP,16)
	ds_swizzle_b32 v139, v135 offset:swizzle(SWAP,16)
	s_waitcnt lgkmcnt(1)
	v_add_f32_e32 v134, v132, v137
	s_waitcnt lgkmcnt(0)
	v_add_f32_e32 v135, v135, v139
	v_mov_b32_e32 v136, v134
	v_mov_b32_e32 v137, v135
	s_nop 0
	v_permlane32_swap_b32_e32 v134, v136
	v_permlane32_swap_b32_e32 v135, v137
	s_and_saveexec_b64 s[12:13], s[6:7]
	s_add_i32 s19, s14, s64
	v_pk_add_f32 v[134:135], v[134:135], v[136:137]
	v_mov_b32_e32 v132, s19
	ds_write2_b32 v132, v134, v135 offset1:1
	s_or_b64 exec, exec, s[12:13]
	v_pk_fma_f32 v[104:105], v[4:5], v[104:105], v[66:67]
	v_lshlrev_b32_e32 v132, 16, v133
	v_pk_fma_f32 v[104:105], v[6:7], v[74:75], v[104:105]
	v_and_b32_e32 v133, 0xffff0000, v133
	v_pk_fma_f32 v[104:105], v[8:9], v[98:99], v[104:105]
	s_nop 0
	v_pk_fma_f32 v[104:105], v[10:11], v[2:3], v[104:105]
	s_nop 0
	v_pk_fma_f32 v[104:105], v[12:13], v[94:95], v[104:105]
	s_nop 0
	v_pk_fma_f32 v[104:105], v[14:15], v[76:77], v[104:105]
	s_nop 0
	v_pk_fma_f32 v[104:105], v[16:17], v[100:101], v[104:105]
	s_nop 0
	v_pk_fma_f32 v[104:105], v[18:19], v[78:79], v[104:105]
	s_nop 0
	v_pk_fma_f32 v[104:105], v[20:21], v[106:107], v[104:105]
	s_nop 0
	v_pk_fma_f32 v[104:105], v[22:23], v[80:81], v[104:105]
	s_nop 0
	v_pk_fma_f32 v[104:105], v[24:25], v[114:115], v[104:105]
	s_nop 0
	v_pk_fma_f32 v[104:105], v[26:27], v[82:83], v[104:105]
	s_nop 0
	v_pk_fma_f32 v[104:105], v[28:29], v[116:117], v[104:105]
	s_nop 0
	v_pk_fma_f32 v[104:105], v[30:31], v[84:85], v[104:105]
	s_nop 0
	v_pk_fma_f32 v[104:105], v[32:33], v[86:87], v[104:105]
	s_nop 0
	v_pk_fma_f32 v[104:105], v[34:35], v[88:89], v[104:105]
	s_nop 0
	v_pk_fma_f32 v[104:105], v[36:37], v[90:91], v[104:105]
	s_nop 0
	v_pk_fma_f32 v[104:105], v[38:39], v[92:93], v[104:105]
	s_nop 0
	v_pk_fma_f32 v[104:105], v[40:41], v[96:97], v[104:105]
	s_nop 0
	v_pk_fma_f32 v[104:105], v[42:43], v[102:103], v[104:105]
	s_nop 0
	v_pk_fma_f32 v[104:105], v[44:45], v[108:109], v[104:105]
	s_nop 0
	v_pk_fma_f32 v[104:105], v[46:47], v[110:111], v[104:105]
	s_nop 0
	v_pk_fma_f32 v[104:105], v[48:49], v[112:113], v[104:105]
	s_nop 0
	v_pk_fma_f32 v[104:105], v[50:51], v[118:119], v[104:105]
	s_nop 0
	v_pk_fma_f32 v[104:105], v[52:53], v[120:121], v[104:105]
	s_nop 0
	v_pk_fma_f32 v[104:105], v[54:55], v[122:123], v[104:105]
	s_nop 0
	v_pk_fma_f32 v[104:105], v[56:57], v[124:125], v[104:105]
	s_nop 0
	v_pk_fma_f32 v[104:105], v[58:59], v[126:127], v[104:105]
	s_nop 0
	v_pk_fma_f32 v[104:105], v[60:61], v[128:129], v[104:105]
	s_nop 0
	v_pk_fma_f32 v[104:105], v[62:63], v[130:131], v[104:105]
	s_nop 0
	v_pk_fma_f32 v[104:105], v[64:65], v[132:133], v[104:105]
	s_nop 0
	v_pk_mul_f32 v[134:135], v[104:105], v[104:105]
	v_add_f32_e32 v136, v104, v105
	v_add_f32_e32 v134, v134, v135
	s_nop 1
	v_mov_b32_dpp v137, v136 quad_perm:[1,0,3,2] row_mask:0xf bank_mask:0xf
	s_nop 1
	v_mov_b32_dpp v135, v134 quad_perm:[1,0,3,2] row_mask:0xf bank_mask:0xf
	s_waitcnt lgkmcnt(0)
	v_add_f32_e32 v136, v136, v137
	s_waitcnt lgkmcnt(0)
	v_add_f32_e32 v134, v134, v135
	s_nop 1
	v_mov_b32_dpp v137, v136 quad_perm:[2,3,0,1] row_mask:0xf bank_mask:0xf
	s_nop 1
	v_mov_b32_dpp v135, v134 quad_perm:[2,3,0,1] row_mask:0xf bank_mask:0xf
	s_waitcnt lgkmcnt(0)
	v_add_f32_e32 v136, v136, v137
	s_waitcnt lgkmcnt(0)
	v_add_f32_e32 v134, v134, v135
	s_nop 1
	v_mov_b32_dpp v137, v136 row_half_mirror row_mask:0xf bank_mask:0xf
	s_nop 1
	v_mov_b32_dpp v137, v137 quad_perm:[3,2,1,0] row_mask:0xf bank_mask:0xf
	s_nop 1
	v_mov_b32_dpp v135, v134 row_half_mirror row_mask:0xf bank_mask:0xf
	s_nop 1
	v_mov_b32_dpp v135, v135 quad_perm:[3,2,1,0] row_mask:0xf bank_mask:0xf
	s_waitcnt lgkmcnt(0)
	v_add_f32_e32 v136, v136, v137
	s_waitcnt lgkmcnt(0)
	v_add_f32_e32 v134, v134, v135
	s_nop 1
	v_mov_b32_dpp v137, v136 row_ror:8 row_mask:0xf bank_mask:0xf
	s_nop 1
	v_mov_b32_dpp v135, v134 row_ror:8 row_mask:0xf bank_mask:0xf
	s_waitcnt lgkmcnt(0)
	v_add_f32_e32 v136, v136, v137
	s_waitcnt lgkmcnt(0)
	v_add_f32_e32 v135, v134, v135
	ds_swizzle_b32 v137, v136 offset:swizzle(SWAP,16)
	ds_swizzle_b32 v139, v135 offset:swizzle(SWAP,16)
	s_waitcnt lgkmcnt(1)
	v_add_f32_e32 v134, v136, v137
	s_waitcnt lgkmcnt(0)
	v_add_f32_e32 v135, v135, v139
	v_mov_b32_e32 v136, v134
	v_mov_b32_e32 v137, v135
	s_nop 0
	v_permlane32_swap_b32_e32 v134, v136
	v_permlane32_swap_b32_e32 v135, v137
	s_and_saveexec_b64 s[12:13], s[6:7]
	s_add_i32 s19, s14, s64
	v_pk_add_f32 v[134:135], v[134:135], v[136:137]
	v_mov_b32_e32 v136, s19
	ds_write2_b32 v136, v134, v135 offset0:2 offset1:3
	s_or_b64 exec, exec, s[12:13]
	v_pk_fma_f32 v[74:75], v[4:5], v[74:75], v[66:67]
	v_lshlrev_b32_e32 v134, 16, v138
	v_pk_fma_f32 v[74:75], v[6:7], v[98:99], v[74:75]
	v_and_b32_e32 v135, 0xffff0000, v138
	v_pk_fma_f32 v[74:75], v[8:9], v[2:3], v[74:75]
	s_nop 0
	v_pk_fma_f32 v[74:75], v[10:11], v[94:95], v[74:75]
	s_nop 0
	v_pk_fma_f32 v[74:75], v[12:13], v[76:77], v[74:75]
	s_nop 0
	v_pk_fma_f32 v[74:75], v[14:15], v[100:101], v[74:75]
	s_nop 0
	v_pk_fma_f32 v[74:75], v[16:17], v[78:79], v[74:75]
	s_nop 0
	v_pk_fma_f32 v[74:75], v[18:19], v[106:107], v[74:75]
	s_nop 0
	v_pk_fma_f32 v[74:75], v[20:21], v[80:81], v[74:75]
	s_nop 0
	v_pk_fma_f32 v[74:75], v[22:23], v[114:115], v[74:75]
	s_nop 0
	v_pk_fma_f32 v[74:75], v[24:25], v[82:83], v[74:75]
	s_nop 0
	v_pk_fma_f32 v[74:75], v[26:27], v[116:117], v[74:75]
	s_nop 0
	v_pk_fma_f32 v[74:75], v[28:29], v[84:85], v[74:75]
	s_nop 0
	v_pk_fma_f32 v[74:75], v[30:31], v[86:87], v[74:75]
	s_nop 0
	v_pk_fma_f32 v[74:75], v[32:33], v[88:89], v[74:75]
	s_nop 0
	v_pk_fma_f32 v[74:75], v[34:35], v[90:91], v[74:75]
	s_nop 0
	v_pk_fma_f32 v[74:75], v[36:37], v[92:93], v[74:75]
	s_nop 0
	v_pk_fma_f32 v[74:75], v[38:39], v[96:97], v[74:75]
	s_nop 0
	v_pk_fma_f32 v[74:75], v[40:41], v[102:103], v[74:75]
	s_nop 0
	v_pk_fma_f32 v[74:75], v[42:43], v[108:109], v[74:75]
	s_nop 0
	v_pk_fma_f32 v[74:75], v[44:45], v[110:111], v[74:75]
	s_nop 0
	v_pk_fma_f32 v[74:75], v[46:47], v[112:113], v[74:75]
	s_nop 0
	v_pk_fma_f32 v[74:75], v[48:49], v[118:119], v[74:75]
	s_nop 0
	v_pk_fma_f32 v[74:75], v[50:51], v[120:121], v[74:75]
	s_nop 0
	v_pk_fma_f32 v[74:75], v[52:53], v[122:123], v[74:75]
	s_nop 0
	v_pk_fma_f32 v[74:75], v[54:55], v[124:125], v[74:75]
	s_nop 0
	v_pk_fma_f32 v[74:75], v[56:57], v[126:127], v[74:75]
	s_nop 0
	v_pk_fma_f32 v[74:75], v[58:59], v[128:129], v[74:75]
	s_nop 0
	v_pk_fma_f32 v[74:75], v[60:61], v[130:131], v[74:75]
	s_nop 0
	v_pk_fma_f32 v[74:75], v[62:63], v[132:133], v[74:75]
	s_nop 0
	v_pk_fma_f32 v[74:75], v[64:65], v[134:135], v[74:75]
	s_nop 0
	v_pk_mul_f32 v[136:137], v[74:75], v[74:75]
	v_add_f32_e32 v138, v74, v75
	v_add_f32_e32 v136, v136, v137
	s_nop 1
	v_mov_b32_dpp v139, v138 quad_perm:[1,0,3,2] row_mask:0xf bank_mask:0xf
	s_nop 1
	v_mov_b32_dpp v137, v136 quad_perm:[1,0,3,2] row_mask:0xf bank_mask:0xf
	s_waitcnt lgkmcnt(0)
	v_add_f32_e32 v138, v138, v139
	s_waitcnt lgkmcnt(0)
	v_add_f32_e32 v136, v136, v137
	s_nop 1
	v_mov_b32_dpp v139, v138 quad_perm:[2,3,0,1] row_mask:0xf bank_mask:0xf
	s_nop 1
	v_mov_b32_dpp v137, v136 quad_perm:[2,3,0,1] row_mask:0xf bank_mask:0xf
	s_waitcnt lgkmcnt(0)
	v_add_f32_e32 v138, v138, v139
	s_waitcnt lgkmcnt(0)
	v_add_f32_e32 v136, v136, v137
	s_nop 1
	v_mov_b32_dpp v139, v138 row_half_mirror row_mask:0xf bank_mask:0xf
	s_nop 1
	v_mov_b32_dpp v139, v139 quad_perm:[3,2,1,0] row_mask:0xf bank_mask:0xf
	s_nop 1
	v_mov_b32_dpp v137, v136 row_half_mirror row_mask:0xf bank_mask:0xf
	s_nop 1
	v_mov_b32_dpp v137, v137 quad_perm:[3,2,1,0] row_mask:0xf bank_mask:0xf
	s_waitcnt lgkmcnt(0)
	v_add_f32_e32 v138, v138, v139
	s_waitcnt lgkmcnt(0)
	v_add_f32_e32 v136, v136, v137
	s_nop 1
	v_mov_b32_dpp v139, v138 row_ror:8 row_mask:0xf bank_mask:0xf
	s_nop 1
	v_mov_b32_dpp v137, v136 row_ror:8 row_mask:0xf bank_mask:0xf
	s_waitcnt lgkmcnt(0)
	v_add_f32_e32 v138, v138, v139
	s_waitcnt lgkmcnt(0)
	v_add_f32_e32 v137, v136, v137
	ds_swizzle_b32 v139, v138 offset:swizzle(SWAP,16)
	ds_swizzle_b32 v141, v137 offset:swizzle(SWAP,16)
	s_waitcnt lgkmcnt(1)
	v_add_f32_e32 v136, v138, v139
	s_waitcnt lgkmcnt(0)
	v_add_f32_e32 v137, v137, v141
	v_mov_b32_e32 v138, v136
	v_mov_b32_e32 v139, v137
	s_nop 0
	v_permlane32_swap_b32_e32 v136, v138
	v_permlane32_swap_b32_e32 v137, v139
	s_and_saveexec_b64 s[12:13], s[6:7]
	s_add_i32 s19, s14, s64
	v_pk_add_f32 v[136:137], v[136:137], v[138:139]
	v_mov_b32_e32 v138, s19
	ds_write2_b32 v138, v136, v137 offset0:4 offset1:5
	s_or_b64 exec, exec, s[12:13]
	v_pk_fma_f32 v[98:99], v[4:5], v[98:99], v[66:67]
	v_lshlrev_b32_e32 v136, 16, v140
	v_pk_fma_f32 v[98:99], v[6:7], v[2:3], v[98:99]
	v_and_b32_e32 v137, 0xffff0000, v140
	v_pk_fma_f32 v[98:99], v[8:9], v[94:95], v[98:99]
	s_nop 0
	v_pk_fma_f32 v[98:99], v[10:11], v[76:77], v[98:99]
	s_nop 0
	v_pk_fma_f32 v[98:99], v[12:13], v[100:101], v[98:99]
	s_nop 0
	v_pk_fma_f32 v[98:99], v[14:15], v[78:79], v[98:99]
	s_nop 0
	v_pk_fma_f32 v[98:99], v[16:17], v[106:107], v[98:99]
	s_nop 0
	v_pk_fma_f32 v[98:99], v[18:19], v[80:81], v[98:99]
	s_nop 0
	v_pk_fma_f32 v[98:99], v[20:21], v[114:115], v[98:99]
	s_nop 0
	v_pk_fma_f32 v[98:99], v[22:23], v[82:83], v[98:99]
	s_nop 0
	v_pk_fma_f32 v[98:99], v[24:25], v[116:117], v[98:99]
	s_nop 0
	v_pk_fma_f32 v[98:99], v[26:27], v[84:85], v[98:99]
	s_nop 0
	v_pk_fma_f32 v[98:99], v[28:29], v[86:87], v[98:99]
	s_nop 0
	v_pk_fma_f32 v[98:99], v[30:31], v[88:89], v[98:99]
	s_nop 0
	v_pk_fma_f32 v[98:99], v[32:33], v[90:91], v[98:99]
	s_nop 0
	v_pk_fma_f32 v[98:99], v[34:35], v[92:93], v[98:99]
	s_nop 0
	v_pk_fma_f32 v[98:99], v[36:37], v[96:97], v[98:99]
	s_nop 0
	v_pk_fma_f32 v[98:99], v[38:39], v[102:103], v[98:99]
	s_nop 0
	v_pk_fma_f32 v[98:99], v[40:41], v[108:109], v[98:99]
	s_nop 0
	v_pk_fma_f32 v[98:99], v[42:43], v[110:111], v[98:99]
	s_nop 0
	v_pk_fma_f32 v[98:99], v[44:45], v[112:113], v[98:99]
	s_nop 0
	v_pk_fma_f32 v[98:99], v[46:47], v[118:119], v[98:99]
	s_nop 0
	v_pk_fma_f32 v[98:99], v[48:49], v[120:121], v[98:99]
	s_nop 0
	v_pk_fma_f32 v[98:99], v[50:51], v[122:123], v[98:99]
	s_nop 0
	v_pk_fma_f32 v[98:99], v[52:53], v[124:125], v[98:99]
	s_nop 0
	v_pk_fma_f32 v[98:99], v[54:55], v[126:127], v[98:99]
	s_nop 0
	v_pk_fma_f32 v[98:99], v[56:57], v[128:129], v[98:99]
	s_nop 0
	v_pk_fma_f32 v[98:99], v[58:59], v[130:131], v[98:99]
	s_nop 0
	v_pk_fma_f32 v[98:99], v[60:61], v[132:133], v[98:99]
	s_nop 0
	v_pk_fma_f32 v[98:99], v[62:63], v[134:135], v[98:99]
	s_nop 0
	v_pk_fma_f32 v[98:99], v[64:65], v[136:137], v[98:99]
	s_nop 0
	v_pk_mul_f32 v[138:139], v[98:99], v[98:99]
	v_add_f32_e32 v140, v98, v99
	v_add_f32_e32 v138, v138, v139
	s_nop 1
	v_mov_b32_dpp v141, v140 quad_perm:[1,0,3,2] row_mask:0xf bank_mask:0xf
	s_nop 1
	v_mov_b32_dpp v139, v138 quad_perm:[1,0,3,2] row_mask:0xf bank_mask:0xf
	s_waitcnt lgkmcnt(0)
	v_add_f32_e32 v140, v140, v141
	s_waitcnt lgkmcnt(0)
	v_add_f32_e32 v138, v138, v139
	s_nop 1
	v_mov_b32_dpp v141, v140 quad_perm:[2,3,0,1] row_mask:0xf bank_mask:0xf
	s_nop 1
	v_mov_b32_dpp v139, v138 quad_perm:[2,3,0,1] row_mask:0xf bank_mask:0xf
	s_waitcnt lgkmcnt(0)
	v_add_f32_e32 v140, v140, v141
	s_waitcnt lgkmcnt(0)
	v_add_f32_e32 v138, v138, v139
	s_nop 1
	v_mov_b32_dpp v141, v140 row_half_mirror row_mask:0xf bank_mask:0xf
	s_nop 1
	v_mov_b32_dpp v141, v141 quad_perm:[3,2,1,0] row_mask:0xf bank_mask:0xf
	s_nop 1
	v_mov_b32_dpp v139, v138 row_half_mirror row_mask:0xf bank_mask:0xf
	s_nop 1
	v_mov_b32_dpp v139, v139 quad_perm:[3,2,1,0] row_mask:0xf bank_mask:0xf
	s_waitcnt lgkmcnt(0)
	v_add_f32_e32 v140, v140, v141
	s_waitcnt lgkmcnt(0)
	v_add_f32_e32 v138, v138, v139
	s_nop 1
	v_mov_b32_dpp v141, v140 row_ror:8 row_mask:0xf bank_mask:0xf
	s_nop 1
	v_mov_b32_dpp v139, v138 row_ror:8 row_mask:0xf bank_mask:0xf
	s_waitcnt lgkmcnt(0)
	v_add_f32_e32 v140, v140, v141
	s_waitcnt lgkmcnt(0)
	v_add_f32_e32 v139, v138, v139
	ds_swizzle_b32 v141, v140 offset:swizzle(SWAP,16)
	ds_swizzle_b32 v143, v139 offset:swizzle(SWAP,16)
	s_waitcnt lgkmcnt(1)
	v_add_f32_e32 v138, v140, v141
	s_waitcnt lgkmcnt(0)
	v_add_f32_e32 v139, v139, v143
	v_mov_b32_e32 v140, v138
	v_mov_b32_e32 v141, v139
	s_nop 0
	v_permlane32_swap_b32_e32 v138, v140
	v_permlane32_swap_b32_e32 v139, v141
	s_and_saveexec_b64 s[12:13], s[6:7]
	s_add_i32 s19, s14, s64
	v_pk_add_f32 v[138:139], v[138:139], v[140:141]
	v_mov_b32_e32 v140, s19
	ds_write2_b32 v140, v138, v139 offset0:6 offset1:7
	s_or_b64 exec, exec, s[12:13]
	v_pk_fma_f32 v[2:3], v[4:5], v[2:3], v[66:67]
	v_lshlrev_b32_e32 v138, 16, v142
	v_pk_fma_f32 v[2:3], v[6:7], v[94:95], v[2:3]
	v_and_b32_e32 v139, 0xffff0000, v142
	v_pk_fma_f32 v[2:3], v[8:9], v[76:77], v[2:3]
	s_nop 0
	v_pk_fma_f32 v[2:3], v[10:11], v[100:101], v[2:3]
	s_nop 0
	v_pk_fma_f32 v[2:3], v[12:13], v[78:79], v[2:3]
	s_nop 0
	v_pk_fma_f32 v[2:3], v[14:15], v[106:107], v[2:3]
	s_nop 0
	v_pk_fma_f32 v[2:3], v[16:17], v[80:81], v[2:3]
	s_nop 0
	v_pk_fma_f32 v[2:3], v[18:19], v[114:115], v[2:3]
	s_nop 0
	v_pk_fma_f32 v[2:3], v[20:21], v[82:83], v[2:3]
	s_nop 0
	v_pk_fma_f32 v[2:3], v[22:23], v[116:117], v[2:3]
	s_nop 0
	v_pk_fma_f32 v[2:3], v[24:25], v[84:85], v[2:3]
	s_nop 0
	v_pk_fma_f32 v[2:3], v[26:27], v[86:87], v[2:3]
	s_nop 0
	v_pk_fma_f32 v[2:3], v[28:29], v[88:89], v[2:3]
	s_nop 0
	v_pk_fma_f32 v[2:3], v[30:31], v[90:91], v[2:3]
	s_nop 0
	v_pk_fma_f32 v[2:3], v[32:33], v[92:93], v[2:3]
	s_nop 0
	v_pk_fma_f32 v[2:3], v[34:35], v[96:97], v[2:3]
	s_nop 0
	v_pk_fma_f32 v[2:3], v[36:37], v[102:103], v[2:3]
	s_nop 0
	v_pk_fma_f32 v[2:3], v[38:39], v[108:109], v[2:3]
	s_nop 0
	v_pk_fma_f32 v[2:3], v[40:41], v[110:111], v[2:3]
	s_nop 0
	v_pk_fma_f32 v[2:3], v[42:43], v[112:113], v[2:3]
	s_nop 0
	v_pk_fma_f32 v[2:3], v[44:45], v[118:119], v[2:3]
	s_nop 0
	v_pk_fma_f32 v[2:3], v[46:47], v[120:121], v[2:3]
	s_nop 0
	v_pk_fma_f32 v[2:3], v[48:49], v[122:123], v[2:3]
	s_nop 0
	v_pk_fma_f32 v[2:3], v[50:51], v[124:125], v[2:3]
	s_nop 0
	v_pk_fma_f32 v[2:3], v[52:53], v[126:127], v[2:3]
	s_nop 0
	v_pk_fma_f32 v[2:3], v[54:55], v[128:129], v[2:3]
	s_nop 0
	v_pk_fma_f32 v[2:3], v[56:57], v[130:131], v[2:3]
	s_nop 0
	v_pk_fma_f32 v[2:3], v[58:59], v[132:133], v[2:3]
	s_nop 0
	v_pk_fma_f32 v[2:3], v[60:61], v[134:135], v[2:3]
	s_nop 0
	v_pk_fma_f32 v[2:3], v[62:63], v[136:137], v[2:3]
	s_nop 0
	v_pk_fma_f32 v[2:3], v[64:65], v[138:139], v[2:3]
	s_nop 0
	v_pk_mul_f32 v[140:141], v[2:3], v[2:3]
	v_add_f32_e32 v142, v2, v3
	v_add_f32_e32 v140, v140, v141
	s_nop 1
	v_mov_b32_dpp v143, v142 quad_perm:[1,0,3,2] row_mask:0xf bank_mask:0xf
	s_nop 1
	v_mov_b32_dpp v141, v140 quad_perm:[1,0,3,2] row_mask:0xf bank_mask:0xf
	s_waitcnt lgkmcnt(0)
	v_add_f32_e32 v142, v142, v143
	s_waitcnt lgkmcnt(0)
	v_add_f32_e32 v140, v140, v141
	s_nop 1
	v_mov_b32_dpp v143, v142 quad_perm:[2,3,0,1] row_mask:0xf bank_mask:0xf
	s_nop 1
	v_mov_b32_dpp v141, v140 quad_perm:[2,3,0,1] row_mask:0xf bank_mask:0xf
	s_waitcnt lgkmcnt(0)
	v_add_f32_e32 v142, v142, v143
	s_waitcnt lgkmcnt(0)
	v_add_f32_e32 v140, v140, v141
	s_nop 1
	v_mov_b32_dpp v143, v142 row_half_mirror row_mask:0xf bank_mask:0xf
	s_nop 1
	v_mov_b32_dpp v143, v143 quad_perm:[3,2,1,0] row_mask:0xf bank_mask:0xf
	s_nop 1
	v_mov_b32_dpp v141, v140 row_half_mirror row_mask:0xf bank_mask:0xf
	s_nop 1
	v_mov_b32_dpp v141, v141 quad_perm:[3,2,1,0] row_mask:0xf bank_mask:0xf
	s_waitcnt lgkmcnt(0)
	v_add_f32_e32 v142, v142, v143
	s_waitcnt lgkmcnt(0)
	v_add_f32_e32 v140, v140, v141
	s_nop 1
	v_mov_b32_dpp v143, v142 row_ror:8 row_mask:0xf bank_mask:0xf
	s_nop 1
	v_mov_b32_dpp v141, v140 row_ror:8 row_mask:0xf bank_mask:0xf
	s_waitcnt lgkmcnt(0)
	v_add_f32_e32 v142, v142, v143
	s_waitcnt lgkmcnt(0)
	v_add_f32_e32 v141, v140, v141
	ds_swizzle_b32 v143, v142 offset:swizzle(SWAP,16)
	ds_swizzle_b32 v145, v141 offset:swizzle(SWAP,16)
	s_waitcnt lgkmcnt(1)
	v_add_f32_e32 v140, v142, v143
	s_waitcnt lgkmcnt(0)
	v_add_f32_e32 v141, v141, v145
	v_mov_b32_e32 v142, v140
	v_mov_b32_e32 v143, v141
	s_nop 0
	v_permlane32_swap_b32_e32 v140, v142
	v_permlane32_swap_b32_e32 v141, v143
	s_and_saveexec_b64 s[12:13], s[6:7]
	s_add_i32 s19, s14, s64
	v_pk_add_f32 v[140:141], v[140:141], v[142:143]
	v_mov_b32_e32 v142, s19
	ds_write2_b32 v142, v140, v141 offset0:8 offset1:9
	s_or_b64 exec, exec, s[12:13]
	v_pk_fma_f32 v[94:95], v[4:5], v[94:95], v[66:67]
	v_lshlrev_b32_e32 v140, 16, v144
	v_pk_fma_f32 v[94:95], v[6:7], v[76:77], v[94:95]
	v_and_b32_e32 v141, 0xffff0000, v144
	v_pk_fma_f32 v[94:95], v[8:9], v[100:101], v[94:95]
	s_nop 0
	v_pk_fma_f32 v[94:95], v[10:11], v[78:79], v[94:95]
	s_nop 0
	v_pk_fma_f32 v[94:95], v[12:13], v[106:107], v[94:95]
	s_nop 0
	v_pk_fma_f32 v[94:95], v[14:15], v[80:81], v[94:95]
	s_nop 0
	v_pk_fma_f32 v[94:95], v[16:17], v[114:115], v[94:95]
	s_nop 0
	v_pk_fma_f32 v[94:95], v[18:19], v[82:83], v[94:95]
	s_nop 0
	v_pk_fma_f32 v[94:95], v[20:21], v[116:117], v[94:95]
	s_nop 0
	v_pk_fma_f32 v[94:95], v[22:23], v[84:85], v[94:95]
	s_nop 0
	v_pk_fma_f32 v[94:95], v[24:25], v[86:87], v[94:95]
	s_nop 0
	v_pk_fma_f32 v[94:95], v[26:27], v[88:89], v[94:95]
	s_nop 0
	v_pk_fma_f32 v[94:95], v[28:29], v[90:91], v[94:95]
	s_nop 0
	v_pk_fma_f32 v[94:95], v[30:31], v[92:93], v[94:95]
	s_nop 0
	v_pk_fma_f32 v[94:95], v[32:33], v[96:97], v[94:95]
	s_nop 0
	v_pk_fma_f32 v[94:95], v[34:35], v[102:103], v[94:95]
	s_nop 0
	v_pk_fma_f32 v[94:95], v[36:37], v[108:109], v[94:95]
	s_nop 0
	v_pk_fma_f32 v[94:95], v[38:39], v[110:111], v[94:95]
	s_nop 0
	v_pk_fma_f32 v[94:95], v[40:41], v[112:113], v[94:95]
	s_nop 0
	v_pk_fma_f32 v[94:95], v[42:43], v[118:119], v[94:95]
	s_nop 0
	v_pk_fma_f32 v[94:95], v[44:45], v[120:121], v[94:95]
	s_nop 0
	v_pk_fma_f32 v[94:95], v[46:47], v[122:123], v[94:95]
	s_nop 0
	v_pk_fma_f32 v[94:95], v[48:49], v[124:125], v[94:95]
	s_nop 0
	v_pk_fma_f32 v[94:95], v[50:51], v[126:127], v[94:95]
	s_nop 0
	v_pk_fma_f32 v[94:95], v[52:53], v[128:129], v[94:95]
	s_nop 0
	v_pk_fma_f32 v[94:95], v[54:55], v[130:131], v[94:95]
	s_nop 0
	v_pk_fma_f32 v[94:95], v[56:57], v[132:133], v[94:95]
	s_nop 0
	v_pk_fma_f32 v[94:95], v[58:59], v[134:135], v[94:95]
	s_nop 0
	v_pk_fma_f32 v[94:95], v[60:61], v[136:137], v[94:95]
	s_nop 0
	v_pk_fma_f32 v[94:95], v[62:63], v[138:139], v[94:95]
	s_nop 0
	v_pk_fma_f32 v[94:95], v[64:65], v[140:141], v[94:95]
	s_nop 0
	v_pk_mul_f32 v[142:143], v[94:95], v[94:95]
	v_add_f32_e32 v144, v94, v95
	v_add_f32_e32 v142, v142, v143
	s_nop 1
	v_mov_b32_dpp v145, v144 quad_perm:[1,0,3,2] row_mask:0xf bank_mask:0xf
	s_nop 1
	v_mov_b32_dpp v143, v142 quad_perm:[1,0,3,2] row_mask:0xf bank_mask:0xf
	s_waitcnt lgkmcnt(0)
	v_add_f32_e32 v144, v144, v145
	s_waitcnt lgkmcnt(0)
	v_add_f32_e32 v142, v142, v143
	s_nop 1
	v_mov_b32_dpp v145, v144 quad_perm:[2,3,0,1] row_mask:0xf bank_mask:0xf
	s_nop 1
	v_mov_b32_dpp v143, v142 quad_perm:[2,3,0,1] row_mask:0xf bank_mask:0xf
	s_waitcnt lgkmcnt(0)
	v_add_f32_e32 v144, v144, v145
	s_waitcnt lgkmcnt(0)
	v_add_f32_e32 v142, v142, v143
	s_nop 1
	v_mov_b32_dpp v145, v144 row_half_mirror row_mask:0xf bank_mask:0xf
	s_nop 1
	v_mov_b32_dpp v145, v145 quad_perm:[3,2,1,0] row_mask:0xf bank_mask:0xf
	s_nop 1
	v_mov_b32_dpp v143, v142 row_half_mirror row_mask:0xf bank_mask:0xf
	s_nop 1
	v_mov_b32_dpp v143, v143 quad_perm:[3,2,1,0] row_mask:0xf bank_mask:0xf
	s_waitcnt lgkmcnt(0)
	v_add_f32_e32 v144, v144, v145
	s_waitcnt lgkmcnt(0)
	v_add_f32_e32 v142, v142, v143
	s_nop 1
	v_mov_b32_dpp v145, v144 row_ror:8 row_mask:0xf bank_mask:0xf
	s_nop 1
	v_mov_b32_dpp v143, v142 row_ror:8 row_mask:0xf bank_mask:0xf
	s_waitcnt lgkmcnt(0)
	v_add_f32_e32 v144, v144, v145
	s_waitcnt lgkmcnt(0)
	v_add_f32_e32 v143, v142, v143
	ds_swizzle_b32 v145, v144 offset:swizzle(SWAP,16)
	ds_swizzle_b32 v147, v143 offset:swizzle(SWAP,16)
	s_waitcnt lgkmcnt(1)
	v_add_f32_e32 v142, v144, v145
	s_waitcnt lgkmcnt(0)
	v_add_f32_e32 v143, v143, v147
	v_mov_b32_e32 v144, v142
	v_mov_b32_e32 v145, v143
	s_nop 0
	v_permlane32_swap_b32_e32 v142, v144
	v_permlane32_swap_b32_e32 v143, v145
	s_and_saveexec_b64 s[12:13], s[6:7]
	s_add_i32 s19, s14, s64
	v_pk_add_f32 v[142:143], v[142:143], v[144:145]
	v_mov_b32_e32 v144, s19
	ds_write2_b32 v144, v142, v143 offset0:10 offset1:11
	s_or_b64 exec, exec, s[12:13]
	v_pk_fma_f32 v[76:77], v[4:5], v[76:77], v[66:67]
	v_lshlrev_b32_e32 v142, 16, v146
	v_pk_fma_f32 v[76:77], v[6:7], v[100:101], v[76:77]
	v_and_b32_e32 v143, 0xffff0000, v146
	v_pk_fma_f32 v[76:77], v[8:9], v[78:79], v[76:77]
	s_nop 0
	v_pk_fma_f32 v[76:77], v[10:11], v[106:107], v[76:77]
	s_nop 0
	v_pk_fma_f32 v[76:77], v[12:13], v[80:81], v[76:77]
	s_nop 0
	v_pk_fma_f32 v[76:77], v[14:15], v[114:115], v[76:77]
	s_nop 0
	v_pk_fma_f32 v[76:77], v[16:17], v[82:83], v[76:77]
	s_nop 0
	v_pk_fma_f32 v[76:77], v[18:19], v[116:117], v[76:77]
	s_nop 0
	v_pk_fma_f32 v[76:77], v[20:21], v[84:85], v[76:77]
	s_nop 0
	v_pk_fma_f32 v[76:77], v[22:23], v[86:87], v[76:77]
	s_nop 0
	v_pk_fma_f32 v[76:77], v[24:25], v[88:89], v[76:77]
	s_nop 0
	v_pk_fma_f32 v[76:77], v[26:27], v[90:91], v[76:77]
	s_nop 0
	v_pk_fma_f32 v[76:77], v[28:29], v[92:93], v[76:77]
	s_nop 0
	v_pk_fma_f32 v[76:77], v[30:31], v[96:97], v[76:77]
	s_nop 0
	v_pk_fma_f32 v[76:77], v[32:33], v[102:103], v[76:77]
	s_nop 0
	v_pk_fma_f32 v[76:77], v[34:35], v[108:109], v[76:77]
	s_nop 0
	v_pk_fma_f32 v[76:77], v[36:37], v[110:111], v[76:77]
	s_nop 0
	v_pk_fma_f32 v[76:77], v[38:39], v[112:113], v[76:77]
	s_nop 0
	v_pk_fma_f32 v[76:77], v[40:41], v[118:119], v[76:77]
	s_nop 0
	v_pk_fma_f32 v[76:77], v[42:43], v[120:121], v[76:77]
	s_nop 0
	v_pk_fma_f32 v[76:77], v[44:45], v[122:123], v[76:77]
	s_nop 0
	v_pk_fma_f32 v[76:77], v[46:47], v[124:125], v[76:77]
	s_nop 0
	v_pk_fma_f32 v[76:77], v[48:49], v[126:127], v[76:77]
	s_nop 0
	v_pk_fma_f32 v[76:77], v[50:51], v[128:129], v[76:77]
	s_nop 0
	v_pk_fma_f32 v[76:77], v[52:53], v[130:131], v[76:77]
	s_nop 0
	v_pk_fma_f32 v[76:77], v[54:55], v[132:133], v[76:77]
	s_nop 0
	v_pk_fma_f32 v[76:77], v[56:57], v[134:135], v[76:77]
	s_nop 0
	v_pk_fma_f32 v[76:77], v[58:59], v[136:137], v[76:77]
	s_nop 0
	v_pk_fma_f32 v[76:77], v[60:61], v[138:139], v[76:77]
	s_nop 0
	v_pk_fma_f32 v[76:77], v[62:63], v[140:141], v[76:77]
	s_nop 0
	v_pk_fma_f32 v[76:77], v[64:65], v[142:143], v[76:77]
	s_nop 0
	v_pk_mul_f32 v[144:145], v[76:77], v[76:77]
	v_add_f32_e32 v146, v76, v77
	v_add_f32_e32 v144, v144, v145
	s_nop 1
	v_mov_b32_dpp v147, v146 quad_perm:[1,0,3,2] row_mask:0xf bank_mask:0xf
	s_nop 1
	v_mov_b32_dpp v145, v144 quad_perm:[1,0,3,2] row_mask:0xf bank_mask:0xf
	s_waitcnt lgkmcnt(0)
	v_add_f32_e32 v146, v146, v147
	s_waitcnt lgkmcnt(0)
	v_add_f32_e32 v144, v144, v145
	s_nop 1
	v_mov_b32_dpp v147, v146 quad_perm:[2,3,0,1] row_mask:0xf bank_mask:0xf
	s_nop 1
	v_mov_b32_dpp v145, v144 quad_perm:[2,3,0,1] row_mask:0xf bank_mask:0xf
	s_waitcnt lgkmcnt(0)
	v_add_f32_e32 v146, v146, v147
	s_waitcnt lgkmcnt(0)
	v_add_f32_e32 v144, v144, v145
	s_nop 1
	v_mov_b32_dpp v147, v146 row_half_mirror row_mask:0xf bank_mask:0xf
	s_nop 1
	v_mov_b32_dpp v147, v147 quad_perm:[3,2,1,0] row_mask:0xf bank_mask:0xf
	s_nop 1
	v_mov_b32_dpp v145, v144 row_half_mirror row_mask:0xf bank_mask:0xf
	s_nop 1
	v_mov_b32_dpp v145, v145 quad_perm:[3,2,1,0] row_mask:0xf bank_mask:0xf
	s_waitcnt lgkmcnt(0)
	v_add_f32_e32 v146, v146, v147
	s_waitcnt lgkmcnt(0)
	v_add_f32_e32 v144, v144, v145
	s_nop 1
	v_mov_b32_dpp v147, v146 row_ror:8 row_mask:0xf bank_mask:0xf
	s_nop 1
	v_mov_b32_dpp v145, v144 row_ror:8 row_mask:0xf bank_mask:0xf
	s_waitcnt lgkmcnt(0)
	v_add_f32_e32 v146, v146, v147
	s_waitcnt lgkmcnt(0)
	v_add_f32_e32 v145, v144, v145
	ds_swizzle_b32 v147, v146 offset:swizzle(SWAP,16)
	ds_swizzle_b32 v149, v145 offset:swizzle(SWAP,16)
	s_waitcnt lgkmcnt(1)
	v_add_f32_e32 v144, v146, v147
	s_waitcnt lgkmcnt(0)
	v_add_f32_e32 v145, v145, v149
	v_mov_b32_e32 v146, v144
	v_mov_b32_e32 v147, v145
	s_nop 0
	v_permlane32_swap_b32_e32 v144, v146
	v_permlane32_swap_b32_e32 v145, v147
	s_and_saveexec_b64 s[12:13], s[6:7]
	s_add_i32 s19, s14, s64
	v_pk_add_f32 v[144:145], v[144:145], v[146:147]
	v_mov_b32_e32 v146, s19
	ds_write2_b32 v146, v144, v145 offset0:12 offset1:13
	s_or_b64 exec, exec, s[12:13]
	v_pk_fma_f32 v[100:101], v[4:5], v[100:101], v[66:67]
	v_lshlrev_b32_e32 v144, 16, v148
	v_pk_fma_f32 v[100:101], v[6:7], v[78:79], v[100:101]
	v_and_b32_e32 v145, 0xffff0000, v148
	v_pk_fma_f32 v[100:101], v[8:9], v[106:107], v[100:101]
	s_nop 0
	v_pk_fma_f32 v[100:101], v[10:11], v[80:81], v[100:101]
	s_nop 0
	v_pk_fma_f32 v[100:101], v[12:13], v[114:115], v[100:101]
	s_nop 0
	v_pk_fma_f32 v[100:101], v[14:15], v[82:83], v[100:101]
	s_nop 0
	v_pk_fma_f32 v[100:101], v[16:17], v[116:117], v[100:101]
	s_nop 0
	v_pk_fma_f32 v[100:101], v[18:19], v[84:85], v[100:101]
	s_nop 0
	v_pk_fma_f32 v[100:101], v[20:21], v[86:87], v[100:101]
	s_nop 0
	v_pk_fma_f32 v[100:101], v[22:23], v[88:89], v[100:101]
	s_nop 0
	v_pk_fma_f32 v[100:101], v[24:25], v[90:91], v[100:101]
	s_nop 0
	v_pk_fma_f32 v[100:101], v[26:27], v[92:93], v[100:101]
	s_nop 0
	v_pk_fma_f32 v[100:101], v[28:29], v[96:97], v[100:101]
	s_nop 0
	v_pk_fma_f32 v[100:101], v[30:31], v[102:103], v[100:101]
	s_nop 0
	v_pk_fma_f32 v[100:101], v[32:33], v[108:109], v[100:101]
	s_nop 0
	v_pk_fma_f32 v[100:101], v[34:35], v[110:111], v[100:101]
	s_nop 0
	v_pk_fma_f32 v[100:101], v[36:37], v[112:113], v[100:101]
	s_nop 0
	v_pk_fma_f32 v[100:101], v[38:39], v[118:119], v[100:101]
	s_nop 0
	v_pk_fma_f32 v[100:101], v[40:41], v[120:121], v[100:101]
	s_nop 0
	v_pk_fma_f32 v[100:101], v[42:43], v[122:123], v[100:101]
	s_nop 0
	v_pk_fma_f32 v[100:101], v[44:45], v[124:125], v[100:101]
	s_nop 0
	v_pk_fma_f32 v[100:101], v[46:47], v[126:127], v[100:101]
	s_nop 0
	v_pk_fma_f32 v[100:101], v[48:49], v[128:129], v[100:101]
	s_nop 0
	v_pk_fma_f32 v[100:101], v[50:51], v[130:131], v[100:101]
	s_nop 0
	v_pk_fma_f32 v[100:101], v[52:53], v[132:133], v[100:101]
	s_nop 0
	v_pk_fma_f32 v[100:101], v[54:55], v[134:135], v[100:101]
	s_nop 0
	v_pk_fma_f32 v[100:101], v[56:57], v[136:137], v[100:101]
	s_nop 0
	v_pk_fma_f32 v[100:101], v[58:59], v[138:139], v[100:101]
	s_nop 0
	v_pk_fma_f32 v[100:101], v[60:61], v[140:141], v[100:101]
	s_nop 0
	v_pk_fma_f32 v[100:101], v[62:63], v[142:143], v[100:101]
	s_nop 0
	v_pk_fma_f32 v[100:101], v[64:65], v[144:145], v[100:101]
	s_nop 0
	v_pk_mul_f32 v[146:147], v[100:101], v[100:101]
	v_add_f32_e32 v148, v100, v101
	v_add_f32_e32 v146, v146, v147
	s_nop 1
	v_mov_b32_dpp v149, v148 quad_perm:[1,0,3,2] row_mask:0xf bank_mask:0xf
	s_nop 1
	v_mov_b32_dpp v147, v146 quad_perm:[1,0,3,2] row_mask:0xf bank_mask:0xf
	s_waitcnt lgkmcnt(0)
	v_add_f32_e32 v148, v148, v149
	s_waitcnt lgkmcnt(0)
	v_add_f32_e32 v146, v146, v147
	s_nop 1
	v_mov_b32_dpp v149, v148 quad_perm:[2,3,0,1] row_mask:0xf bank_mask:0xf
	s_nop 1
	v_mov_b32_dpp v147, v146 quad_perm:[2,3,0,1] row_mask:0xf bank_mask:0xf
	s_waitcnt lgkmcnt(0)
	v_add_f32_e32 v148, v148, v149
	s_waitcnt lgkmcnt(0)
	v_add_f32_e32 v146, v146, v147
	s_nop 1
	v_mov_b32_dpp v149, v148 row_half_mirror row_mask:0xf bank_mask:0xf
	s_nop 1
	v_mov_b32_dpp v149, v149 quad_perm:[3,2,1,0] row_mask:0xf bank_mask:0xf
	s_nop 1
	v_mov_b32_dpp v147, v146 row_half_mirror row_mask:0xf bank_mask:0xf
	s_nop 1
	v_mov_b32_dpp v147, v147 quad_perm:[3,2,1,0] row_mask:0xf bank_mask:0xf
	s_waitcnt lgkmcnt(0)
	v_add_f32_e32 v148, v148, v149
	s_waitcnt lgkmcnt(0)
	v_add_f32_e32 v146, v146, v147
	s_nop 1
	v_mov_b32_dpp v149, v148 row_ror:8 row_mask:0xf bank_mask:0xf
	s_nop 1
	v_mov_b32_dpp v147, v146 row_ror:8 row_mask:0xf bank_mask:0xf
	s_waitcnt lgkmcnt(0)
	v_add_f32_e32 v148, v148, v149
	s_waitcnt lgkmcnt(0)
	v_add_f32_e32 v147, v146, v147
	ds_swizzle_b32 v149, v148 offset:swizzle(SWAP,16)
	ds_swizzle_b32 v151, v147 offset:swizzle(SWAP,16)
	s_waitcnt lgkmcnt(1)
	v_add_f32_e32 v146, v148, v149
	s_waitcnt lgkmcnt(0)
	v_add_f32_e32 v147, v147, v151
	v_mov_b32_e32 v148, v146
	v_mov_b32_e32 v149, v147
	s_nop 0
	v_permlane32_swap_b32_e32 v146, v148
	v_permlane32_swap_b32_e32 v147, v149
	s_and_saveexec_b64 s[12:13], s[6:7]
	s_add_i32 s19, s14, s64
	v_pk_add_f32 v[146:147], v[146:147], v[148:149]
	v_mov_b32_e32 v148, s19
	ds_write2_b32 v148, v146, v147 offset0:14 offset1:15
	s_or_b64 exec, exec, s[12:13]
	v_pk_fma_f32 v[78:79], v[4:5], v[78:79], v[66:67]
	v_lshlrev_b32_e32 v146, 16, v150
	v_pk_fma_f32 v[78:79], v[6:7], v[106:107], v[78:79]
	v_and_b32_e32 v147, 0xffff0000, v150
	v_pk_fma_f32 v[78:79], v[8:9], v[80:81], v[78:79]
	s_nop 0
	v_pk_fma_f32 v[78:79], v[10:11], v[114:115], v[78:79]
	s_nop 0
	v_pk_fma_f32 v[78:79], v[12:13], v[82:83], v[78:79]
	s_nop 0
	v_pk_fma_f32 v[78:79], v[14:15], v[116:117], v[78:79]
	s_nop 0
	v_pk_fma_f32 v[78:79], v[16:17], v[84:85], v[78:79]
	s_nop 0
	v_pk_fma_f32 v[78:79], v[18:19], v[86:87], v[78:79]
	s_nop 0
	v_pk_fma_f32 v[78:79], v[20:21], v[88:89], v[78:79]
	s_nop 0
	v_pk_fma_f32 v[78:79], v[22:23], v[90:91], v[78:79]
	s_nop 0
	v_pk_fma_f32 v[78:79], v[24:25], v[92:93], v[78:79]
	s_nop 0
	v_pk_fma_f32 v[78:79], v[26:27], v[96:97], v[78:79]
	s_nop 0
	v_pk_fma_f32 v[78:79], v[28:29], v[102:103], v[78:79]
	s_nop 0
	v_pk_fma_f32 v[78:79], v[30:31], v[108:109], v[78:79]
	s_nop 0
	v_pk_fma_f32 v[78:79], v[32:33], v[110:111], v[78:79]
	s_nop 0
	v_pk_fma_f32 v[78:79], v[34:35], v[112:113], v[78:79]
	s_nop 0
	v_pk_fma_f32 v[78:79], v[36:37], v[118:119], v[78:79]
	s_nop 0
	v_pk_fma_f32 v[78:79], v[38:39], v[120:121], v[78:79]
	s_nop 0
	v_pk_fma_f32 v[78:79], v[40:41], v[122:123], v[78:79]
	s_nop 0
	v_pk_fma_f32 v[78:79], v[42:43], v[124:125], v[78:79]
	s_nop 0
	v_pk_fma_f32 v[78:79], v[44:45], v[126:127], v[78:79]
	s_nop 0
	v_pk_fma_f32 v[78:79], v[46:47], v[128:129], v[78:79]
	s_nop 0
	v_pk_fma_f32 v[78:79], v[48:49], v[130:131], v[78:79]
	s_nop 0
	v_pk_fma_f32 v[78:79], v[50:51], v[132:133], v[78:79]
	s_nop 0
	v_pk_fma_f32 v[78:79], v[52:53], v[134:135], v[78:79]
	s_nop 0
	v_pk_fma_f32 v[78:79], v[54:55], v[136:137], v[78:79]
	s_nop 0
	v_pk_fma_f32 v[78:79], v[56:57], v[138:139], v[78:79]
	s_nop 0
	v_pk_fma_f32 v[78:79], v[58:59], v[140:141], v[78:79]
	s_nop 0
	v_pk_fma_f32 v[78:79], v[60:61], v[142:143], v[78:79]
	s_nop 0
	v_pk_fma_f32 v[78:79], v[62:63], v[144:145], v[78:79]
	s_nop 0
	v_pk_fma_f32 v[78:79], v[64:65], v[146:147], v[78:79]
	s_nop 0
	v_pk_mul_f32 v[148:149], v[78:79], v[78:79]
	v_add_f32_e32 v150, v78, v79
	v_add_f32_e32 v148, v148, v149
	s_nop 1
	v_mov_b32_dpp v151, v150 quad_perm:[1,0,3,2] row_mask:0xf bank_mask:0xf
	s_nop 1
	v_mov_b32_dpp v149, v148 quad_perm:[1,0,3,2] row_mask:0xf bank_mask:0xf
	s_waitcnt lgkmcnt(0)
	v_add_f32_e32 v150, v150, v151
	s_waitcnt lgkmcnt(0)
	v_add_f32_e32 v148, v148, v149
	s_nop 1
	v_mov_b32_dpp v151, v150 quad_perm:[2,3,0,1] row_mask:0xf bank_mask:0xf
	s_nop 1
	v_mov_b32_dpp v149, v148 quad_perm:[2,3,0,1] row_mask:0xf bank_mask:0xf
	s_waitcnt lgkmcnt(0)
	v_add_f32_e32 v150, v150, v151
	s_waitcnt lgkmcnt(0)
	v_add_f32_e32 v148, v148, v149
	s_nop 1
	v_mov_b32_dpp v151, v150 row_half_mirror row_mask:0xf bank_mask:0xf
	s_nop 1
	v_mov_b32_dpp v151, v151 quad_perm:[3,2,1,0] row_mask:0xf bank_mask:0xf
	s_nop 1
	v_mov_b32_dpp v149, v148 row_half_mirror row_mask:0xf bank_mask:0xf
	s_nop 1
	v_mov_b32_dpp v149, v149 quad_perm:[3,2,1,0] row_mask:0xf bank_mask:0xf
	s_waitcnt lgkmcnt(0)
	v_add_f32_e32 v150, v150, v151
	s_waitcnt lgkmcnt(0)
	v_add_f32_e32 v148, v148, v149
	s_nop 1
	v_mov_b32_dpp v151, v150 row_ror:8 row_mask:0xf bank_mask:0xf
	s_nop 1
	v_mov_b32_dpp v149, v148 row_ror:8 row_mask:0xf bank_mask:0xf
	s_waitcnt lgkmcnt(0)
	v_add_f32_e32 v150, v150, v151
	s_waitcnt lgkmcnt(0)
	v_add_f32_e32 v149, v148, v149
	ds_swizzle_b32 v151, v150 offset:swizzle(SWAP,16)
	ds_swizzle_b32 v153, v149 offset:swizzle(SWAP,16)
	s_waitcnt lgkmcnt(1)
	v_add_f32_e32 v148, v150, v151
	s_waitcnt lgkmcnt(0)
	v_add_f32_e32 v149, v149, v153
	v_mov_b32_e32 v150, v148
	v_mov_b32_e32 v151, v149
	s_nop 0
	v_permlane32_swap_b32_e32 v148, v150
	v_permlane32_swap_b32_e32 v149, v151
	s_and_saveexec_b64 s[12:13], s[6:7]
	s_add_i32 s19, s14, s64
	v_pk_add_f32 v[148:149], v[148:149], v[150:151]
	v_mov_b32_e32 v150, s19
	ds_write2_b32 v150, v148, v149 offset0:16 offset1:17
	s_or_b64 exec, exec, s[12:13]
	v_pk_fma_f32 v[106:107], v[4:5], v[106:107], v[66:67]
	v_lshlrev_b32_e32 v148, 16, v152
	v_pk_fma_f32 v[106:107], v[6:7], v[80:81], v[106:107]
	v_and_b32_e32 v149, 0xffff0000, v152
	v_pk_fma_f32 v[106:107], v[8:9], v[114:115], v[106:107]
	s_nop 0
	v_pk_fma_f32 v[106:107], v[10:11], v[82:83], v[106:107]
	s_nop 0
	v_pk_fma_f32 v[106:107], v[12:13], v[116:117], v[106:107]
	s_nop 0
	v_pk_fma_f32 v[106:107], v[14:15], v[84:85], v[106:107]
	s_nop 0
	v_pk_fma_f32 v[106:107], v[16:17], v[86:87], v[106:107]
	s_nop 0
	v_pk_fma_f32 v[106:107], v[18:19], v[88:89], v[106:107]
	s_nop 0
	v_pk_fma_f32 v[106:107], v[20:21], v[90:91], v[106:107]
	s_nop 0
	v_pk_fma_f32 v[106:107], v[22:23], v[92:93], v[106:107]
	s_nop 0
	v_pk_fma_f32 v[106:107], v[24:25], v[96:97], v[106:107]
	s_nop 0
	v_pk_fma_f32 v[106:107], v[26:27], v[102:103], v[106:107]
	s_nop 0
	v_pk_fma_f32 v[106:107], v[28:29], v[108:109], v[106:107]
	s_nop 0
	v_pk_fma_f32 v[106:107], v[30:31], v[110:111], v[106:107]
	s_nop 0
	v_pk_fma_f32 v[106:107], v[32:33], v[112:113], v[106:107]
	s_nop 0
	v_pk_fma_f32 v[106:107], v[34:35], v[118:119], v[106:107]
	s_nop 0
	v_pk_fma_f32 v[106:107], v[36:37], v[120:121], v[106:107]
	s_nop 0
	v_pk_fma_f32 v[106:107], v[38:39], v[122:123], v[106:107]
	s_nop 0
	v_pk_fma_f32 v[106:107], v[40:41], v[124:125], v[106:107]
	s_nop 0
	v_pk_fma_f32 v[106:107], v[42:43], v[126:127], v[106:107]
	s_nop 0
	v_pk_fma_f32 v[106:107], v[44:45], v[128:129], v[106:107]
	s_nop 0
	v_pk_fma_f32 v[106:107], v[46:47], v[130:131], v[106:107]
	s_nop 0
	v_pk_fma_f32 v[106:107], v[48:49], v[132:133], v[106:107]
	s_nop 0
	v_pk_fma_f32 v[106:107], v[50:51], v[134:135], v[106:107]
	s_nop 0
	v_pk_fma_f32 v[106:107], v[52:53], v[136:137], v[106:107]
	s_nop 0
	v_pk_fma_f32 v[106:107], v[54:55], v[138:139], v[106:107]
	s_nop 0
	v_pk_fma_f32 v[106:107], v[56:57], v[140:141], v[106:107]
	s_nop 0
	v_pk_fma_f32 v[106:107], v[58:59], v[142:143], v[106:107]
	s_nop 0
	v_pk_fma_f32 v[106:107], v[60:61], v[144:145], v[106:107]
	s_nop 0
	v_pk_fma_f32 v[106:107], v[62:63], v[146:147], v[106:107]
	s_nop 0
	v_pk_fma_f32 v[106:107], v[64:65], v[148:149], v[106:107]
	s_nop 0
	v_pk_mul_f32 v[150:151], v[106:107], v[106:107]
	v_add_f32_e32 v152, v106, v107
	v_add_f32_e32 v150, v150, v151
	s_nop 1
	v_mov_b32_dpp v153, v152 quad_perm:[1,0,3,2] row_mask:0xf bank_mask:0xf
	s_nop 1
	v_mov_b32_dpp v151, v150 quad_perm:[1,0,3,2] row_mask:0xf bank_mask:0xf
	s_waitcnt lgkmcnt(0)
	v_add_f32_e32 v152, v152, v153
	s_waitcnt lgkmcnt(0)
	v_add_f32_e32 v150, v150, v151
	s_nop 1
	v_mov_b32_dpp v153, v152 quad_perm:[2,3,0,1] row_mask:0xf bank_mask:0xf
	s_nop 1
	v_mov_b32_dpp v151, v150 quad_perm:[2,3,0,1] row_mask:0xf bank_mask:0xf
	s_waitcnt lgkmcnt(0)
	v_add_f32_e32 v152, v152, v153
	s_waitcnt lgkmcnt(0)
	v_add_f32_e32 v150, v150, v151
	s_nop 1
	v_mov_b32_dpp v153, v152 row_half_mirror row_mask:0xf bank_mask:0xf
	s_nop 1
	v_mov_b32_dpp v153, v153 quad_perm:[3,2,1,0] row_mask:0xf bank_mask:0xf
	s_nop 1
	v_mov_b32_dpp v151, v150 row_half_mirror row_mask:0xf bank_mask:0xf
	s_nop 1
	v_mov_b32_dpp v151, v151 quad_perm:[3,2,1,0] row_mask:0xf bank_mask:0xf
	s_waitcnt lgkmcnt(0)
	v_add_f32_e32 v152, v152, v153
	s_waitcnt lgkmcnt(0)
	v_add_f32_e32 v150, v150, v151
	s_nop 1
	v_mov_b32_dpp v153, v152 row_ror:8 row_mask:0xf bank_mask:0xf
	s_nop 1
	v_mov_b32_dpp v151, v150 row_ror:8 row_mask:0xf bank_mask:0xf
	s_waitcnt lgkmcnt(0)
	v_add_f32_e32 v152, v152, v153
	s_waitcnt lgkmcnt(0)
	v_add_f32_e32 v151, v150, v151
	ds_swizzle_b32 v153, v152 offset:swizzle(SWAP,16)
	ds_swizzle_b32 v155, v151 offset:swizzle(SWAP,16)
	s_waitcnt lgkmcnt(1)
	v_add_f32_e32 v150, v152, v153
	s_waitcnt lgkmcnt(0)
	v_add_f32_e32 v151, v151, v155
	v_mov_b32_e32 v152, v150
	v_mov_b32_e32 v153, v151
	s_nop 0
	v_permlane32_swap_b32_e32 v150, v152
	v_permlane32_swap_b32_e32 v151, v153
	s_and_saveexec_b64 s[12:13], s[6:7]
	s_add_i32 s19, s14, s64
	v_pk_add_f32 v[150:151], v[150:151], v[152:153]
	v_mov_b32_e32 v152, s19
	ds_write2_b32 v152, v150, v151 offset0:18 offset1:19
	s_or_b64 exec, exec, s[12:13]
	v_pk_fma_f32 v[80:81], v[4:5], v[80:81], v[66:67]
	v_lshlrev_b32_e32 v150, 16, v154
	v_pk_fma_f32 v[80:81], v[6:7], v[114:115], v[80:81]
	v_and_b32_e32 v151, 0xffff0000, v154
	v_pk_fma_f32 v[80:81], v[8:9], v[82:83], v[80:81]
	s_nop 0
	v_pk_fma_f32 v[80:81], v[10:11], v[116:117], v[80:81]
	s_nop 0
	v_pk_fma_f32 v[80:81], v[12:13], v[84:85], v[80:81]
	s_nop 0
	v_pk_fma_f32 v[80:81], v[14:15], v[86:87], v[80:81]
	s_nop 0
	v_pk_fma_f32 v[80:81], v[16:17], v[88:89], v[80:81]
	s_nop 0
	v_pk_fma_f32 v[80:81], v[18:19], v[90:91], v[80:81]
	s_nop 0
	v_pk_fma_f32 v[80:81], v[20:21], v[92:93], v[80:81]
	s_nop 0
	v_pk_fma_f32 v[80:81], v[22:23], v[96:97], v[80:81]
	s_nop 0
	v_pk_fma_f32 v[80:81], v[24:25], v[102:103], v[80:81]
	s_nop 0
	v_pk_fma_f32 v[80:81], v[26:27], v[108:109], v[80:81]
	s_nop 0
	v_pk_fma_f32 v[80:81], v[28:29], v[110:111], v[80:81]
	s_nop 0
	v_pk_fma_f32 v[80:81], v[30:31], v[112:113], v[80:81]
	s_nop 0
	v_pk_fma_f32 v[80:81], v[32:33], v[118:119], v[80:81]
	s_nop 0
	v_pk_fma_f32 v[80:81], v[34:35], v[120:121], v[80:81]
	s_nop 0
	v_pk_fma_f32 v[80:81], v[36:37], v[122:123], v[80:81]
	s_nop 0
	v_pk_fma_f32 v[80:81], v[38:39], v[124:125], v[80:81]
	s_nop 0
	v_pk_fma_f32 v[80:81], v[40:41], v[126:127], v[80:81]
	s_nop 0
	v_pk_fma_f32 v[80:81], v[42:43], v[128:129], v[80:81]
	s_nop 0
	v_pk_fma_f32 v[80:81], v[44:45], v[130:131], v[80:81]
	s_nop 0
	v_pk_fma_f32 v[80:81], v[46:47], v[132:133], v[80:81]
	s_nop 0
	v_pk_fma_f32 v[80:81], v[48:49], v[134:135], v[80:81]
	s_nop 0
	v_pk_fma_f32 v[80:81], v[50:51], v[136:137], v[80:81]
	s_nop 0
	v_pk_fma_f32 v[80:81], v[52:53], v[138:139], v[80:81]
	s_nop 0
	v_pk_fma_f32 v[80:81], v[54:55], v[140:141], v[80:81]
	s_nop 0
	v_pk_fma_f32 v[80:81], v[56:57], v[142:143], v[80:81]
	s_nop 0
	v_pk_fma_f32 v[80:81], v[58:59], v[144:145], v[80:81]
	s_nop 0
	v_pk_fma_f32 v[80:81], v[60:61], v[146:147], v[80:81]
	s_nop 0
	v_pk_fma_f32 v[80:81], v[62:63], v[148:149], v[80:81]
	s_nop 0
	v_pk_fma_f32 v[80:81], v[64:65], v[150:151], v[80:81]
	s_nop 0
	v_pk_mul_f32 v[152:153], v[80:81], v[80:81]
	v_add_f32_e32 v154, v80, v81
	v_add_f32_e32 v152, v152, v153
	s_nop 1
	v_mov_b32_dpp v155, v154 quad_perm:[1,0,3,2] row_mask:0xf bank_mask:0xf
	s_nop 1
	v_mov_b32_dpp v153, v152 quad_perm:[1,0,3,2] row_mask:0xf bank_mask:0xf
	s_waitcnt lgkmcnt(0)
	v_add_f32_e32 v154, v154, v155
	s_waitcnt lgkmcnt(0)
	v_add_f32_e32 v152, v152, v153
	s_nop 1
	v_mov_b32_dpp v155, v154 quad_perm:[2,3,0,1] row_mask:0xf bank_mask:0xf
	s_nop 1
	v_mov_b32_dpp v153, v152 quad_perm:[2,3,0,1] row_mask:0xf bank_mask:0xf
	s_waitcnt lgkmcnt(0)
	v_add_f32_e32 v154, v154, v155
	s_waitcnt lgkmcnt(0)
	v_add_f32_e32 v152, v152, v153
	s_nop 1
	v_mov_b32_dpp v155, v154 row_half_mirror row_mask:0xf bank_mask:0xf
	s_nop 1
	v_mov_b32_dpp v155, v155 quad_perm:[3,2,1,0] row_mask:0xf bank_mask:0xf
	s_nop 1
	v_mov_b32_dpp v153, v152 row_half_mirror row_mask:0xf bank_mask:0xf
	s_nop 1
	v_mov_b32_dpp v153, v153 quad_perm:[3,2,1,0] row_mask:0xf bank_mask:0xf
	s_waitcnt lgkmcnt(0)
	v_add_f32_e32 v154, v154, v155
	s_waitcnt lgkmcnt(0)
	v_add_f32_e32 v152, v152, v153
	s_nop 1
	v_mov_b32_dpp v155, v154 row_ror:8 row_mask:0xf bank_mask:0xf
	s_nop 1
	v_mov_b32_dpp v153, v152 row_ror:8 row_mask:0xf bank_mask:0xf
	s_waitcnt lgkmcnt(0)
	v_add_f32_e32 v154, v154, v155
	s_waitcnt lgkmcnt(0)
	v_add_f32_e32 v153, v152, v153
	ds_swizzle_b32 v155, v154 offset:swizzle(SWAP,16)
	ds_swizzle_b32 v157, v153 offset:swizzle(SWAP,16)
	s_waitcnt lgkmcnt(1)
	v_add_f32_e32 v152, v154, v155
	s_waitcnt lgkmcnt(0)
	v_add_f32_e32 v153, v153, v157
	v_mov_b32_e32 v154, v152
	v_mov_b32_e32 v155, v153
	s_nop 0
	v_permlane32_swap_b32_e32 v152, v154
	v_permlane32_swap_b32_e32 v153, v155
	s_and_saveexec_b64 s[12:13], s[6:7]
	s_add_i32 s19, s14, s64
	v_pk_add_f32 v[152:153], v[152:153], v[154:155]
	v_mov_b32_e32 v154, s19
	ds_write2_b32 v154, v152, v153 offset0:20 offset1:21
	s_or_b64 exec, exec, s[12:13]
	v_pk_fma_f32 v[114:115], v[4:5], v[114:115], v[66:67]
	v_lshlrev_b32_e32 v152, 16, v156
	v_pk_fma_f32 v[114:115], v[6:7], v[82:83], v[114:115]
	v_and_b32_e32 v153, 0xffff0000, v156
	v_pk_fma_f32 v[114:115], v[8:9], v[116:117], v[114:115]
	s_nop 0
	v_pk_fma_f32 v[114:115], v[10:11], v[84:85], v[114:115]
	s_nop 0
	v_pk_fma_f32 v[114:115], v[12:13], v[86:87], v[114:115]
	s_nop 0
	v_pk_fma_f32 v[114:115], v[14:15], v[88:89], v[114:115]
	s_nop 0
	v_pk_fma_f32 v[114:115], v[16:17], v[90:91], v[114:115]
	s_nop 0
	v_pk_fma_f32 v[114:115], v[18:19], v[92:93], v[114:115]
	s_nop 0
	v_pk_fma_f32 v[114:115], v[20:21], v[96:97], v[114:115]
	s_nop 0
	v_pk_fma_f32 v[114:115], v[22:23], v[102:103], v[114:115]
	s_nop 0
	v_pk_fma_f32 v[114:115], v[24:25], v[108:109], v[114:115]
	s_nop 0
	v_pk_fma_f32 v[114:115], v[26:27], v[110:111], v[114:115]
	s_nop 0
	v_pk_fma_f32 v[114:115], v[28:29], v[112:113], v[114:115]
	s_nop 0
	v_pk_fma_f32 v[114:115], v[30:31], v[118:119], v[114:115]
	s_nop 0
	v_pk_fma_f32 v[114:115], v[32:33], v[120:121], v[114:115]
	s_nop 0
	v_pk_fma_f32 v[114:115], v[34:35], v[122:123], v[114:115]
	s_nop 0
	v_pk_fma_f32 v[114:115], v[36:37], v[124:125], v[114:115]
	s_nop 0
	v_pk_fma_f32 v[114:115], v[38:39], v[126:127], v[114:115]
	s_nop 0
	v_pk_fma_f32 v[114:115], v[40:41], v[128:129], v[114:115]
	s_nop 0
	v_pk_fma_f32 v[114:115], v[42:43], v[130:131], v[114:115]
	s_nop 0
	v_pk_fma_f32 v[114:115], v[44:45], v[132:133], v[114:115]
	s_nop 0
	v_pk_fma_f32 v[114:115], v[46:47], v[134:135], v[114:115]
	s_nop 0
	v_pk_fma_f32 v[114:115], v[48:49], v[136:137], v[114:115]
	s_nop 0
	v_pk_fma_f32 v[114:115], v[50:51], v[138:139], v[114:115]
	s_nop 0
	v_pk_fma_f32 v[114:115], v[52:53], v[140:141], v[114:115]
	s_nop 0
	v_pk_fma_f32 v[114:115], v[54:55], v[142:143], v[114:115]
	s_nop 0
	v_pk_fma_f32 v[114:115], v[56:57], v[144:145], v[114:115]
	s_nop 0
	v_pk_fma_f32 v[114:115], v[58:59], v[146:147], v[114:115]
	s_nop 0
	v_pk_fma_f32 v[114:115], v[60:61], v[148:149], v[114:115]
	s_nop 0
	v_pk_fma_f32 v[114:115], v[62:63], v[150:151], v[114:115]
	s_nop 0
	v_pk_fma_f32 v[114:115], v[64:65], v[152:153], v[114:115]
	s_nop 0
	v_pk_mul_f32 v[154:155], v[114:115], v[114:115]
	v_add_f32_e32 v156, v114, v115
	v_add_f32_e32 v154, v154, v155
	s_nop 1
	v_mov_b32_dpp v157, v156 quad_perm:[1,0,3,2] row_mask:0xf bank_mask:0xf
	s_nop 1
	v_mov_b32_dpp v155, v154 quad_perm:[1,0,3,2] row_mask:0xf bank_mask:0xf
	s_waitcnt lgkmcnt(0)
	v_add_f32_e32 v156, v156, v157
	s_waitcnt lgkmcnt(0)
	v_add_f32_e32 v154, v154, v155
	s_nop 1
	v_mov_b32_dpp v157, v156 quad_perm:[2,3,0,1] row_mask:0xf bank_mask:0xf
	s_nop 1
	v_mov_b32_dpp v155, v154 quad_perm:[2,3,0,1] row_mask:0xf bank_mask:0xf
	s_waitcnt lgkmcnt(0)
	v_add_f32_e32 v156, v156, v157
	s_waitcnt lgkmcnt(0)
	v_add_f32_e32 v154, v154, v155
	s_nop 1
	v_mov_b32_dpp v157, v156 row_half_mirror row_mask:0xf bank_mask:0xf
	s_nop 1
	v_mov_b32_dpp v157, v157 quad_perm:[3,2,1,0] row_mask:0xf bank_mask:0xf
	s_nop 1
	v_mov_b32_dpp v155, v154 row_half_mirror row_mask:0xf bank_mask:0xf
	s_nop 1
	v_mov_b32_dpp v155, v155 quad_perm:[3,2,1,0] row_mask:0xf bank_mask:0xf
	s_waitcnt lgkmcnt(0)
	v_add_f32_e32 v156, v156, v157
	s_waitcnt lgkmcnt(0)
	v_add_f32_e32 v154, v154, v155
	s_nop 1
	v_mov_b32_dpp v157, v156 row_ror:8 row_mask:0xf bank_mask:0xf
	s_nop 1
	v_mov_b32_dpp v155, v154 row_ror:8 row_mask:0xf bank_mask:0xf
	s_waitcnt lgkmcnt(0)
	v_add_f32_e32 v156, v156, v157
	s_waitcnt lgkmcnt(0)
	v_add_f32_e32 v155, v154, v155
	ds_swizzle_b32 v157, v156 offset:swizzle(SWAP,16)
	ds_swizzle_b32 v159, v155 offset:swizzle(SWAP,16)
	s_waitcnt lgkmcnt(1)
	v_add_f32_e32 v154, v156, v157
	s_waitcnt lgkmcnt(0)
	v_add_f32_e32 v155, v155, v159
	v_mov_b32_e32 v156, v154
	v_mov_b32_e32 v157, v155
	s_nop 0
	v_permlane32_swap_b32_e32 v154, v156
	v_permlane32_swap_b32_e32 v155, v157
	s_and_saveexec_b64 s[12:13], s[6:7]
	s_add_i32 s19, s14, s64
	v_pk_add_f32 v[154:155], v[154:155], v[156:157]
	v_mov_b32_e32 v156, s19
	ds_write2_b32 v156, v154, v155 offset0:22 offset1:23
	s_or_b64 exec, exec, s[12:13]
	v_pk_fma_f32 v[82:83], v[4:5], v[82:83], v[66:67]
	v_lshlrev_b32_e32 v154, 16, v158
	v_pk_fma_f32 v[82:83], v[6:7], v[116:117], v[82:83]
	v_and_b32_e32 v155, 0xffff0000, v158
	v_pk_fma_f32 v[82:83], v[8:9], v[84:85], v[82:83]
	s_nop 0
	v_pk_fma_f32 v[82:83], v[10:11], v[86:87], v[82:83]
	s_nop 0
	v_pk_fma_f32 v[82:83], v[12:13], v[88:89], v[82:83]
	s_nop 0
	v_pk_fma_f32 v[82:83], v[14:15], v[90:91], v[82:83]
	s_nop 0
	v_pk_fma_f32 v[82:83], v[16:17], v[92:93], v[82:83]
	s_nop 0
	v_pk_fma_f32 v[82:83], v[18:19], v[96:97], v[82:83]
	s_nop 0
	v_pk_fma_f32 v[82:83], v[20:21], v[102:103], v[82:83]
	s_nop 0
	v_pk_fma_f32 v[82:83], v[22:23], v[108:109], v[82:83]
	s_nop 0
	v_pk_fma_f32 v[82:83], v[24:25], v[110:111], v[82:83]
	s_nop 0
	v_pk_fma_f32 v[82:83], v[26:27], v[112:113], v[82:83]
	s_nop 0
	v_pk_fma_f32 v[82:83], v[28:29], v[118:119], v[82:83]
	s_nop 0
	v_pk_fma_f32 v[82:83], v[30:31], v[120:121], v[82:83]
	s_nop 0
	v_pk_fma_f32 v[82:83], v[32:33], v[122:123], v[82:83]
	s_nop 0
	v_pk_fma_f32 v[82:83], v[34:35], v[124:125], v[82:83]
	s_nop 0
	v_pk_fma_f32 v[82:83], v[36:37], v[126:127], v[82:83]
	s_nop 0
	v_pk_fma_f32 v[82:83], v[38:39], v[128:129], v[82:83]
	s_nop 0
	v_pk_fma_f32 v[82:83], v[40:41], v[130:131], v[82:83]
	s_nop 0
	v_pk_fma_f32 v[82:83], v[42:43], v[132:133], v[82:83]
	s_nop 0
	v_pk_fma_f32 v[82:83], v[44:45], v[134:135], v[82:83]
	s_nop 0
	v_pk_fma_f32 v[82:83], v[46:47], v[136:137], v[82:83]
	s_nop 0
	v_pk_fma_f32 v[82:83], v[48:49], v[138:139], v[82:83]
	s_nop 0
	v_pk_fma_f32 v[82:83], v[50:51], v[140:141], v[82:83]
	s_nop 0
	v_pk_fma_f32 v[82:83], v[52:53], v[142:143], v[82:83]
	s_nop 0
	v_pk_fma_f32 v[82:83], v[54:55], v[144:145], v[82:83]
	s_nop 0
	v_pk_fma_f32 v[82:83], v[56:57], v[146:147], v[82:83]
	s_nop 0
	v_pk_fma_f32 v[82:83], v[58:59], v[148:149], v[82:83]
	s_nop 0
	v_pk_fma_f32 v[82:83], v[60:61], v[150:151], v[82:83]
	s_nop 0
	v_pk_fma_f32 v[82:83], v[62:63], v[152:153], v[82:83]
	s_nop 0
	v_pk_fma_f32 v[82:83], v[64:65], v[154:155], v[82:83]
	s_nop 0
	v_pk_mul_f32 v[156:157], v[82:83], v[82:83]
	v_add_f32_e32 v158, v82, v83
	v_add_f32_e32 v156, v156, v157
	s_nop 1
	v_mov_b32_dpp v159, v158 quad_perm:[1,0,3,2] row_mask:0xf bank_mask:0xf
	s_nop 1
	v_mov_b32_dpp v157, v156 quad_perm:[1,0,3,2] row_mask:0xf bank_mask:0xf
	s_waitcnt lgkmcnt(0)
	v_add_f32_e32 v158, v158, v159
	s_waitcnt lgkmcnt(0)
	v_add_f32_e32 v156, v156, v157
	s_nop 1
	v_mov_b32_dpp v159, v158 quad_perm:[2,3,0,1] row_mask:0xf bank_mask:0xf
	s_nop 1
	v_mov_b32_dpp v157, v156 quad_perm:[2,3,0,1] row_mask:0xf bank_mask:0xf
	s_waitcnt lgkmcnt(0)
	v_add_f32_e32 v158, v158, v159
	s_waitcnt lgkmcnt(0)
	v_add_f32_e32 v156, v156, v157
	s_nop 1
	v_mov_b32_dpp v159, v158 row_half_mirror row_mask:0xf bank_mask:0xf
	s_nop 1
	v_mov_b32_dpp v159, v159 quad_perm:[3,2,1,0] row_mask:0xf bank_mask:0xf
	s_nop 1
	v_mov_b32_dpp v157, v156 row_half_mirror row_mask:0xf bank_mask:0xf
	s_nop 1
	v_mov_b32_dpp v157, v157 quad_perm:[3,2,1,0] row_mask:0xf bank_mask:0xf
	s_waitcnt lgkmcnt(0)
	v_add_f32_e32 v158, v158, v159
	s_waitcnt lgkmcnt(0)
	v_add_f32_e32 v156, v156, v157
	s_nop 1
	v_mov_b32_dpp v159, v158 row_ror:8 row_mask:0xf bank_mask:0xf
	s_nop 1
	v_mov_b32_dpp v157, v156 row_ror:8 row_mask:0xf bank_mask:0xf
	s_waitcnt lgkmcnt(0)
	v_add_f32_e32 v158, v158, v159
	s_waitcnt lgkmcnt(0)
	v_add_f32_e32 v157, v156, v157
	ds_swizzle_b32 v159, v158 offset:swizzle(SWAP,16)
	ds_swizzle_b32 v161, v157 offset:swizzle(SWAP,16)
	s_waitcnt lgkmcnt(1)
	v_add_f32_e32 v156, v158, v159
	s_waitcnt lgkmcnt(0)
	v_add_f32_e32 v157, v157, v161
	v_mov_b32_e32 v158, v156
	v_mov_b32_e32 v159, v157
	s_nop 0
	v_permlane32_swap_b32_e32 v156, v158
	v_permlane32_swap_b32_e32 v157, v159
	s_and_saveexec_b64 s[12:13], s[6:7]
	s_add_i32 s19, s14, s64
	v_pk_add_f32 v[156:157], v[156:157], v[158:159]
	v_mov_b32_e32 v158, s19
	ds_write2_b32 v158, v156, v157 offset0:24 offset1:25
	s_or_b64 exec, exec, s[12:13]
	v_pk_fma_f32 v[116:117], v[4:5], v[116:117], v[66:67]
	v_lshlrev_b32_e32 v156, 16, v160
	v_pk_fma_f32 v[116:117], v[6:7], v[84:85], v[116:117]
	v_and_b32_e32 v157, 0xffff0000, v160
	v_pk_fma_f32 v[116:117], v[8:9], v[86:87], v[116:117]
	s_nop 0
	v_pk_fma_f32 v[116:117], v[10:11], v[88:89], v[116:117]
	s_nop 0
	v_pk_fma_f32 v[116:117], v[12:13], v[90:91], v[116:117]
	s_nop 0
	v_pk_fma_f32 v[116:117], v[14:15], v[92:93], v[116:117]
	s_nop 0
	v_pk_fma_f32 v[116:117], v[16:17], v[96:97], v[116:117]
	s_nop 0
	v_pk_fma_f32 v[116:117], v[18:19], v[102:103], v[116:117]
	s_nop 0
	v_pk_fma_f32 v[116:117], v[20:21], v[108:109], v[116:117]
	s_nop 0
	v_pk_fma_f32 v[116:117], v[22:23], v[110:111], v[116:117]
	s_nop 0
	v_pk_fma_f32 v[116:117], v[24:25], v[112:113], v[116:117]
	s_nop 0
	v_pk_fma_f32 v[116:117], v[26:27], v[118:119], v[116:117]
	s_nop 0
	v_pk_fma_f32 v[116:117], v[28:29], v[120:121], v[116:117]
	s_nop 0
	v_pk_fma_f32 v[116:117], v[30:31], v[122:123], v[116:117]
	s_nop 0
	v_pk_fma_f32 v[116:117], v[32:33], v[124:125], v[116:117]
	s_nop 0
	v_pk_fma_f32 v[116:117], v[34:35], v[126:127], v[116:117]
	s_nop 0
	v_pk_fma_f32 v[116:117], v[36:37], v[128:129], v[116:117]
	s_nop 0
	v_pk_fma_f32 v[116:117], v[38:39], v[130:131], v[116:117]
	s_nop 0
	v_pk_fma_f32 v[116:117], v[40:41], v[132:133], v[116:117]
	s_nop 0
	v_pk_fma_f32 v[116:117], v[42:43], v[134:135], v[116:117]
	s_nop 0
	v_pk_fma_f32 v[116:117], v[44:45], v[136:137], v[116:117]
	s_nop 0
	v_pk_fma_f32 v[116:117], v[46:47], v[138:139], v[116:117]
	s_nop 0
	v_pk_fma_f32 v[116:117], v[48:49], v[140:141], v[116:117]
	s_nop 0
	v_pk_fma_f32 v[116:117], v[50:51], v[142:143], v[116:117]
	s_nop 0
	v_pk_fma_f32 v[116:117], v[52:53], v[144:145], v[116:117]
	s_nop 0
	v_pk_fma_f32 v[116:117], v[54:55], v[146:147], v[116:117]
	s_nop 0
	v_pk_fma_f32 v[116:117], v[56:57], v[148:149], v[116:117]
	s_nop 0
	v_pk_fma_f32 v[116:117], v[58:59], v[150:151], v[116:117]
	s_nop 0
	v_pk_fma_f32 v[116:117], v[60:61], v[152:153], v[116:117]
	s_nop 0
	v_pk_fma_f32 v[116:117], v[62:63], v[154:155], v[116:117]
	s_nop 0
	v_pk_fma_f32 v[116:117], v[64:65], v[156:157], v[116:117]
	s_nop 0
	v_pk_mul_f32 v[158:159], v[116:117], v[116:117]
	v_add_f32_e32 v160, v116, v117
	v_add_f32_e32 v158, v158, v159
	s_nop 1
	v_mov_b32_dpp v161, v160 quad_perm:[1,0,3,2] row_mask:0xf bank_mask:0xf
	s_nop 1
	v_mov_b32_dpp v159, v158 quad_perm:[1,0,3,2] row_mask:0xf bank_mask:0xf
	s_waitcnt lgkmcnt(0)
	v_add_f32_e32 v160, v160, v161
	s_waitcnt lgkmcnt(0)
	v_add_f32_e32 v158, v158, v159
	s_nop 1
	v_mov_b32_dpp v161, v160 quad_perm:[2,3,0,1] row_mask:0xf bank_mask:0xf
	s_nop 1
	v_mov_b32_dpp v159, v158 quad_perm:[2,3,0,1] row_mask:0xf bank_mask:0xf
	s_waitcnt lgkmcnt(0)
	v_add_f32_e32 v160, v160, v161
	s_waitcnt lgkmcnt(0)
	v_add_f32_e32 v158, v158, v159
	s_nop 1
	v_mov_b32_dpp v161, v160 row_half_mirror row_mask:0xf bank_mask:0xf
	s_nop 1
	v_mov_b32_dpp v161, v161 quad_perm:[3,2,1,0] row_mask:0xf bank_mask:0xf
	s_nop 1
	v_mov_b32_dpp v159, v158 row_half_mirror row_mask:0xf bank_mask:0xf
	s_nop 1
	v_mov_b32_dpp v159, v159 quad_perm:[3,2,1,0] row_mask:0xf bank_mask:0xf
	s_waitcnt lgkmcnt(0)
	v_add_f32_e32 v160, v160, v161
	s_waitcnt lgkmcnt(0)
	v_add_f32_e32 v158, v158, v159
	s_nop 1
	v_mov_b32_dpp v161, v160 row_ror:8 row_mask:0xf bank_mask:0xf
	s_nop 1
	v_mov_b32_dpp v159, v158 row_ror:8 row_mask:0xf bank_mask:0xf
	s_waitcnt lgkmcnt(0)
	v_add_f32_e32 v160, v160, v161
	s_waitcnt lgkmcnt(0)
	v_add_f32_e32 v159, v158, v159
	ds_swizzle_b32 v161, v160 offset:swizzle(SWAP,16)
	ds_swizzle_b32 v163, v159 offset:swizzle(SWAP,16)
	s_waitcnt lgkmcnt(1)
	v_add_f32_e32 v158, v160, v161
	s_waitcnt lgkmcnt(0)
	v_add_f32_e32 v159, v159, v163
	v_mov_b32_e32 v160, v158
	v_mov_b32_e32 v161, v159
	s_nop 0
	v_permlane32_swap_b32_e32 v158, v160
	v_permlane32_swap_b32_e32 v159, v161
	s_and_saveexec_b64 s[12:13], s[6:7]
	s_add_i32 s19, s14, s64
	v_pk_add_f32 v[158:159], v[158:159], v[160:161]
	v_mov_b32_e32 v160, s19
	ds_write2_b32 v160, v158, v159 offset0:26 offset1:27
	s_or_b64 exec, exec, s[12:13]
	v_pk_fma_f32 v[84:85], v[4:5], v[84:85], v[66:67]
	v_lshlrev_b32_e32 v158, 16, v162
	v_pk_fma_f32 v[84:85], v[6:7], v[86:87], v[84:85]
	v_and_b32_e32 v159, 0xffff0000, v162
	v_pk_fma_f32 v[84:85], v[8:9], v[88:89], v[84:85]
	s_nop 0
	v_pk_fma_f32 v[84:85], v[10:11], v[90:91], v[84:85]
	s_nop 0
	v_pk_fma_f32 v[84:85], v[12:13], v[92:93], v[84:85]
	s_nop 0
	v_pk_fma_f32 v[84:85], v[14:15], v[96:97], v[84:85]
	s_nop 0
	v_pk_fma_f32 v[84:85], v[16:17], v[102:103], v[84:85]
	s_nop 0
	v_pk_fma_f32 v[84:85], v[18:19], v[108:109], v[84:85]
	s_nop 0
	v_pk_fma_f32 v[84:85], v[20:21], v[110:111], v[84:85]
	s_nop 0
	v_pk_fma_f32 v[84:85], v[22:23], v[112:113], v[84:85]
	s_nop 0
	v_pk_fma_f32 v[84:85], v[24:25], v[118:119], v[84:85]
	s_nop 0
	v_pk_fma_f32 v[84:85], v[26:27], v[120:121], v[84:85]
	s_nop 0
	v_pk_fma_f32 v[84:85], v[28:29], v[122:123], v[84:85]
	s_nop 0
	v_pk_fma_f32 v[84:85], v[30:31], v[124:125], v[84:85]
	s_nop 0
	v_pk_fma_f32 v[84:85], v[32:33], v[126:127], v[84:85]
	s_nop 0
	v_pk_fma_f32 v[84:85], v[34:35], v[128:129], v[84:85]
	s_nop 0
	v_pk_fma_f32 v[84:85], v[36:37], v[130:131], v[84:85]
	s_nop 0
	v_pk_fma_f32 v[84:85], v[38:39], v[132:133], v[84:85]
	s_nop 0
	v_pk_fma_f32 v[84:85], v[40:41], v[134:135], v[84:85]
	s_nop 0
	v_pk_fma_f32 v[84:85], v[42:43], v[136:137], v[84:85]
	s_nop 0
	v_pk_fma_f32 v[84:85], v[44:45], v[138:139], v[84:85]
	s_nop 0
	v_pk_fma_f32 v[84:85], v[46:47], v[140:141], v[84:85]
	s_nop 0
	v_pk_fma_f32 v[84:85], v[48:49], v[142:143], v[84:85]
	s_nop 0
	v_pk_fma_f32 v[84:85], v[50:51], v[144:145], v[84:85]
	s_nop 0
	v_pk_fma_f32 v[84:85], v[52:53], v[146:147], v[84:85]
	s_nop 0
	v_pk_fma_f32 v[84:85], v[54:55], v[148:149], v[84:85]
	s_nop 0
	v_pk_fma_f32 v[84:85], v[56:57], v[150:151], v[84:85]
	s_nop 0
	v_pk_fma_f32 v[84:85], v[58:59], v[152:153], v[84:85]
	s_nop 0
	v_pk_fma_f32 v[84:85], v[60:61], v[154:155], v[84:85]
	s_nop 0
	v_pk_fma_f32 v[84:85], v[62:63], v[156:157], v[84:85]
	s_nop 0
	v_pk_fma_f32 v[84:85], v[64:65], v[158:159], v[84:85]
	s_nop 0
	v_pk_mul_f32 v[160:161], v[84:85], v[84:85]
	v_add_f32_e32 v162, v84, v85
	v_add_f32_e32 v160, v160, v161
	s_nop 1
	v_mov_b32_dpp v163, v162 quad_perm:[1,0,3,2] row_mask:0xf bank_mask:0xf
	s_nop 1
	v_mov_b32_dpp v161, v160 quad_perm:[1,0,3,2] row_mask:0xf bank_mask:0xf
	s_waitcnt lgkmcnt(0)
	v_add_f32_e32 v162, v162, v163
	s_waitcnt lgkmcnt(0)
	v_add_f32_e32 v160, v160, v161
	s_nop 1
	v_mov_b32_dpp v163, v162 quad_perm:[2,3,0,1] row_mask:0xf bank_mask:0xf
	s_nop 1
	v_mov_b32_dpp v161, v160 quad_perm:[2,3,0,1] row_mask:0xf bank_mask:0xf
	s_waitcnt lgkmcnt(0)
	v_add_f32_e32 v162, v162, v163
	s_waitcnt lgkmcnt(0)
	v_add_f32_e32 v160, v160, v161
	s_nop 1
	v_mov_b32_dpp v163, v162 row_half_mirror row_mask:0xf bank_mask:0xf
	s_nop 1
	v_mov_b32_dpp v163, v163 quad_perm:[3,2,1,0] row_mask:0xf bank_mask:0xf
	s_nop 1
	v_mov_b32_dpp v161, v160 row_half_mirror row_mask:0xf bank_mask:0xf
	s_nop 1
	v_mov_b32_dpp v161, v161 quad_perm:[3,2,1,0] row_mask:0xf bank_mask:0xf
	s_waitcnt lgkmcnt(0)
	v_add_f32_e32 v162, v162, v163
	s_waitcnt lgkmcnt(0)
	v_add_f32_e32 v160, v160, v161
	s_nop 1
	v_mov_b32_dpp v163, v162 row_ror:8 row_mask:0xf bank_mask:0xf
	s_nop 1
	v_mov_b32_dpp v161, v160 row_ror:8 row_mask:0xf bank_mask:0xf
	s_waitcnt lgkmcnt(0)
	v_add_f32_e32 v162, v162, v163
	s_waitcnt lgkmcnt(0)
	v_add_f32_e32 v161, v160, v161
	ds_swizzle_b32 v163, v162 offset:swizzle(SWAP,16)
	ds_swizzle_b32 v169, v161 offset:swizzle(SWAP,16)
	s_waitcnt lgkmcnt(1)
	v_add_f32_e32 v160, v162, v163
	s_waitcnt lgkmcnt(0)
	v_add_f32_e32 v161, v161, v169
	v_mov_b32_e32 v162, v160
	v_mov_b32_e32 v163, v161
	s_nop 0
	v_permlane32_swap_b32_e32 v160, v162
	v_permlane32_swap_b32_e32 v161, v163
	s_and_saveexec_b64 s[12:13], s[6:7]
	s_add_i32 s19, s14, s64
	v_pk_add_f32 v[160:161], v[160:161], v[162:163]
	v_mov_b32_e32 v162, s19
	ds_write2_b32 v162, v160, v161 offset0:28 offset1:29
	s_or_b64 exec, exec, s[12:13]
	v_pk_fma_f32 v[86:87], v[4:5], v[86:87], v[66:67]
	s_nop 0
	v_pk_fma_f32 v[86:87], v[6:7], v[88:89], v[86:87]
	v_lshlrev_b32_e32 v88, 16, v168
	v_pk_fma_f32 v[86:87], v[8:9], v[90:91], v[86:87]
	v_and_b32_e32 v89, 0xffff0000, v168
	v_pk_fma_f32 v[86:87], v[10:11], v[92:93], v[86:87]
	s_nop 0
	v_pk_fma_f32 v[86:87], v[12:13], v[96:97], v[86:87]
	s_nop 0
	v_pk_fma_f32 v[86:87], v[14:15], v[102:103], v[86:87]
	s_nop 0
	v_pk_fma_f32 v[86:87], v[16:17], v[108:109], v[86:87]
	s_nop 0
	v_pk_fma_f32 v[86:87], v[18:19], v[110:111], v[86:87]
	s_nop 0
	v_pk_fma_f32 v[86:87], v[20:21], v[112:113], v[86:87]
	s_nop 0
	v_pk_fma_f32 v[86:87], v[22:23], v[118:119], v[86:87]
	s_nop 0
	v_pk_fma_f32 v[86:87], v[24:25], v[120:121], v[86:87]
	s_nop 0
	v_pk_fma_f32 v[86:87], v[26:27], v[122:123], v[86:87]
	s_nop 0
	v_pk_fma_f32 v[86:87], v[28:29], v[124:125], v[86:87]
	s_nop 0
	v_pk_fma_f32 v[86:87], v[30:31], v[126:127], v[86:87]
	s_nop 0
	v_pk_fma_f32 v[86:87], v[32:33], v[128:129], v[86:87]
	s_nop 0
	v_pk_fma_f32 v[86:87], v[34:35], v[130:131], v[86:87]
	s_nop 0
	v_pk_fma_f32 v[86:87], v[36:37], v[132:133], v[86:87]
	s_nop 0
	v_pk_fma_f32 v[86:87], v[38:39], v[134:135], v[86:87]
	s_nop 0
	v_pk_fma_f32 v[86:87], v[40:41], v[136:137], v[86:87]
	s_nop 0
	v_pk_fma_f32 v[86:87], v[42:43], v[138:139], v[86:87]
	s_nop 0
	v_pk_fma_f32 v[86:87], v[44:45], v[140:141], v[86:87]
	s_nop 0
	v_pk_fma_f32 v[86:87], v[46:47], v[142:143], v[86:87]
	s_nop 0
	v_pk_fma_f32 v[86:87], v[48:49], v[144:145], v[86:87]
	s_nop 0
	v_pk_fma_f32 v[86:87], v[50:51], v[146:147], v[86:87]
	s_nop 0
	v_pk_fma_f32 v[86:87], v[52:53], v[148:149], v[86:87]
	s_nop 0
	v_pk_fma_f32 v[86:87], v[54:55], v[150:151], v[86:87]
	s_nop 0
	v_pk_fma_f32 v[86:87], v[56:57], v[152:153], v[86:87]
	s_nop 0
	v_pk_fma_f32 v[86:87], v[58:59], v[154:155], v[86:87]
	s_nop 0
	v_pk_fma_f32 v[86:87], v[60:61], v[156:157], v[86:87]
	s_nop 0
	v_pk_fma_f32 v[86:87], v[62:63], v[158:159], v[86:87]
	s_nop 0
	v_pk_fma_f32 v[86:87], v[64:65], v[88:89], v[86:87]
	s_nop 0
	v_pk_mul_f32 v[88:89], v[86:87], v[86:87]
	v_add_f32_e32 v90, v86, v87
	v_add_f32_e32 v88, v88, v89
	s_nop 1
	v_mov_b32_dpp v91, v90 quad_perm:[1,0,3,2] row_mask:0xf bank_mask:0xf
	s_nop 1
	v_mov_b32_dpp v89, v88 quad_perm:[1,0,3,2] row_mask:0xf bank_mask:0xf
	s_waitcnt lgkmcnt(0)
	v_add_f32_e32 v90, v90, v91
	s_waitcnt lgkmcnt(0)
	v_add_f32_e32 v88, v88, v89
	s_nop 1
	v_mov_b32_dpp v91, v90 quad_perm:[2,3,0,1] row_mask:0xf bank_mask:0xf
	s_nop 1
	v_mov_b32_dpp v89, v88 quad_perm:[2,3,0,1] row_mask:0xf bank_mask:0xf
	s_waitcnt lgkmcnt(0)
	v_add_f32_e32 v90, v90, v91
	s_waitcnt lgkmcnt(0)
	v_add_f32_e32 v88, v88, v89
	s_nop 1
	v_mov_b32_dpp v91, v90 row_half_mirror row_mask:0xf bank_mask:0xf
	s_nop 1
	v_mov_b32_dpp v91, v91 quad_perm:[3,2,1,0] row_mask:0xf bank_mask:0xf
	s_nop 1
	v_mov_b32_dpp v89, v88 row_half_mirror row_mask:0xf bank_mask:0xf
	s_nop 1
	v_mov_b32_dpp v89, v89 quad_perm:[3,2,1,0] row_mask:0xf bank_mask:0xf
	s_waitcnt lgkmcnt(0)
	v_add_f32_e32 v90, v90, v91
	s_waitcnt lgkmcnt(0)
	v_add_f32_e32 v88, v88, v89
	s_nop 1
	v_mov_b32_dpp v91, v90 row_ror:8 row_mask:0xf bank_mask:0xf
	s_nop 1
	v_mov_b32_dpp v89, v88 row_ror:8 row_mask:0xf bank_mask:0xf
	s_waitcnt lgkmcnt(0)
	v_add_f32_e32 v90, v90, v91
	s_waitcnt lgkmcnt(0)
	v_add_f32_e32 v89, v88, v89
	ds_swizzle_b32 v91, v90 offset:swizzle(SWAP,16)
	ds_swizzle_b32 v92, v89 offset:swizzle(SWAP,16)
	s_waitcnt lgkmcnt(1)
	v_add_f32_e32 v88, v90, v91
	s_waitcnt lgkmcnt(0)
	v_add_f32_e32 v89, v89, v92
	v_mov_b32_e32 v90, v88
	v_mov_b32_e32 v91, v89
	s_nop 0
	v_permlane32_swap_b32_e32 v88, v90
	v_permlane32_swap_b32_e32 v89, v91
	s_and_saveexec_b64 s[12:13], s[6:7]
	s_cbranch_execz .LBB0_432
	s_add_i32 s19, s14, s64
	v_pk_add_f32 v[88:89], v[88:89], v[90:91]
	v_mov_b32_e32 v90, s19
	ds_write2_b32 v90, v88, v89 offset0:30 offset1:31
	s_branch .LBB0_432

.LBB0_1032:
	v_mbcnt_lo_u32_b32 v128, -1, 0
	v_mbcnt_hi_u32_b32 v128, -1, v128
	s_mov_b32 s10, 0x41800000
	v_lshrrev_b32_e32 v130, 1, v128
	v_and_or_b32 v130, v130, 24, s39
	v_and_b32_e32 v129, 15, v128
	v_lshl_add_u32 v131, v130, 2, s14
	v_and_b32_e32 v128, 16, v128
	v_add_u32_e32 v152, 0x20000, v131
	v_add_u32_e32 v151, 0x20400, v131
	v_cmp_eq_u32_e32 vcc, 0, v128
	v_or3_b32 v153, s51, v129, v128
	v_lshrrev_b32_e32 v128, 1, v128
	v_sub_u32_e32 v158, v130, v128
	ds_read_b128 v[132:135], v152
	ds_read_b128 v[136:139], v152 offset:16
	ds_read_b128 v[140:143], v151
	ds_read_b128 v[128:131], v151 offset:16
	s_mov_b32 s12, 0x40088889
	s_add_u32 s8, s31, s62
	s_addc_u32 s9, s33, 0
	v_lshl_add_u32 v153, v153, 10, v158
	s_waitcnt lgkmcnt(0)
	v_pk_mul_f32 v[140:141], v[140:141], s[12:13] op_sel_hi:[1,0]
	v_pk_mul_f32 v[132:133], v[132:133], s[10:11] op_sel_hi:[1,0]
	v_pk_mul_f32 v[142:143], v[142:143], s[12:13] op_sel_hi:[1,0]
	v_pk_mul_f32 v[134:135], v[134:135], s[10:11] op_sel_hi:[1,0]
	v_pk_mul_f32 v[128:129], v[128:129], s[12:13] op_sel_hi:[1,0]
	v_pk_mul_f32 v[136:137], v[136:137], s[10:11] op_sel_hi:[1,0]
	v_pk_mul_f32 v[130:131], v[130:131], s[12:13] op_sel_hi:[1,0]
	v_pk_mul_f32 v[138:139], v[138:139], s[10:11] op_sel_hi:[1,0]
	v_pk_fma_f32 v[68:69], v[68:69], v[140:141], v[132:133]
	v_pk_fma_f32 v[70:71], v[70:71], v[142:143], v[134:135]
	v_pk_fma_f32 v[76:77], v[76:77], v[128:129], v[136:137]
	v_pk_fma_f32 v[78:79], v[78:79], v[130:131], v[138:139]
	v_pk_fma_f32 v[84:85], v[84:85], v[140:141], v[132:133]
	v_pk_fma_f32 v[86:87], v[86:87], v[142:143], v[134:135]
	v_pk_fma_f32 v[92:93], v[92:93], v[128:129], v[136:137]
	v_pk_fma_f32 v[94:95], v[94:95], v[130:131], v[138:139]
	v_cvt_pk_fp8_f32 v154, v68, v69
	v_cvt_pk_fp8_f32 v155, v76, v77
	v_cvt_pk_fp8_f32 v156, v84, v85
	v_cvt_pk_fp8_f32 v157, v92, v93
	v_cvt_pk_fp8_f32 v154, v70, v71 op_sel:[0,0,1]
	v_cvt_pk_fp8_f32 v155, v78, v79 op_sel:[0,0,1]
	v_cvt_pk_fp8_f32 v156, v86, v87 op_sel:[0,0,1]
	v_cvt_pk_fp8_f32 v157, v94, v95 op_sel:[0,0,1]
	v_add_u32_e32 v158, 0x8000, v153
	s_nop 0
	v_permlane16_swap_b32_e32 v154, v156
	v_permlane16_swap_b32_e32 v155, v157
	global_store_dwordx4 v158, v[154:157], s[8:9]
	v_pk_fma_f32 v[104:105], v[104:105], v[140:141], v[132:133]
	v_pk_fma_f32 v[106:107], v[106:107], v[142:143], v[134:135]
	v_pk_fma_f32 v[112:113], v[112:113], v[128:129], v[136:137]
	v_pk_fma_f32 v[114:115], v[114:115], v[130:131], v[138:139]
	v_pk_fma_f32 v[120:121], v[120:121], v[140:141], v[132:133]
	v_pk_fma_f32 v[122:123], v[122:123], v[142:143], v[134:135]
	v_pk_fma_f32 v[124:125], v[124:125], v[128:129], v[136:137]
	v_pk_fma_f32 v[126:127], v[126:127], v[130:131], v[138:139]
	v_cvt_pk_fp8_f32 v68, v104, v105
	v_cvt_pk_fp8_f32 v69, v112, v113
	v_cvt_pk_fp8_f32 v70, v120, v121
	v_cvt_pk_fp8_f32 v71, v124, v125
	v_cvt_pk_fp8_f32 v68, v106, v107 op_sel:[0,0,1]
	v_cvt_pk_fp8_f32 v69, v114, v115 op_sel:[0,0,1]
	v_cvt_pk_fp8_f32 v70, v122, v123 op_sel:[0,0,1]
	v_cvt_pk_fp8_f32 v71, v126, v127 op_sel:[0,0,1]
	s_nop 0
	v_permlane16_swap_b32_e32 v68, v70
	v_permlane16_swap_b32_e32 v69, v71
	global_store_dwordx4 v153, v[68:71], s[8:9]
	v_pk_fma_f32 v[96:97], v[96:97], v[140:141], v[132:133]
	v_pk_fma_f32 v[98:99], v[98:99], v[142:143], v[134:135]
	v_pk_fma_f32 v[100:101], v[100:101], v[128:129], v[136:137]
	v_pk_fma_f32 v[102:103], v[102:103], v[130:131], v[138:139]
	v_pk_fma_f32 v[108:109], v[108:109], v[140:141], v[132:133]
	v_pk_fma_f32 v[110:111], v[110:111], v[142:143], v[134:135]
	v_pk_fma_f32 v[116:117], v[116:117], v[128:129], v[136:137]
	v_pk_fma_f32 v[118:119], v[118:119], v[130:131], v[138:139]
	v_cvt_pk_fp8_f32 v154, v96, v97
	v_cvt_pk_fp8_f32 v155, v100, v101
	v_cvt_pk_fp8_f32 v156, v108, v109
	v_cvt_pk_fp8_f32 v157, v116, v117
	v_cvt_pk_fp8_f32 v154, v98, v99 op_sel:[0,0,1]
	v_cvt_pk_fp8_f32 v155, v102, v103 op_sel:[0,0,1]
	v_cvt_pk_fp8_f32 v156, v110, v111 op_sel:[0,0,1]
	v_cvt_pk_fp8_f32 v157, v118, v119 op_sel:[0,0,1]
	v_add_u32_e32 v158, 0x20000, v153
	s_nop 0
	v_permlane16_swap_b32_e32 v154, v156
	v_permlane16_swap_b32_e32 v155, v157
	global_store_dwordx4 v158, v[154:157], s[8:9]
	v_pk_fma_f32 v[64:65], v[64:65], v[140:141], v[132:133]
	v_pk_fma_f32 v[66:67], v[66:67], v[142:143], v[134:135]
	v_pk_fma_f32 v[72:73], v[72:73], v[128:129], v[136:137]
	v_pk_fma_f32 v[74:75], v[74:75], v[130:131], v[138:139]
	v_pk_fma_f32 v[80:81], v[80:81], v[140:141], v[132:133]
	v_pk_fma_f32 v[82:83], v[82:83], v[142:143], v[134:135]
	v_pk_fma_f32 v[88:89], v[88:89], v[128:129], v[136:137]
	v_pk_fma_f32 v[90:91], v[90:91], v[130:131], v[138:139]
	v_cvt_pk_fp8_f32 v68, v64, v65
	v_cvt_pk_fp8_f32 v69, v72, v73
	v_cvt_pk_fp8_f32 v70, v80, v81
	v_cvt_pk_fp8_f32 v71, v88, v89
	v_cvt_pk_fp8_f32 v68, v66, v67 op_sel:[0,0,1]
	v_cvt_pk_fp8_f32 v69, v74, v75 op_sel:[0,0,1]
	v_cvt_pk_fp8_f32 v70, v82, v83 op_sel:[0,0,1]
	v_cvt_pk_fp8_f32 v71, v90, v91 op_sel:[0,0,1]
	v_add_u32_e32 v158, 0x28000, v153
	s_nop 0
	v_permlane16_swap_b32_e32 v68, v70
	v_permlane16_swap_b32_e32 v69, v71
	global_store_dwordx4 v158, v[68:71], s[8:9]
	ds_read_b128 v[132:135], v152 offset:512
	ds_read_b128 v[136:139], v152 offset:528
	ds_read_b128 v[140:143], v151 offset:512
	ds_read_b128 v[128:131], v151 offset:528
	s_waitcnt lgkmcnt(0)
	v_pk_mul_f32 v[140:141], v[140:141], s[12:13] op_sel_hi:[1,0]
	v_pk_mul_f32 v[132:133], v[132:133], s[10:11] op_sel_hi:[1,0]
	v_pk_mul_f32 v[142:143], v[142:143], s[12:13] op_sel_hi:[1,0]
	v_pk_mul_f32 v[134:135], v[134:135], s[10:11] op_sel_hi:[1,0]
	v_pk_mul_f32 v[128:129], v[128:129], s[12:13] op_sel_hi:[1,0]
	v_pk_mul_f32 v[136:137], v[136:137], s[10:11] op_sel_hi:[1,0]
	v_pk_mul_f32 v[130:131], v[130:131], s[12:13] op_sel_hi:[1,0]
	v_pk_mul_f32 v[138:139], v[138:139], s[10:11] op_sel_hi:[1,0]
	v_pk_fma_f32 v[40:41], v[40:41], v[140:141], v[132:133]
	v_pk_fma_f32 v[42:43], v[42:43], v[142:143], v[134:135]
	v_pk_fma_f32 v[48:49], v[48:49], v[128:129], v[136:137]
	v_pk_fma_f32 v[50:51], v[50:51], v[130:131], v[138:139]
	v_pk_fma_f32 v[56:57], v[56:57], v[140:141], v[132:133]
	v_pk_fma_f32 v[58:59], v[58:59], v[142:143], v[134:135]
	v_pk_fma_f32 v[60:61], v[60:61], v[128:129], v[136:137]
	v_pk_fma_f32 v[62:63], v[62:63], v[130:131], v[138:139]
	v_cvt_pk_fp8_f32 v154, v40, v41
	v_cvt_pk_fp8_f32 v155, v48, v49
	v_cvt_pk_fp8_f32 v156, v56, v57
	v_cvt_pk_fp8_f32 v157, v60, v61
	v_cvt_pk_fp8_f32 v154, v42, v43 op_sel:[0,0,1]
	v_cvt_pk_fp8_f32 v155, v50, v51 op_sel:[0,0,1]
	v_cvt_pk_fp8_f32 v156, v58, v59 op_sel:[0,0,1]
	v_cvt_pk_fp8_f32 v157, v62, v63 op_sel:[0,0,1]
	s_nop 0
	v_permlane16_swap_b32_e32 v154, v156
	v_permlane16_swap_b32_e32 v155, v157
	global_store_dwordx4 v153, v[154:157], s[8:9] offset:128
	v_pk_fma_f32 v[8:9], v[8:9], v[140:141], v[132:133]
	v_pk_fma_f32 v[10:11], v[10:11], v[142:143], v[134:135]
	v_pk_fma_f32 v[16:17], v[16:17], v[128:129], v[136:137]
	v_pk_fma_f32 v[18:19], v[18:19], v[130:131], v[138:139]
	v_pk_fma_f32 v[24:25], v[24:25], v[140:141], v[132:133]
	v_pk_fma_f32 v[26:27], v[26:27], v[142:143], v[134:135]
	v_pk_fma_f32 v[28:29], v[28:29], v[128:129], v[136:137]
	v_pk_fma_f32 v[30:31], v[30:31], v[130:131], v[138:139]
	v_cvt_pk_fp8_f32 v68, v8, v9
	v_cvt_pk_fp8_f32 v69, v16, v17
	v_cvt_pk_fp8_f32 v70, v24, v25
	v_cvt_pk_fp8_f32 v71, v28, v29
	v_cvt_pk_fp8_f32 v68, v10, v11 op_sel:[0,0,1]
	v_cvt_pk_fp8_f32 v69, v18, v19 op_sel:[0,0,1]
	v_cvt_pk_fp8_f32 v70, v26, v27 op_sel:[0,0,1]
	v_cvt_pk_fp8_f32 v71, v30, v31 op_sel:[0,0,1]
	v_add_u32_e32 v158, 0x8000, v153
	s_nop 0
	v_permlane16_swap_b32_e32 v68, v70
	v_permlane16_swap_b32_e32 v69, v71
	global_store_dwordx4 v158, v[68:71], s[8:9] offset:128
	v_pk_fma_f32 v[32:33], v[32:33], v[140:141], v[132:133]
	v_pk_fma_f32 v[34:35], v[34:35], v[142:143], v[134:135]
	v_pk_fma_f32 v[36:37], v[36:37], v[128:129], v[136:137]
	v_pk_fma_f32 v[38:39], v[38:39], v[130:131], v[138:139]
	v_pk_fma_f32 v[44:45], v[44:45], v[140:141], v[132:133]
	v_pk_fma_f32 v[46:47], v[46:47], v[142:143], v[134:135]
	v_pk_fma_f32 v[52:53], v[52:53], v[128:129], v[136:137]
	v_pk_fma_f32 v[54:55], v[54:55], v[130:131], v[138:139]
	v_cvt_pk_fp8_f32 v154, v32, v33
	v_cvt_pk_fp8_f32 v155, v36, v37
	v_cvt_pk_fp8_f32 v156, v44, v45
	v_cvt_pk_fp8_f32 v157, v52, v53
	v_cvt_pk_fp8_f32 v154, v34, v35 op_sel:[0,0,1]
	v_cvt_pk_fp8_f32 v155, v38, v39 op_sel:[0,0,1]
	v_cvt_pk_fp8_f32 v156, v46, v47 op_sel:[0,0,1]
	v_cvt_pk_fp8_f32 v157, v54, v55 op_sel:[0,0,1]
	v_add_u32_e32 v158, 0x20000, v153
	s_nop 0
	v_permlane16_swap_b32_e32 v154, v156
	v_permlane16_swap_b32_e32 v155, v157
	global_store_dwordx4 v158, v[154:157], s[8:9] offset:128
	v_pk_fma_f32 v[0:1], v[0:1], v[140:141], v[132:133]
	v_pk_fma_f32 v[2:3], v[2:3], v[142:143], v[134:135]
	v_pk_fma_f32 v[4:5], v[4:5], v[128:129], v[136:137]
	v_pk_fma_f32 v[6:7], v[6:7], v[130:131], v[138:139]
	v_pk_fma_f32 v[12:13], v[12:13], v[140:141], v[132:133]
	v_pk_fma_f32 v[14:15], v[14:15], v[142:143], v[134:135]
	v_pk_fma_f32 v[20:21], v[20:21], v[128:129], v[136:137]
	v_pk_fma_f32 v[22:23], v[22:23], v[130:131], v[138:139]
	v_cvt_pk_fp8_f32 v68, v0, v1
	v_cvt_pk_fp8_f32 v69, v4, v5
	v_cvt_pk_fp8_f32 v70, v12, v13
	v_cvt_pk_fp8_f32 v71, v20, v21
	v_cvt_pk_fp8_f32 v68, v2, v3 op_sel:[0,0,1]
	v_cvt_pk_fp8_f32 v69, v6, v7 op_sel:[0,0,1]
	v_cvt_pk_fp8_f32 v70, v14, v15 op_sel:[0,0,1]
	v_cvt_pk_fp8_f32 v71, v22, v23 op_sel:[0,0,1]
	v_add_u32_e32 v158, 0x28000, v153
	s_nop 0
	v_permlane16_swap_b32_e32 v68, v70
	v_permlane16_swap_b32_e32 v69, v71
	global_store_dwordx4 v158, v[68:71], s[8:9] offset:128
	s_mov_b64 s[8:9], -1
	s_andn2_b64 vcc, exec, s[4:5]
	s_cbranch_vccnz .LBB0_1011
	s_andn2_b64 vcc, exec, s[2:3]
	v_mov_b32 v104, 0
	v_mov_b32 v105, 0
	v_mov_b32 v106, 0
	v_mov_b32 v107, 0
	v_mov_b32 v112, 0
	v_mov_b32 v113, 0
	v_mov_b32 v114, 0
	v_mov_b32 v115, 0
	v_mov_b32 v120, 0
	v_mov_b32 v121, 0
	v_mov_b32 v122, 0
	v_mov_b32 v123, 0
	v_mov_b32 v124, 0
	v_mov_b32 v125, 0
	v_mov_b32 v126, 0
	v_mov_b32 v127, 0
	v_mov_b32 v68, 0
	v_mov_b32 v69, 0
	v_mov_b32 v70, 0
	v_mov_b32 v71, 0
	v_mov_b32 v76, 0
	v_mov_b32 v77, 0
	v_mov_b32 v78, 0
	v_mov_b32 v79, 0
	v_mov_b32 v84, 0
	v_mov_b32 v85, 0
	v_mov_b32 v86, 0
	v_mov_b32 v87, 0
	v_mov_b32 v92, 0
	v_mov_b32 v93, 0
	v_mov_b32 v94, 0
	v_mov_b32 v95, 0
	v_mov_b32 v40, 0
	v_mov_b32 v41, 0
	v_mov_b32 v42, 0
	v_mov_b32 v43, 0
	v_mov_b32 v48, 0
	v_mov_b32 v49, 0
	v_mov_b32 v50, 0
	v_mov_b32 v51, 0
	v_mov_b32 v56, 0
	v_mov_b32 v57, 0
	v_mov_b32 v58, 0
	v_mov_b32 v59, 0
	v_mov_b32 v60, 0
	v_mov_b32 v61, 0
	v_mov_b32 v62, 0
	v_mov_b32 v63, 0
	v_mov_b32 v8, 0
	v_mov_b32 v9, 0
	v_mov_b32 v10, 0
	v_mov_b32 v11, 0
	v_mov_b32 v16, 0
	v_mov_b32 v17, 0
	v_mov_b32 v18, 0
	v_mov_b32 v19, 0
	v_mov_b32 v24, 0
	v_mov_b32 v25, 0
	v_mov_b32 v26, 0
	v_mov_b32 v27, 0
	v_mov_b32 v28, 0
	v_mov_b32 v29, 0
	v_mov_b32 v30, 0
	v_mov_b32 v31, 0
	v_mov_b32 v96, 0
	v_mov_b32 v97, 0
	v_mov_b32 v98, 0
	v_mov_b32 v99, 0
	v_mov_b32 v100, 0
	v_mov_b32 v101, 0
	v_mov_b32 v102, 0
	v_mov_b32 v103, 0
	v_mov_b32 v108, 0
	v_mov_b32 v109, 0
	v_mov_b32 v110, 0
	v_mov_b32 v111, 0
	v_mov_b32 v116, 0
	v_mov_b32 v117, 0
	v_mov_b32 v118, 0
	v_mov_b32 v119, 0
	v_mov_b32 v64, 0
	v_mov_b32 v65, 0
	v_mov_b32 v66, 0
	v_mov_b32 v67, 0
	v_mov_b32 v72, 0
	v_mov_b32 v73, 0
	v_mov_b32 v74, 0
	v_mov_b32 v75, 0
	v_mov_b32 v80, 0
	v_mov_b32 v81, 0
	v_mov_b32 v82, 0
	v_mov_b32 v83, 0
	v_mov_b32 v88, 0
	v_mov_b32 v89, 0
	v_mov_b32 v90, 0
	v_mov_b32 v91, 0
	v_mov_b32 v32, 0
	v_mov_b32 v33, 0
	v_mov_b32 v34, 0
	v_mov_b32 v35, 0
	v_mov_b32 v36, 0
	v_mov_b32 v37, 0
	v_mov_b32 v38, 0
	v_mov_b32 v39, 0
	v_mov_b32 v44, 0
	v_mov_b32 v45, 0
	v_mov_b32 v46, 0
	v_mov_b32 v47, 0
	v_mov_b32 v52, 0
	v_mov_b32 v53, 0
	v_mov_b32 v54, 0
	v_mov_b32 v55, 0
	v_mov_b32 v0, 0
	v_mov_b32 v1, 0
	v_mov_b32 v2, 0
	v_mov_b32 v3, 0
	v_mov_b32 v4, 0
	v_mov_b32 v5, 0
	v_mov_b32 v6, 0
	v_mov_b32 v7, 0
	v_mov_b32 v12, 0
	v_mov_b32 v13, 0
	v_mov_b32 v14, 0
	v_mov_b32 v15, 0
	v_mov_b32 v20, 0
	v_mov_b32 v21, 0
	v_mov_b32 v22, 0
	v_mov_b32 v23, 0
	s_cbranch_vccnz .LBB0_1010
	s_barrier
	s_branch .LBB0_1010

.LBB0_1094:
	s_waitcnt vmcnt(2)
	v_ashrrev_i32_e32 v89, 31, v92
	v_mov_b32_e32 v88, v92
	v_lshlrev_b64 v[88:89], 10, v[88:89]
	v_lshl_add_u64 v[88:89], v[124:125], 0, v[88:89]
	global_load_dwordx4 v[96:99], v[88:89], off
	v_ashrrev_i32_e32 v89, 31, v93
	v_mov_b32_e32 v88, v93
	v_lshlrev_b64 v[88:89], 10, v[88:89]
	v_lshl_add_u64 v[88:89], v[124:125], 0, v[88:89]
	global_load_dwordx4 v[106:109], v[88:89], off
	v_ashrrev_i32_e32 v89, 31, v94
	v_mov_b32_e32 v88, v94
	v_lshlrev_b64 v[88:89], 10, v[88:89]
	s_add_i32 s20, s4, 1
	v_lshl_add_u64 v[88:89], v[124:125], 0, v[88:89]
	s_cmp_ge_i32 s20, s12
	global_load_dwordx4 v[110:113], v[88:89], off
	v_ashrrev_i32_e32 v89, 31, v95
	v_mov_b32_e32 v88, v95
	s_cselect_b64 s[6:7], -1, 0
	s_cmp_lt_i32 s20, s12
	v_lshlrev_b64 v[88:89], 10, v[88:89]
	s_cselect_b32 s3, s20, s4
	v_lshl_add_u64 v[88:89], v[124:125], 0, v[88:89]
	s_lshl_b32 s4, s3, 1
	global_load_dwordx4 v[114:117], v[88:89], off
	s_ashr_i32 s5, s4, 31
	s_lshl_b64 s[8:9], s[4:5], 4
	s_add_u32 s4, s13, s8
	s_addc_u32 s5, s14, s9
	s_add_u32 s8, s15, s8
	s_addc_u32 s9, s16, s9
	s_ashr_i32 s3, s2, 31
	s_lshl_b64 s[10:11], s[2:3], 11
	v_lshl_add_u64 v[88:89], v[122:123], 0, s[10:11]
	global_load_dwordx4 v[92:95], v[88:89], off
	s_nop 0
	global_load_dwordx4 v[88:91], v[88:89], off offset:16
	v_ashrrev_i32_e32 v185, 31, v84
	v_mov_b32_e32 v184, v84
	v_lshlrev_b64 v[184:185], 10, v[184:185]
	v_lshl_add_u64 v[184:185], v[124:125], 0, v[184:185]
	global_load_dwordx4 v[222:225], v[184:185], off
	v_ashrrev_i32_e32 v185, 31, v85
	v_mov_b32_e32 v184, v85
	v_lshlrev_b64 v[184:185], 10, v[184:185]
	v_lshl_add_u64 v[184:185], v[124:125], 0, v[184:185]
	global_load_dwordx4 v[226:229], v[184:185], off
	v_ashrrev_i32_e32 v185, 31, v86
	v_mov_b32_e32 v184, v86
	v_lshlrev_b64 v[184:185], 10, v[184:185]
	v_lshl_add_u64 v[184:185], v[124:125], 0, v[184:185]
	global_load_dwordx4 v[230:233], v[184:185], off
	v_ashrrev_i32_e32 v185, 31, v87
	v_mov_b32_e32 v184, v87
	v_lshlrev_b64 v[184:185], 10, v[184:185]
	v_lshl_add_u64 v[184:185], v[124:125], 0, v[184:185]
	global_load_dwordx4 v[244:247], v[184:185], off
	s_add_i32 s24, s2, 1
	s_ashr_i32 s25, s24, 31
	s_lshl_b64 s[24:25], s[24:25], 11
	v_lshl_add_u64 v[186:187], v[122:123], 0, s[24:25]
	global_load_dwordx4 v[192:195], v[186:187], off
	global_load_dwordx4 v[196:199], v[186:187], off offset:16
	s_waitcnt vmcnt(12)
	v_mov_b32_e32 v104, v103
	s_mov_b32 s22, 0x3d800000
	s_mov_b32 s10, 0x3fd744fd
	v_cndmask_b32_e64 v121, 0, 1, s[0:1]
	s_waitcnt vmcnt(11)
	v_cvt_pk_f32_fp8_sdwa v[136:137], v96 src0_sel:WORD_1
	v_cvt_pk_f32_fp8_e32 v[118:119], v96
	v_cvt_pk_f32_fp8_sdwa v[140:141], v97 src0_sel:WORD_1
	v_cvt_pk_f32_fp8_e32 v[138:139], v97
	v_cvt_pk_f32_fp8_e32 v[146:147], v98
	s_waitcnt vmcnt(10)
	v_cvt_pk_f32_fp8_sdwa v[144:145], v106 src0_sel:WORD_1
	v_cvt_pk_f32_fp8_e32 v[142:143], v106
	v_cvt_pk_f32_fp8_sdwa v[154:155], v107 src0_sel:WORD_1
	v_cvt_pk_f32_fp8_e32 v[152:153], v107
	v_pk_mul_f32 v[144:145], v[100:101], v[144:145] op_sel:[1,0]
	v_pk_mul_f32 v[142:143], v[100:101], v[142:143] op_sel:[1,0]
	v_pk_fma_f32 v[136:137], v[100:101], v[136:137], v[144:145] op_sel_hi:[0,1,1]
	s_waitcnt vmcnt(9)
	v_cvt_pk_f32_fp8_sdwa v[160:161], v110 src0_sel:WORD_1
	v_cvt_pk_f32_fp8_e32 v[150:151], v110
	v_cvt_pk_f32_fp8_e32 v[162:163], v111
	v_cvt_pk_f32_fp8_sdwa v[164:165], v111 src0_sel:WORD_1
	v_pk_fma_f32 v[118:119], v[100:101], v[118:119], v[142:143] op_sel_hi:[0,1,1]
	v_cvt_pk_f32_fp8_e32 v[156:157], v108
	v_cvt_pk_f32_fp8_sdwa v[158:159], v108 src0_sel:WORD_1
	v_cvt_pk_f32_fp8_sdwa v[148:149], v98 src0_sel:WORD_1
	v_cvt_pk_f32_fp8_e32 v[166:167], v112
	s_waitcnt vmcnt(8)
	v_cvt_pk_f32_fp8_sdwa v[172:173], v114 src0_sel:WORD_1
	v_cvt_pk_f32_fp8_e32 v[170:171], v114
	v_cvt_pk_f32_fp8_e32 v[174:175], v115
	v_cvt_pk_f32_fp8_sdwa v[114:115], v115 src0_sel:WORD_1
	v_pk_mul_f32 v[172:173], v[104:105], v[172:173] op_sel_hi:[0,1]
	v_pk_fma_f32 v[144:145], v[102:103], v[160:161], v[172:173] op_sel_hi:[0,1,1]
	v_pk_add_f32 v[136:137], v[136:137], v[144:145]
	v_pk_mul_f32 v[144:145], v[34:35], s[22:23] op_sel_hi:[1,0]
	v_pk_mul_f32 v[170:171], v[104:105], v[170:171] op_sel_hi:[0,1]
	s_waitcnt vmcnt(7)
	v_lshlrev_b32_e32 v160, 16, v92
	v_and_b32_e32 v161, 0xffff0000, v92
	v_lshlrev_b32_e32 v92, 16, v93
	v_and_b32_e32 v93, 0xffff0000, v93
	v_pk_mul_f32 v[136:137], v[144:145], v[136:137]
	v_pk_fma_f32 v[142:143], v[102:103], v[150:151], v[170:171] op_sel_hi:[0,1,1]
	v_pk_fma_f32 v[136:137], v[92:93], s[10:11], v[136:137] op_sel_hi:[1,0,1]
	v_pk_mul_f32 v[92:93], v[100:101], v[154:155] op_sel:[1,0]
	v_pk_add_f32 v[118:119], v[118:119], v[142:143]
	v_pk_mul_f32 v[142:143], v[100:101], v[152:153] op_sel:[1,0]
	v_pk_fma_f32 v[92:93], v[100:101], v[140:141], v[92:93] op_sel_hi:[0,1,1]
	v_pk_mul_f32 v[114:115], v[104:105], v[114:115] op_sel_hi:[0,1]
	v_pk_mul_f32 v[140:141], v[104:105], v[174:175] op_sel_hi:[0,1]
	v_cvt_pk_f32_fp8_e32 v[176:177], v116
	v_cvt_pk_f32_fp8_sdwa v[178:179], v116 src0_sel:WORD_1
	v_pk_fma_f32 v[138:139], v[100:101], v[138:139], v[142:143] op_sel_hi:[0,1,1]
	v_pk_fma_f32 v[140:141], v[102:103], v[162:163], v[140:141] op_sel_hi:[0,1,1]
	v_pk_fma_f32 v[114:115], v[102:103], v[164:165], v[114:115] op_sel_hi:[0,1,1]
	v_cvt_pk_f32_fp8_sdwa v[168:169], v112 src0_sel:WORD_1
	v_pk_add_f32 v[92:93], v[92:93], v[114:115]
	v_pk_add_f32 v[114:115], v[138:139], v[140:141]
	v_pk_mul_f32 v[138:139], v[38:39], s[22:23] op_sel_hi:[1,0]
	v_lshlrev_b32_e32 v170, 16, v94
	v_and_b32_e32 v171, 0xffff0000, v94
	v_lshlrev_b32_e32 v94, 16, v95
	v_and_b32_e32 v95, 0xffff0000, v95
	v_pk_mul_f32 v[92:93], v[138:139], v[92:93]
	v_cvt_pk_f32_fp8_e32 v[106:107], v109
	v_pk_fma_f32 v[154:155], v[94:95], s[10:11], v[92:93] op_sel_hi:[1,0,1]
	v_pk_mul_f32 v[94:95], v[100:101], v[156:157] op_sel:[1,0]
	v_cvt_pk_f32_fp8_sdwa v[108:109], v109 src0_sel:WORD_1
	v_cvt_pk_f32_fp8_e32 v[180:181], v117
	v_cvt_pk_f32_fp8_sdwa v[116:117], v117 src0_sel:WORD_1
	v_pk_mul_f32 v[92:93], v[100:101], v[158:159] op_sel:[1,0]
	v_pk_fma_f32 v[94:95], v[100:101], v[146:147], v[94:95] op_sel_hi:[0,1,1]
	v_pk_mul_f32 v[140:141], v[104:105], v[178:179] op_sel_hi:[0,1]
	v_pk_mul_f32 v[146:147], v[104:105], v[176:177] op_sel_hi:[0,1]
	v_cvt_pk_f32_fp8_e32 v[96:97], v99
	v_cvt_pk_f32_fp8_sdwa v[98:99], v99 src0_sel:WORD_1
	v_cvt_pk_f32_fp8_e32 v[110:111], v113
	v_cvt_pk_f32_fp8_sdwa v[112:113], v113 src0_sel:WORD_1
	v_pk_fma_f32 v[92:93], v[100:101], v[148:149], v[92:93] op_sel_hi:[0,1,1]
	v_pk_fma_f32 v[146:147], v[102:103], v[166:167], v[146:147] op_sel_hi:[0,1,1]
	v_pk_fma_f32 v[140:141], v[102:103], v[168:169], v[140:141] op_sel_hi:[0,1,1]
	v_pk_add_f32 v[92:93], v[92:93], v[140:141]
	v_pk_add_f32 v[94:95], v[94:95], v[146:147]
	v_pk_mul_f32 v[140:141], v[42:43], s[22:23] op_sel_hi:[1,0]
	v_pk_mul_f32 v[148:149], v[40:41], s[22:23] op_sel_hi:[1,0]
	s_waitcnt vmcnt(6)
	v_lshlrev_b32_e32 v172, 16, v88
	v_and_b32_e32 v173, 0xffff0000, v88
	v_lshlrev_b32_e32 v88, 16, v89
	v_and_b32_e32 v89, 0xffff0000, v89
	v_pk_mul_f32 v[94:95], v[148:149], v[94:95]
	v_pk_mul_f32 v[92:93], v[140:141], v[92:93]
	v_pk_fma_f32 v[158:159], v[172:173], s[10:11], v[94:95] op_sel_hi:[1,0,1]
	v_pk_fma_f32 v[156:157], v[88:89], s[10:11], v[92:93] op_sel_hi:[1,0,1]
	v_pk_mul_f32 v[88:89], v[100:101], v[108:109] op_sel:[1,0]
	v_pk_mul_f32 v[94:95], v[104:105], v[116:117] op_sel_hi:[0,1]
	v_pk_mul_f32 v[150:151], v[32:33], s[22:23] op_sel_hi:[1,0]
	v_pk_fma_f32 v[88:89], v[100:101], v[98:99], v[88:89] op_sel_hi:[0,1,1]
	v_pk_fma_f32 v[94:95], v[102:103], v[112:113], v[94:95] op_sel_hi:[0,1,1]
	v_pk_mul_f32 v[118:119], v[150:151], v[118:119]
	v_pk_mul_f32 v[142:143], v[36:37], s[22:23] op_sel_hi:[1,0]
	v_pk_add_f32 v[88:89], v[88:89], v[94:95]
	v_pk_mul_f32 v[146:147], v[50:51], s[22:23] op_sel_hi:[1,0]
	v_lshlrev_b32_e32 v182, 16, v90
	v_and_b32_e32 v183, 0xffff0000, v90
	v_lshlrev_b32_e32 v90, 16, v91
	v_and_b32_e32 v91, 0xffff0000, v91
	v_pk_fma_f32 v[118:119], v[160:161], s[10:11], v[118:119] op_sel_hi:[1,0,1]
	v_pk_mul_f32 v[114:115], v[142:143], v[114:115]
	v_pk_mul_f32 v[92:93], v[100:101], v[106:107] op_sel:[1,0]
	v_pk_mul_f32 v[88:89], v[146:147], v[88:89]
	v_pk_fma_f32 v[114:115], v[170:171], s[10:11], v[114:115] op_sel_hi:[1,0,1]
	v_pk_fma_f32 v[92:93], v[100:101], v[96:97], v[92:93] op_sel_hi:[0,1,1]
	v_pk_mul_f32 v[96:97], v[104:105], v[180:181] op_sel_hi:[0,1]
	v_pk_fma_f32 v[116:117], v[90:91], s[10:11], v[88:89] op_sel_hi:[1,0,1]
	v_add_f32_e32 v88, v118, v119
	v_add_f32_e32 v89, v136, v137
	v_pk_fma_f32 v[96:97], v[102:103], v[110:111], v[96:97] op_sel_hi:[0,1,1]
	v_add_f32_e32 v88, v88, v89
	v_add_f32_e32 v89, v114, v115
	v_add_f32_e32 v90, v154, v155
	v_pk_add_f32 v[92:93], v[92:93], v[96:97]
	v_pk_mul_f32 v[152:153], v[48:49], s[22:23] op_sel_hi:[1,0]
	v_add_f32_e32 v88, 0, v88
	v_add_f32_e32 v89, v89, v90
	v_pk_mul_f32 v[92:93], v[152:153], v[92:93]
	v_add_f32_e32 v88, v88, v89
	v_add_f32_e32 v89, v158, v159
	v_add_f32_e32 v90, v156, v157
	v_pk_fma_f32 v[160:161], v[182:183], s[10:11], v[92:93] op_sel_hi:[1,0,1]
	v_add_f32_e32 v89, v89, v90
	v_add_f32_e32 v88, v88, v89
	v_add_f32_e32 v89, v160, v161
	v_add_f32_e32 v90, v116, v117
	v_add_f32_e32 v89, v89, v90
	v_add_f32_e32 v88, v88, v89
	s_nop 1
	v_mov_b32_dpp v89, v88 quad_perm:[1,0,3,2] row_mask:0xf bank_mask:0xf
	s_mov_b64 s[10:11], -1
	s_waitcnt lgkmcnt(0)
	v_add_f32_e32 v88, v88, v89
	s_nop 1
	v_mov_b32_dpp v89, v88 quad_perm:[2,3,0,1] row_mask:0xf bank_mask:0xf
	s_waitcnt lgkmcnt(0)
	v_add_f32_e32 v88, v88, v89
	s_nop 1
	v_mov_b32_dpp v89, v88 row_half_mirror row_mask:0xf bank_mask:0xf
	s_nop 1
	v_mov_b32_dpp v89, v89 quad_perm:[3,2,1,0] row_mask:0xf bank_mask:0xf
	s_waitcnt lgkmcnt(0)
	v_add_f32_e32 v88, v88, v89
	s_nop 1
	v_mov_b32_dpp v89, v88 row_ror:8 row_mask:0xf bank_mask:0xf
	s_waitcnt lgkmcnt(0)
	v_add_f32_e32 v104, v88, v89
	global_load_dwordx4 v[88:91], v201, s[4:5] offset:16
	global_load_dwordx4 v[92:95], v201, s[4:5]
	global_load_dwordx4 v[96:99], v201, s[8:9] offset:16
	global_load_dwordx4 v[100:103], v201, s[8:9]
	ds_swizzle_b32 v105, v104 offset:swizzle(SWAP,16)
	s_mov_b32 s4, 0x3727c5ac
	s_lshl_b64 s[8:9], s[2:3], 10
	s_waitcnt lgkmcnt(0)
	v_add_f32_e32 v104, v104, v105
	v_mov_b32_e32 v105, v104
	s_nop 1
	v_permlane32_swap_b32_e32 v104, v105
	v_add_f32_e32 v104, v104, v105
	v_fmac_f32_e32 v137, 0xba800000, v104
	v_fmac_f32_e32 v119, 0xba800000, v104
	v_fmamk_f32 v136, v104, 0xba800000, v136
	v_fmamk_f32 v118, v104, 0xba800000, v118
	v_mul_f32_e32 v105, v119, v119
	v_mul_f32_e32 v106, v137, v137
	v_fmac_f32_e32 v105, v118, v118
	v_fmac_f32_e32 v106, v136, v136
	v_fmac_f32_e32 v155, 0xba800000, v104
	v_fmac_f32_e32 v115, 0xba800000, v104
	v_add_f32_e32 v105, v105, v106
	v_fmamk_f32 v154, v104, 0xba800000, v154
	v_fmamk_f32 v114, v104, 0xba800000, v114
	v_mul_f32_e32 v106, v115, v115
	v_mul_f32_e32 v107, v155, v155
	v_fmac_f32_e32 v106, v114, v114
	v_fmac_f32_e32 v107, v154, v154
	v_add_f32_e32 v106, v106, v107
	v_fmac_f32_e32 v157, 0xba800000, v104
	v_fmac_f32_e32 v159, 0xba800000, v104
	v_add_f32_e32 v105, v105, v106
	v_fmamk_f32 v156, v104, 0xba800000, v156
	v_fmamk_f32 v158, v104, 0xba800000, v158
	v_mul_f32_e32 v106, v159, v159
	v_mul_f32_e32 v107, v157, v157
	v_fmac_f32_e32 v106, v158, v158
	v_fmac_f32_e32 v107, v156, v156
	v_add_f32_e32 v106, v106, v107
	v_fmac_f32_e32 v117, 0xba800000, v104
	v_fmac_f32_e32 v161, 0xba800000, v104
	v_add_f32_e32 v105, v106, v105
	v_fmamk_f32 v116, v104, 0xba800000, v116
	v_fmamk_f32 v160, v104, 0xba800000, v160
	v_mul_f32_e32 v104, v161, v161
	v_mul_f32_e32 v106, v117, v117
	v_fmac_f32_e32 v104, v160, v160
	v_fmac_f32_e32 v106, v116, v116
	v_add_f32_e32 v104, v104, v106
	v_add_f32_e32 v104, v104, v105
	s_nop 1
	v_mov_b32_dpp v105, v104 quad_perm:[1,0,3,2] row_mask:0xf bank_mask:0xf
	s_waitcnt lgkmcnt(0)
	v_add_f32_e32 v104, v104, v105
	s_nop 1
	v_mov_b32_dpp v105, v104 quad_perm:[2,3,0,1] row_mask:0xf bank_mask:0xf
	s_waitcnt lgkmcnt(0)
	v_add_f32_e32 v104, v104, v105
	s_nop 1
	v_mov_b32_dpp v105, v104 row_half_mirror row_mask:0xf bank_mask:0xf
	s_nop 1
	v_mov_b32_dpp v105, v105 quad_perm:[3,2,1,0] row_mask:0xf bank_mask:0xf
	s_waitcnt lgkmcnt(0)
	v_add_f32_e32 v104, v104, v105
	s_nop 1
	v_mov_b32_dpp v105, v104 row_ror:8 row_mask:0xf bank_mask:0xf
	s_waitcnt lgkmcnt(0)
	v_add_f32_e32 v104, v104, v105
	ds_swizzle_b32 v105, v104 offset:swizzle(SWAP,16)
	s_waitcnt lgkmcnt(0)
	v_add_f32_e32 v104, v104, v105
	v_mov_b32_e32 v105, v104
	s_nop 1
	v_permlane32_swap_b32_e32 v104, v105
	v_add_f32_e32 v104, v104, v105
	v_mov_b32_e32 v105, s4
	v_fmac_f32_e32 v105, 0x3a800000, v104
	s_mov_b32 s4, 0x800000
	v_mul_f32_e32 v104, 0x4b800000, v105
	v_cmp_gt_f32_e32 vcc, s4, v105
	v_readlane_b32 s4, v254, 28
	v_readlane_b32 s5, v254, 29
	v_cndmask_b32_e32 v104, v105, v104, vcc
	v_rsq_f32_e32 v104, v104
	s_nop 0
	v_mul_f32_e32 v105, 0x45800000, v104
	v_cndmask_b32_e32 v162, v104, v105, vcc
	v_pk_mul_f32 v[104:105], v[118:119], v[162:163] op_sel_hi:[1,0]
	v_pk_mul_f32 v[106:107], v[136:137], v[162:163] op_sel_hi:[1,0]
	v_pk_mul_f32 v[108:109], v[114:115], v[162:163] op_sel_hi:[1,0]
	v_pk_mul_f32 v[110:111], v[154:155], v[162:163] op_sel_hi:[1,0]
	v_pk_mul_f32 v[112:113], v[158:159], v[162:163] op_sel_hi:[1,0]
	v_pk_mul_f32 v[114:115], v[156:157], v[162:163] op_sel_hi:[1,0]
	v_pk_mul_f32 v[136:137], v[160:161], v[162:163] op_sel_hi:[1,0]
	v_pk_mul_f32 v[116:117], v[116:117], v[162:163] op_sel_hi:[1,0]
	v_pk_fma_f32 v[106:107], v[14:15], v[106:107], v[30:31]
	v_pk_fma_f32 v[104:105], v[12:13], v[104:105], v[28:29]
	v_pk_fma_f32 v[110:111], v[10:11], v[110:111], v[26:27]
	v_pk_fma_f32 v[108:109], v[8:9], v[108:109], v[24:25]
	v_pk_fma_f32 v[114:115], v[6:7], v[114:115], v[22:23]
	v_pk_fma_f32 v[112:113], v[4:5], v[112:113], v[20:21]
	v_pk_fma_f32 v[118:119], v[2:3], v[116:117], v[18:19]
	v_pk_fma_f32 v[116:117], v[0:1], v[136:137], v[16:17]
	s_and_b64 vcc, exec, s[4:5]
	v_pk_add_f32 v[136:137], v[44:45], 1.0 op_sel_hi:[1,0]
	v_cmp_ne_u32_e64 s[4:5], 1, v121
	s_cbranch_vccz .LBB0_1100
	v_cvt_pk_bf16_f32 v154, v104, v105
	v_cvt_pk_bf16_f32 v155, v106, v107
	v_lshl_add_u64 v[158:159], s[8:9], 1, v[130:131]
	v_cvt_pk_bf16_f32 v156, v108, v109
	v_cvt_pk_bf16_f32 v157, v110, v111
	global_store_dwordx4 v[158:159], v[154:157], off
	v_pk_add_f32 v[160:161], v[60:61], 1.0 op_sel_hi:[1,0]
	v_pk_add_f32 v[164:165], v[56:57], 1.0 op_sel_hi:[1,0]
	v_cvt_pk_bf16_f32 v154, v112, v113
	v_cvt_pk_bf16_f32 v155, v114, v115
	v_cvt_pk_bf16_f32 v156, v116, v117
	v_cvt_pk_bf16_f32 v157, v118, v119
	global_store_dwordx4 v[158:159], v[154:157], off offset:16
	v_pk_add_f32 v[158:159], v[62:63], 1.0 op_sel_hi:[1,0]
	v_pk_fma_f32 v[162:163], v[160:161], v[108:109], v[68:69]
	v_pk_add_f32 v[154:155], v[46:47], 1.0 op_sel_hi:[1,0]
	v_pk_add_f32 v[160:161], v[58:59], 1.0 op_sel_hi:[1,0]
	v_pk_add_f32 v[168:169], v[52:53], 1.0 op_sel_hi:[1,0]
	v_pk_add_f32 v[166:167], v[54:55], 1.0 op_sel_hi:[1,0]
	v_pk_fma_f32 v[154:155], v[154:155], v[106:107], v[66:67]
	v_pk_fma_f32 v[156:157], v[136:137], v[104:105], v[64:65]
	v_pk_fma_f32 v[158:159], v[158:159], v[110:111], v[70:71]
	v_pk_fma_f32 v[160:161], v[160:161], v[114:115], v[74:75]
	v_pk_fma_f32 v[164:165], v[164:165], v[112:113], v[72:73]
	v_pk_fma_f32 v[166:167], v[166:167], v[118:119], v[78:79]
	v_pk_fma_f32 v[168:169], v[168:169], v[116:117], v[76:77]
	s_and_b64 vcc, exec, s[4:5]
	s_cbranch_vccnz .LBB0_1097
	v_mov_b32_e32 v170, v201
	v_mov_b32_e32 v171, v201
	v_mov_b32_e32 v172, v201
	v_mov_b32_e32 v173, v201
	v_cvt_pk_fp8_f32 v170, v156, v157
	v_cvt_pk_fp8_f32 v171, v162, v163
	v_cvt_pk_fp8_f32 v172, v164, v165
	v_cvt_pk_fp8_f32 v173, v168, v169
	v_cvt_pk_fp8_f32 v170, v154, v155 op_sel:[0,0,1]
	v_cvt_pk_fp8_f32 v171, v158, v159 op_sel:[0,0,1]
	v_cvt_pk_fp8_f32 v172, v160, v161 op_sel:[0,0,1]
	v_cvt_pk_fp8_f32 v173, v166, v167 op_sel:[0,0,1]
	v_lshl_add_u64 v[174:175], v[132:133], 0, s[8:9]
	s_mov_b64 s[10:11], 0
	global_store_dwordx4 v[174:175], v[170:173], off

.LBB0_1102:
	v_ashrrev_i32_e32 v105, 31, v84
	v_mov_b32_e32 v104, v84
	v_ashrrev_i32_e32 v109, 31, v85
	v_mov_b32_e32 v108, v85
	v_lshlrev_b64 v[104:105], 10, v[104:105]
	v_lshlrev_b64 v[84:85], 10, v[108:109]
	v_lshl_add_u64 v[104:105], v[124:125], 0, v[104:105]
	v_lshl_add_u64 v[84:85], v[124:125], 0, v[84:85]
	s_add_i32 s8, s2, 1
	v_ashrrev_i32_e32 v85, 31, v86
	v_mov_b32_e32 v84, v86
	v_lshlrev_b64 v[84:85], 10, v[84:85]
	v_lshl_add_u64 v[84:85], v[124:125], 0, v[84:85]
	v_ashrrev_i32_e32 v85, 31, v87
	v_mov_b32_e32 v84, v87
	v_lshlrev_b64 v[84:85], 10, v[84:85]
	v_lshl_add_u64 v[84:85], v[124:125], 0, v[84:85]
	s_ashr_i32 s9, s8, 31
	s_lshl_b64 s[10:11], s[8:9], 11
	v_lshl_add_u64 v[84:85], v[122:123], 0, s[10:11]
	v_mov_b32_e32 v84, v83
	s_mov_b32 s10, 0x3fd744fd
	s_mov_b32 s3, 0x3727c5ac
	v_readlane_b32 s22, v254, 28
	v_readlane_b32 s23, v254, 29
	s_lshl_b64 s[8:9], s[8:9], 10
	s_waitcnt vmcnt(9)
	v_mov_b64_e32 v[104:105], v[222:223]
	v_mov_b64_e32 v[106:107], v[224:225]
	v_mov_b64_e32 v[108:109], v[226:227]
	v_mov_b64_e32 v[110:111], v[228:229]
	v_mov_b64_e32 v[154:155], v[230:231]
	v_mov_b64_e32 v[156:157], v[232:233]
	v_mov_b64_e32 v[174:175], v[244:245]
	v_mov_b64_e32 v[176:177], v[246:247]
	v_cvt_pk_f32_fp8_e32 v[202:203], v104
	v_cvt_pk_f32_fp8_sdwa v[204:205], v104 src0_sel:WORD_1
	v_cvt_pk_f32_fp8_e32 v[190:191], v105
	v_cvt_pk_f32_fp8_sdwa v[168:169], v105 src0_sel:WORD_1
	v_cvt_pk_f32_fp8_e32 v[114:115], v106
	v_cvt_pk_f32_fp8_sdwa v[116:117], v106 src0_sel:WORD_1
	v_cvt_pk_f32_fp8_e32 v[86:87], v107
	v_cvt_pk_f32_fp8_sdwa v[104:105], v107 src0_sel:WORD_1
	v_cvt_pk_f32_fp8_e32 v[206:207], v108
	v_cvt_pk_f32_fp8_sdwa v[208:209], v108 src0_sel:WORD_1
	v_cvt_pk_f32_fp8_e32 v[210:211], v109
	v_cvt_pk_f32_fp8_sdwa v[212:213], v109 src0_sel:WORD_1
	v_cvt_pk_f32_fp8_e32 v[160:161], v110
	v_cvt_pk_f32_fp8_sdwa v[162:163], v110 src0_sel:WORD_1
	v_cvt_pk_f32_fp8_e32 v[106:107], v111
	v_cvt_pk_f32_fp8_sdwa v[108:109], v111 src0_sel:WORD_1
	v_cvt_pk_f32_fp8_e32 v[218:219], v174
	v_cvt_pk_f32_fp8_sdwa v[220:221], v174 src0_sel:WORD_1
	v_cvt_pk_f32_fp8_e32 v[214:215], v154
	v_cvt_pk_f32_fp8_sdwa v[216:217], v154 src0_sel:WORD_1
	v_cvt_pk_f32_fp8_e32 v[178:179], v155
	v_cvt_pk_f32_fp8_sdwa v[180:181], v155 src0_sel:WORD_1
	v_cvt_pk_f32_fp8_e32 v[164:165], v156
	v_cvt_pk_f32_fp8_sdwa v[166:167], v156 src0_sel:WORD_1
	v_cvt_pk_f32_fp8_e32 v[110:111], v157
	v_cvt_pk_f32_fp8_sdwa v[112:113], v157 src0_sel:WORD_1
	v_cvt_pk_f32_fp8_e32 v[184:185], v175
	v_cvt_pk_f32_fp8_sdwa v[188:189], v175 src0_sel:WORD_1
	v_cvt_pk_f32_fp8_e32 v[172:173], v176
	v_cvt_pk_f32_fp8_sdwa v[174:175], v176 src0_sel:WORD_1
	v_cvt_pk_f32_fp8_e32 v[154:155], v177
	v_cvt_pk_f32_fp8_sdwa v[156:157], v177 src0_sel:WORD_1
	s_waitcnt vmcnt(8)
	v_lshlrev_b32_e32 v182, 16, v194
	v_and_b32_e32 v183, 0xffff0000, v194
	v_lshlrev_b32_e32 v186, 16, v195
	v_and_b32_e32 v187, 0xffff0000, v195
	s_waitcnt vmcnt(7)
	v_lshlrev_b32_e32 v170, 16, v196
	v_and_b32_e32 v171, 0xffff0000, v196
	v_lshlrev_b32_e32 v176, 16, v197
	v_and_b32_e32 v177, 0xffff0000, v197
	v_lshlrev_b32_e32 v118, 16, v198
	v_and_b32_e32 v119, 0xffff0000, v198
	v_lshlrev_b32_e32 v158, 16, v199
	v_and_b32_e32 v159, 0xffff0000, v199
	v_pk_mul_f32 v[194:195], v[80:81], v[208:209] op_sel:[1,0]
	v_pk_mul_f32 v[196:197], v[80:81], v[206:207] op_sel:[1,0]
	v_pk_mul_f32 v[198:199], v[84:85], v[220:221] op_sel_hi:[0,1]
	v_pk_mul_f32 v[206:207], v[84:85], v[218:219] op_sel_hi:[0,1]
	v_pk_mul_f32 v[208:209], v[80:81], v[212:213] op_sel:[1,0]
	v_pk_mul_f32 v[210:211], v[80:81], v[210:211] op_sel:[1,0]
	v_pk_mul_f32 v[162:163], v[80:81], v[162:163] op_sel:[1,0]
	v_pk_mul_f32 v[160:161], v[80:81], v[160:161] op_sel:[1,0]
	v_pk_mul_f32 v[108:109], v[80:81], v[108:109] op_sel:[1,0]
	v_pk_mul_f32 v[106:107], v[80:81], v[106:107] op_sel:[1,0]
	v_pk_fma_f32 v[196:197], v[80:81], v[202:203], v[196:197] op_sel_hi:[0,1,1]
	v_pk_fma_f32 v[194:195], v[80:81], v[204:205], v[194:195] op_sel_hi:[0,1,1]
	v_pk_fma_f32 v[202:203], v[82:83], v[214:215], v[206:207] op_sel_hi:[0,1,1]
	v_pk_fma_f32 v[198:199], v[82:83], v[216:217], v[198:199] op_sel_hi:[0,1,1]
	v_pk_fma_f32 v[190:191], v[80:81], v[190:191], v[210:211] op_sel_hi:[0,1,1]
	v_pk_fma_f32 v[168:169], v[80:81], v[168:169], v[208:209] op_sel_hi:[0,1,1]
	v_pk_mul_f32 v[188:189], v[84:85], v[188:189] op_sel_hi:[0,1]
	v_pk_mul_f32 v[184:185], v[84:85], v[184:185] op_sel_hi:[0,1]
	v_pk_fma_f32 v[114:115], v[80:81], v[114:115], v[160:161] op_sel_hi:[0,1,1]
	v_pk_fma_f32 v[116:117], v[80:81], v[116:117], v[162:163] op_sel_hi:[0,1,1]
	v_pk_mul_f32 v[160:161], v[84:85], v[174:175] op_sel_hi:[0,1]
	v_pk_mul_f32 v[162:163], v[84:85], v[172:173] op_sel_hi:[0,1]
	v_pk_fma_f32 v[86:87], v[80:81], v[86:87], v[106:107] op_sel_hi:[0,1,1]
	v_pk_fma_f32 v[80:81], v[80:81], v[104:105], v[108:109] op_sel_hi:[0,1,1]
	v_pk_mul_f32 v[104:105], v[84:85], v[156:157] op_sel_hi:[0,1]
	v_pk_mul_f32 v[84:85], v[84:85], v[154:155] op_sel_hi:[0,1]
	v_pk_add_f32 v[194:195], v[194:195], v[198:199]
	v_pk_add_f32 v[196:197], v[196:197], v[202:203]
	v_pk_fma_f32 v[178:179], v[82:83], v[178:179], v[184:185] op_sel_hi:[0,1,1]
	v_pk_fma_f32 v[180:181], v[82:83], v[180:181], v[188:189] op_sel_hi:[0,1,1]
	v_pk_fma_f32 v[162:163], v[82:83], v[164:165], v[162:163] op_sel_hi:[0,1,1]
	v_pk_fma_f32 v[160:161], v[82:83], v[166:167], v[160:161] op_sel_hi:[0,1,1]
	v_pk_fma_f32 v[84:85], v[82:83], v[110:111], v[84:85] op_sel_hi:[0,1,1]
	v_pk_fma_f32 v[82:83], v[82:83], v[112:113], v[104:105] op_sel_hi:[0,1,1]
	v_lshlrev_b32_e32 v222, 16, v192
	v_and_b32_e32 v223, 0xffff0000, v192
	v_lshlrev_b32_e32 v192, 16, v193
	v_and_b32_e32 v193, 0xffff0000, v193
	v_pk_mul_f32 v[150:151], v[150:151], v[196:197]
	v_pk_mul_f32 v[144:145], v[144:145], v[194:195]
	v_pk_add_f32 v[168:169], v[168:169], v[180:181]
	v_pk_add_f32 v[178:179], v[190:191], v[178:179]
	v_pk_add_f32 v[80:81], v[80:81], v[82:83]
	v_pk_fma_f32 v[144:145], v[192:193], s[10:11], v[144:145] op_sel_hi:[1,0,1]
	v_pk_fma_f32 v[150:151], v[222:223], s[10:11], v[150:151] op_sel_hi:[1,0,1]
	v_pk_mul_f32 v[142:143], v[142:143], v[178:179]
	v_pk_mul_f32 v[138:139], v[138:139], v[168:169]
	v_pk_add_f32 v[82:83], v[86:87], v[84:85]
	v_pk_mul_f32 v[80:81], v[146:147], v[80:81]
	v_pk_fma_f32 v[138:139], v[186:187], s[10:11], v[138:139] op_sel_hi:[1,0,1]
	v_pk_fma_f32 v[142:143], v[182:183], s[10:11], v[142:143] op_sel_hi:[1,0,1]
	v_pk_add_f32 v[116:117], v[116:117], v[160:161]
	v_pk_add_f32 v[114:115], v[114:115], v[162:163]
	v_pk_mul_f32 v[82:83], v[152:153], v[82:83]
	v_pk_fma_f32 v[108:109], v[158:159], s[10:11], v[80:81] op_sel_hi:[1,0,1]
	v_add_f32_e32 v80, v150, v151
	v_add_f32_e32 v81, v144, v145
	v_pk_mul_f32 v[114:115], v[148:149], v[114:115]
	v_pk_mul_f32 v[116:117], v[140:141], v[116:117]
	v_pk_fma_f32 v[110:111], v[118:119], s[10:11], v[82:83] op_sel_hi:[1,0,1]
	v_add_f32_e32 v80, v80, v81
	v_add_f32_e32 v81, v142, v143
	v_add_f32_e32 v82, v138, v139
	v_pk_fma_f32 v[116:117], v[176:177], s[10:11], v[116:117] op_sel_hi:[1,0,1]
	v_pk_fma_f32 v[114:115], v[170:171], s[10:11], v[114:115] op_sel_hi:[1,0,1]
	v_add_f32_e32 v80, 0, v80
	v_add_f32_e32 v81, v81, v82
	v_add_f32_e32 v80, v80, v81
	v_add_f32_e32 v81, v114, v115
	v_add_f32_e32 v82, v116, v117
	v_add_f32_e32 v81, v81, v82
	v_add_f32_e32 v80, v80, v81
	v_add_f32_e32 v81, v110, v111
	v_add_f32_e32 v82, v108, v109
	v_add_f32_e32 v81, v81, v82
	v_add_f32_e32 v80, v80, v81
	s_nop 1
	v_mov_b32_dpp v81, v80 quad_perm:[1,0,3,2] row_mask:0xf bank_mask:0xf
	s_mov_b64 s[10:11], -1
	s_waitcnt lgkmcnt(0)
	v_add_f32_e32 v80, v80, v81
	s_nop 1
	v_mov_b32_dpp v81, v80 quad_perm:[2,3,0,1] row_mask:0xf bank_mask:0xf
	s_waitcnt lgkmcnt(0)
	v_add_f32_e32 v80, v80, v81
	s_nop 1
	v_mov_b32_dpp v81, v80 row_half_mirror row_mask:0xf bank_mask:0xf
	s_nop 1
	v_mov_b32_dpp v81, v81 quad_perm:[3,2,1,0] row_mask:0xf bank_mask:0xf
	s_waitcnt lgkmcnt(0)
	v_add_f32_e32 v80, v80, v81
	s_nop 1
	v_mov_b32_dpp v81, v80 row_ror:8 row_mask:0xf bank_mask:0xf
	s_waitcnt lgkmcnt(0)
	v_add_f32_e32 v80, v80, v81
	ds_swizzle_b32 v81, v80 offset:swizzle(SWAP,16)
	s_waitcnt lgkmcnt(0)
	v_add_f32_e32 v80, v80, v81
	v_mov_b32_e32 v81, v80
	s_nop 1
	v_permlane32_swap_b32_e32 v80, v81
	v_add_f32_e32 v80, v80, v81
	v_fmac_f32_e32 v145, 0xba800000, v80
	v_fmac_f32_e32 v151, 0xba800000, v80
	v_fmamk_f32 v144, v80, 0xba800000, v144
	v_fmamk_f32 v150, v80, 0xba800000, v150
	v_mul_f32_e32 v81, v151, v151
	v_mul_f32_e32 v82, v145, v145
	v_fmac_f32_e32 v81, v150, v150
	v_fmac_f32_e32 v82, v144, v144
	v_fmac_f32_e32 v139, 0xba800000, v80
	v_fmac_f32_e32 v143, 0xba800000, v80
	v_add_f32_e32 v81, v81, v82
	v_fmamk_f32 v138, v80, 0xba800000, v138
	v_fmamk_f32 v142, v80, 0xba800000, v142
	v_mul_f32_e32 v82, v143, v143
	v_mul_f32_e32 v83, v139, v139
	v_fmac_f32_e32 v82, v142, v142
	v_fmac_f32_e32 v83, v138, v138
	v_add_f32_e32 v82, v82, v83
	v_fmac_f32_e32 v117, 0xba800000, v80
	v_fmac_f32_e32 v115, 0xba800000, v80
	v_add_f32_e32 v81, v81, v82
	v_fmamk_f32 v116, v80, 0xba800000, v116
	v_fmamk_f32 v114, v80, 0xba800000, v114
	v_mul_f32_e32 v82, v115, v115
	v_mul_f32_e32 v83, v117, v117
	v_fmac_f32_e32 v82, v114, v114
	v_fmac_f32_e32 v83, v116, v116
	v_add_f32_e32 v82, v82, v83
	v_fmac_f32_e32 v109, 0xba800000, v80
	v_fmac_f32_e32 v111, 0xba800000, v80
	v_add_f32_e32 v81, v82, v81
	v_fmamk_f32 v108, v80, 0xba800000, v108
	v_fmamk_f32 v110, v80, 0xba800000, v110
	v_mul_f32_e32 v80, v111, v111
	v_mul_f32_e32 v82, v109, v109
	v_fmac_f32_e32 v80, v110, v110
	v_fmac_f32_e32 v82, v108, v108
	v_add_f32_e32 v80, v80, v82
	v_add_f32_e32 v80, v80, v81
	s_nop 1
	v_mov_b32_dpp v81, v80 quad_perm:[1,0,3,2] row_mask:0xf bank_mask:0xf
	s_waitcnt lgkmcnt(0)
	v_add_f32_e32 v80, v80, v81
	s_nop 1
	v_mov_b32_dpp v81, v80 quad_perm:[2,3,0,1] row_mask:0xf bank_mask:0xf
	s_waitcnt lgkmcnt(0)
	v_add_f32_e32 v80, v80, v81
	s_nop 1
	v_mov_b32_dpp v81, v80 row_half_mirror row_mask:0xf bank_mask:0xf
	s_nop 1
	v_mov_b32_dpp v81, v81 quad_perm:[3,2,1,0] row_mask:0xf bank_mask:0xf
	s_waitcnt lgkmcnt(0)
	v_add_f32_e32 v80, v80, v81
	s_nop 1
	v_mov_b32_dpp v81, v80 row_ror:8 row_mask:0xf bank_mask:0xf
	s_waitcnt lgkmcnt(0)
	v_add_f32_e32 v80, v80, v81
	ds_swizzle_b32 v81, v80 offset:swizzle(SWAP,16)
	s_waitcnt lgkmcnt(0)
	v_add_f32_e32 v80, v80, v81
	v_mov_b32_e32 v81, v80
	s_nop 1
	v_permlane32_swap_b32_e32 v80, v81
	v_add_f32_e32 v80, v80, v81
	v_mov_b32_e32 v81, s3
	v_fmac_f32_e32 v81, 0x3a800000, v80
	s_mov_b32 s3, 0x800000
	v_mul_f32_e32 v80, 0x4b800000, v81
	v_cmp_gt_f32_e32 vcc, s3, v81
	s_nop 1
	v_cndmask_b32_e32 v80, v81, v80, vcc
	v_rsq_f32_e32 v80, v80
	s_nop 0
	v_mul_f32_e32 v81, 0x45800000, v80
	v_cndmask_b32_e32 v112, v80, v81, vcc
	v_pk_mul_f32 v[80:81], v[150:151], v[112:113] op_sel_hi:[1,0]
	v_pk_mul_f32 v[82:83], v[144:145], v[112:113] op_sel_hi:[1,0]
	v_pk_mul_f32 v[84:85], v[142:143], v[112:113] op_sel_hi:[1,0]
	v_pk_mul_f32 v[86:87], v[138:139], v[112:113] op_sel_hi:[1,0]
	v_pk_mul_f32 v[104:105], v[114:115], v[112:113] op_sel_hi:[1,0]
	v_pk_mul_f32 v[106:107], v[116:117], v[112:113] op_sel_hi:[1,0]
	v_pk_mul_f32 v[114:115], v[110:111], v[112:113] op_sel_hi:[1,0]
	v_pk_mul_f32 v[108:109], v[108:109], v[112:113] op_sel_hi:[1,0]
	v_pk_fma_f32 v[82:83], v[14:15], v[82:83], v[30:31]
	v_pk_fma_f32 v[80:81], v[12:13], v[80:81], v[28:29]
	v_pk_fma_f32 v[86:87], v[10:11], v[86:87], v[26:27]
	v_pk_fma_f32 v[84:85], v[8:9], v[84:85], v[24:25]
	v_pk_fma_f32 v[106:107], v[6:7], v[106:107], v[22:23]
	v_pk_fma_f32 v[104:105], v[4:5], v[104:105], v[20:21]
	v_pk_fma_f32 v[110:111], v[2:3], v[108:109], v[18:19]
	v_pk_fma_f32 v[108:109], v[0:1], v[114:115], v[16:17]
	s_and_b64 vcc, exec, s[22:23]
	s_cbranch_vccz .LBB0_1108
	v_cvt_pk_bf16_f32 v112, v80, v81
	v_cvt_pk_bf16_f32 v113, v82, v83
	v_cvt_pk_bf16_f32 v114, v84, v85
	v_cvt_pk_bf16_f32 v115, v86, v87
	v_lshl_add_u64 v[116:117], s[8:9], 1, v[130:131]
	global_store_dwordx4 v[116:117], v[112:115], off
	v_pk_add_f32 v[118:119], v[60:61], 1.0 op_sel_hi:[1,0]
	v_pk_add_f32 v[138:139], v[56:57], 1.0 op_sel_hi:[1,0]
	v_cvt_pk_bf16_f32 v112, v104, v105
	v_cvt_pk_bf16_f32 v113, v106, v107
	v_cvt_pk_bf16_f32 v114, v108, v109
	v_cvt_pk_bf16_f32 v115, v110, v111
	global_store_dwordx4 v[116:117], v[112:115], off offset:16
	v_pk_add_f32 v[116:117], v[62:63], 1.0 op_sel_hi:[1,0]
	v_pk_add_f32 v[142:143], v[52:53], 1.0 op_sel_hi:[1,0]
	v_pk_add_f32 v[112:113], v[46:47], 1.0 op_sel_hi:[1,0]
	v_pk_fma_f32 v[114:115], v[136:137], v[80:81], v[64:65]
	v_pk_fma_f32 v[136:137], v[118:119], v[84:85], v[68:69]
	v_pk_add_f32 v[118:119], v[58:59], 1.0 op_sel_hi:[1,0]
	v_pk_add_f32 v[140:141], v[54:55], 1.0 op_sel_hi:[1,0]
	v_pk_fma_f32 v[112:113], v[112:113], v[82:83], v[66:67]
	v_pk_fma_f32 v[116:117], v[116:117], v[86:87], v[70:71]
	v_pk_fma_f32 v[118:119], v[118:119], v[106:107], v[74:75]
	v_pk_fma_f32 v[138:139], v[138:139], v[104:105], v[72:73]
	v_pk_fma_f32 v[140:141], v[140:141], v[110:111], v[78:79]
	v_pk_fma_f32 v[142:143], v[142:143], v[108:109], v[76:77]
	s_and_b64 vcc, exec, s[4:5]
	s_mov_b64 s[4:5], -1
	s_cbranch_vccnz .LBB0_1105
	v_mov_b32_e32 v144, v201
	v_mov_b32_e32 v145, v201
	v_mov_b32_e32 v146, v201
	v_mov_b32_e32 v147, v201
	v_cvt_pk_fp8_f32 v144, v114, v115
	v_cvt_pk_fp8_f32 v145, v136, v137
	v_cvt_pk_fp8_f32 v146, v138, v139
	v_cvt_pk_fp8_f32 v147, v142, v143
	v_cvt_pk_fp8_f32 v144, v112, v113 op_sel:[0,0,1]
	v_cvt_pk_fp8_f32 v145, v116, v117 op_sel:[0,0,1]
	v_cvt_pk_fp8_f32 v146, v118, v119 op_sel:[0,0,1]
	v_cvt_pk_fp8_f32 v147, v140, v141 op_sel:[0,0,1]
	v_lshl_add_u64 v[148:149], v[132:133], 0, s[8:9]
	s_mov_b64 s[4:5], 0
	global_store_dwordx4 v[148:149], v[144:147], off
